# GEMM K-loops: drop the back-to-back s_setprio 0 / s_setprio 1 pair in the middle of each 32-MFMA block (on v7)
# speedup vs baseline: 1.0004x; 1.0004x over previous
; #define PG8_STAGE(bufoff, gbase, voff) do { _Pragma("unroll") for (int _i = 0; _i < 2; ++_i) \
;         __builtin_amdgcn_global_load_lds((const unsigned*)((const char*)(gbase) + (voff)[_i]), (LAS unsigned*)(lds + (bufoff) + ldsw + _i * 8192), 16, 0, 0); } while (0)
; #define PG8_STAGE_A(bufoff, kptr, half, VO) do { if constexpr (GATHER) { _Pragma("unroll") for (int _i = 0; _i < 2; ++_i) \
;         __builtin_amdgcn_global_load_lds((const unsigned*)((const char*)(kptr) + (VO)[half][_i]), (LAS unsigned*)(lds + (bufoff) + ldsw + _i * 8192), 16, 0, 0); } \
;         else { PG8_STAGE(bufoff, (kptr) + (half) * hstepA, voffA); } } while (0)
; #define PG8_WAIT_V(n) asm volatile("s_waitcnt vmcnt(" #n ")" ::: "memory")
;     ...
;         for (int t = 0; t < nt; t += 2) {
;             const bool last = (t == nt - 2);
;             const char* a1 = cA + (size_t)(t + 1) * kstep;
;             const char* a2 = last ? nA : cA + (size_t)(t + 2) * kstep; const char* b2 = last ? nB : cB + (size_t)(t + 2) * kstep;
;             const char* a3 = a2 + kstep; const char* b3 = b2 + kstep;
;             unsigned g2[2][2];
;             if constexpr (GATHER) {
; #pragma unroll
;                 for (int _h = 0; _h < 2; ++_h)
; #pragma unroll
;                     for (int _i = 0; _i < 2; ++_i) g2[_h][_i] = last ? gN[_h][_i] : gC[_h][_i]; }
;             if constexpr (SP2) {
;             PG8_LDB(B0, 0, 0); PG8_LDB(B1, 0, 1); PG8_SCHED; PG8_LDA(At, 0, 0); PG8_STAGE_A(PG8_SA(1, 1), a1, 1, gC);
;             PG8_WAIT_V(8); PG8_WAIT_L(0); PG8_BAR; PG8_MMA(0, 0, At, B0); PG8_MMA(0, 1, At, B1); PG8_BAR; PG8_SCHED;
;             PG8_LDA(At, 0, 1); PG8_STAGE(PG8_SB(0, 0), b2, voffB); PG8_STAGE(PG8_SB(0, 1), b2 + hstepB, voffB); PG8_STAGE_A(PG8_SA(0, 0), a2, 0, g2);
;             PG8_WAIT_V(8); PG8_WAIT_L(0); PG8_BAR; PG8_MMA(1, 0, At, B0); PG8_MMA(1, 1, At, B1); PG8_BAR; PG8_SCHED;
;             PG8_LDB(B0, 1, 0); PG8_LDB(B1, 1, 1); PG8_SCHED; PG8_LDA(At, 1, 0); PG8_STAGE_A(PG8_SA(0, 1), a2, 1, g2);
;             PG8_WAIT_V(8); PG8_WAIT_L(0); PG8_BAR; PG8_MMA(0, 0, At, B0); PG8_MMA(0, 1, At, B1); PG8_BAR; PG8_SCHED;
;             PG8_LDA(At, 1, 1); PG8_STAGE(PG8_SB(1, 0), b3, voffB); PG8_STAGE(PG8_SB(1, 1), b3 + hstepB, voffB); PG8_STAGE_A(PG8_SA(1, 0), a3, 0, g2);
;             PG8_WAIT_V(8); PG8_WAIT_L(0); PG8_BAR; PG8_MMA(1, 0, At, B0); PG8_MMA(1, 1, At, B1); PG8_BAR; PG8_SCHED;
.LBB0_224:
	s_add_u32 s0, s24, 0xfff80080
	s_addc_u32 s1, s25, -1
	s_add_i32 s20, 0, 0x10000
	s_cmp_eq_u32 s19, 28
	s_cselect_b32 s31, s4, s1
	s_cselect_b32 s30, s14, s0
	s_cselect_b32 s1, s15, s18
	s_cselect_b32 s0, s16, s17
	s_add_i32 s22, 0, 0x14000
	v_add_u32_e32 v160, s20, v143
	v_add_u32_e32 v176, s22, v143
	ds_read_b128 v[148:151], v160
	ds_read_b128 v[152:155], v160 offset:1024
	ds_read_b128 v[156:159], v160 offset:2048
	ds_read_b128 v[160:163], v160 offset:3072
	ds_read_b128 v[164:167], v176
	ds_read_b128 v[168:171], v176 offset:1024
	ds_read_b128 v[172:175], v176 offset:2048
	ds_read_b128 v[176:179], v176 offset:3072
	v_lshl_add_u64 v[204:205], s[24:25], 0, v[138:139]
	s_add_i32 m0, s13, 0xc000
	ds_read_b128 v[180:183], v147
	ds_read_b128 v[184:187], v147 offset:1024
	ds_read_b128 v[188:191], v147 offset:2048
	ds_read_b128 v[192:195], v147 offset:3072
	ds_read_b128 v[196:199], v147 offset:4096
	ds_read_b128 v[200:203], v147 offset:5120
	ds_read_b128 v[216:219], v147 offset:6144
	ds_read_b128 v[220:223], v147 offset:7168
	global_load_lds_dwordx4 v[204:205], off
	v_lshl_add_u64 v[204:205], s[24:25], 0, v[140:141]
	s_add_i32 m0, s13, 0xe000
	s_nop 0
	global_load_lds_dwordx4 v[204:205], off
	s_waitcnt vmcnt(8)
	s_waitcnt lgkmcnt(0)
	s_barrier
	s_setprio 1
	s_waitcnt lgkmcnt(0)
	v_mfma_f32_16x16x32_bf16 v[126:129], v[148:151], v[180:183], v[126:129]
	v_mfma_f32_16x16x32_bf16 v[122:125], v[156:159], v[180:183], v[122:125]
	v_mfma_f32_16x16x32_bf16 v[118:121], v[148:151], v[188:191], v[118:121]
	v_mfma_f32_16x16x32_bf16 v[114:117], v[156:159], v[188:191], v[114:117]
	v_mfma_f32_16x16x32_bf16 v[102:105], v[148:151], v[196:199], v[102:105]
	v_mfma_f32_16x16x32_bf16 v[98:101], v[156:159], v[196:199], v[98:101]
	v_mfma_f32_16x16x32_bf16 v[86:89], v[148:151], v[216:219], v[86:89]
	v_mfma_f32_16x16x32_bf16 v[82:85], v[156:159], v[216:219], v[82:85]
	v_mfma_f32_16x16x32_bf16 v[126:129], v[152:155], v[184:187], v[126:129]
	v_mfma_f32_16x16x32_bf16 v[122:125], v[160:163], v[184:187], v[122:125]
	v_mfma_f32_16x16x32_bf16 v[118:121], v[152:155], v[192:195], v[118:121]
	v_mfma_f32_16x16x32_bf16 v[114:117], v[160:163], v[192:195], v[114:117]
	v_mfma_f32_16x16x32_bf16 v[102:105], v[152:155], v[200:203], v[102:105]
	v_mfma_f32_16x16x32_bf16 v[98:101], v[160:163], v[200:203], v[98:101]
	v_mfma_f32_16x16x32_bf16 v[86:89], v[152:155], v[220:223], v[86:89]
	v_mfma_f32_16x16x32_bf16 v[82:85], v[160:163], v[220:223], v[82:85]
	v_mfma_f32_16x16x32_bf16 v[110:113], v[164:167], v[180:183], v[110:113]
	v_mfma_f32_16x16x32_bf16 v[106:109], v[172:175], v[180:183], v[106:109]
	v_mfma_f32_16x16x32_bf16 v[94:97], v[164:167], v[188:191], v[94:97]
	v_mfma_f32_16x16x32_bf16 v[90:93], v[172:175], v[188:191], v[90:93]
	v_mfma_f32_16x16x32_bf16 v[78:81], v[164:167], v[196:199], v[78:81]
	v_mfma_f32_16x16x32_bf16 v[74:77], v[172:175], v[196:199], v[74:77]
	v_mfma_f32_16x16x32_bf16 v[70:73], v[164:167], v[216:219], v[70:73]
	v_mfma_f32_16x16x32_bf16 v[66:69], v[172:175], v[216:219], v[66:69]
	v_mfma_f32_16x16x32_bf16 v[110:113], v[168:171], v[184:187], v[110:113]
	v_mfma_f32_16x16x32_bf16 v[106:109], v[176:179], v[184:187], v[106:109]
	v_mfma_f32_16x16x32_bf16 v[94:97], v[168:171], v[192:195], v[94:97]
	v_mfma_f32_16x16x32_bf16 v[90:93], v[176:179], v[192:195], v[90:93]
	v_mfma_f32_16x16x32_bf16 v[78:81], v[168:171], v[200:203], v[78:81]
	v_mfma_f32_16x16x32_bf16 v[74:77], v[176:179], v[200:203], v[74:77]
	v_mfma_f32_16x16x32_bf16 v[70:73], v[168:171], v[220:223], v[70:73]
	v_mfma_f32_16x16x32_bf16 v[66:69], v[176:179], v[220:223], v[66:69]
	s_setprio 0
	s_barrier
	s_add_i32 s20, s20, s12
	v_lshl_add_u64 v[204:205], s[0:1], 0, v[132:133]
	s_mov_b32 m0, s20
	ds_read_b128 v[180:183], v147 offset:16384
	ds_read_b128 v[184:187], v147 offset:17408
	ds_read_b128 v[188:191], v147 offset:18432
	ds_read_b128 v[192:195], v147 offset:19456
	ds_read_b128 v[196:199], v147 offset:20480
	ds_read_b128 v[200:203], v147 offset:21504
	ds_read_b128 v[216:219], v147 offset:22528
	ds_read_b128 v[220:223], v147 offset:23552
	global_load_lds_dwordx4 v[204:205], off
	s_add_i32 m0, s20, 0x2000
	s_add_u32 s20, s0, 0x80000
	v_lshl_add_u64 v[208:209], s[0:1], 0, v[136:137]
	s_addc_u32 s21, s1, 0
	s_add_i32 s22, s22, s12
	global_load_lds_dwordx4 v[208:209], off
	v_lshl_add_u64 v[210:211], s[20:21], 0, v[132:133]
	s_mov_b32 m0, s22
	v_lshl_add_u64 v[212:213], s[30:31], 0, v[134:135]
	global_load_lds_dwordx4 v[210:211], off
	v_lshl_add_u64 v[210:211], s[20:21], 0, v[136:137]
	s_add_i32 m0, s22, 0x2000
	s_nop 0
	global_load_lds_dwordx4 v[210:211], off
	v_lshl_add_u64 v[210:211], s[30:31], 0, v[130:131]
	s_mov_b32 m0, s13
	s_nop 0
	global_load_lds_dwordx4 v[210:211], off
	s_mov_b32 m0, s26
	s_nop 0
	global_load_lds_dwordx4 v[212:213], off
	s_waitcnt vmcnt(8)
	s_waitcnt lgkmcnt(0)
	s_barrier
; #define PG8_STAGE(bufoff, gbase, voff) do { _Pragma("unroll") for (int _i = 0; _i < 2; ++_i) \
;         __builtin_amdgcn_global_load_lds((const unsigned*)((const char*)(gbase) + (voff)[_i]), (LAS unsigned*)(lds + (bufoff) + ldsw + _i * 8192), 16, 0, 0); } while (0)
; #define PG8_STAGE_A(bufoff, kptr, half, VO) do { if constexpr (GATHER) { _Pragma("unroll") for (int _i = 0; _i < 2; ++_i) \
;         __builtin_amdgcn_global_load_lds((const unsigned*)((const char*)(kptr) + (VO)[half][_i]), (LAS unsigned*)(lds + (bufoff) + ldsw + _i * 8192), 16, 0, 0); } \
;         else { PG8_STAGE(bufoff, (kptr) + (half) * hstepA, voffA); } } while (0)
; #define PG8_WAIT_V(n) asm volatile("s_waitcnt vmcnt(" #n ")" ::: "memory")
;     ...
;         for (int t = 0; t < nt; t += 2) {
;             const bool last = (t == nt - 2);
;             const char* a1 = cA + (size_t)(t + 1) * kstep;
;             const char* a2 = last ? nA : cA + (size_t)(t + 2) * kstep; const char* b2 = last ? nB : cB + (size_t)(t + 2) * kstep;
;             const char* a3 = a2 + kstep; const char* b3 = b2 + kstep;
;             unsigned g2[2][2];
;             if constexpr (GATHER) {
; #pragma unroll
;                 for (int _h = 0; _h < 2; ++_h)
; #pragma unroll
;                     for (int _i = 0; _i < 2; ++_i) g2[_h][_i] = last ? gN[_h][_i] : gC[_h][_i]; }
;             if constexpr (SP2) {
;             PG8_LDB(B0, 0, 0); PG8_LDB(B1, 0, 1); PG8_SCHED; PG8_LDA(At, 0, 0); PG8_STAGE_A(PG8_SA(1, 1), a1, 1, gC);
;             PG8_WAIT_V(8); PG8_WAIT_L(0); PG8_BAR; PG8_MMA(0, 0, At, B0); PG8_MMA(0, 1, At, B1); PG8_BAR; PG8_SCHED;
;             PG8_LDA(At, 0, 1); PG8_STAGE(PG8_SB(0, 0), b2, voffB); PG8_STAGE(PG8_SB(0, 1), b2 + hstepB, voffB); PG8_STAGE_A(PG8_SA(0, 0), a2, 0, g2);
;             PG8_WAIT_V(8); PG8_WAIT_L(0); PG8_BAR; PG8_MMA(1, 0, At, B0); PG8_MMA(1, 1, At, B1); PG8_BAR; PG8_SCHED;
;             PG8_LDB(B0, 1, 0); PG8_LDB(B1, 1, 1); PG8_SCHED; PG8_LDA(At, 1, 0); PG8_STAGE_A(PG8_SA(0, 1), a2, 1, g2);
;             PG8_WAIT_V(8); PG8_WAIT_L(0); PG8_BAR; PG8_MMA(0, 0, At, B0); PG8_MMA(0, 1, At, B1); PG8_BAR; PG8_SCHED;
;             PG8_LDA(At, 1, 1); PG8_STAGE(PG8_SB(1, 0), b3, voffB); PG8_STAGE(PG8_SB(1, 1), b3 + hstepB, voffB); PG8_STAGE_A(PG8_SA(1, 0), a3, 0, g2);
;             PG8_WAIT_V(8); PG8_WAIT_L(0); PG8_BAR; PG8_MMA(1, 0, At, B0); PG8_MMA(1, 1, At, B1); PG8_BAR; PG8_SCHED;
	s_setprio 1
	s_waitcnt lgkmcnt(0)
	v_mfma_f32_16x16x32_bf16 v[62:65], v[148:151], v[180:183], v[62:65]
	v_mfma_f32_16x16x32_bf16 v[58:61], v[156:159], v[180:183], v[58:61]
	v_mfma_f32_16x16x32_bf16 v[54:57], v[148:151], v[188:191], v[54:57]
	v_mfma_f32_16x16x32_bf16 v[50:53], v[156:159], v[188:191], v[50:53]
	v_mfma_f32_16x16x32_bf16 v[38:41], v[148:151], v[196:199], v[38:41]
	v_mfma_f32_16x16x32_bf16 v[34:37], v[156:159], v[196:199], v[34:37]
	v_mfma_f32_16x16x32_bf16 v[22:25], v[148:151], v[216:219], v[22:25]
	v_mfma_f32_16x16x32_bf16 v[18:21], v[156:159], v[216:219], v[18:21]
	v_mfma_f32_16x16x32_bf16 v[62:65], v[152:155], v[184:187], v[62:65]
	v_mfma_f32_16x16x32_bf16 v[58:61], v[160:163], v[184:187], v[58:61]
	v_mfma_f32_16x16x32_bf16 v[54:57], v[152:155], v[192:195], v[54:57]
	v_mfma_f32_16x16x32_bf16 v[50:53], v[160:163], v[192:195], v[50:53]
	v_mfma_f32_16x16x32_bf16 v[38:41], v[152:155], v[200:203], v[38:41]
	v_mfma_f32_16x16x32_bf16 v[34:37], v[160:163], v[200:203], v[34:37]
	v_mfma_f32_16x16x32_bf16 v[22:25], v[152:155], v[220:223], v[22:25]
	v_mfma_f32_16x16x32_bf16 v[18:21], v[160:163], v[220:223], v[18:21]
	v_mfma_f32_16x16x32_bf16 v[46:49], v[164:167], v[180:183], v[46:49]
	v_mfma_f32_16x16x32_bf16 v[42:45], v[172:175], v[180:183], v[42:45]
	v_mfma_f32_16x16x32_bf16 v[30:33], v[164:167], v[188:191], v[30:33]
	v_mfma_f32_16x16x32_bf16 v[26:29], v[172:175], v[188:191], v[26:29]
	v_mfma_f32_16x16x32_bf16 v[14:17], v[164:167], v[196:199], v[14:17]
	v_mfma_f32_16x16x32_bf16 v[10:13], v[172:175], v[196:199], v[10:13]
	v_mfma_f32_16x16x32_bf16 v[6:9], v[164:167], v[216:219], v[6:9]
	v_mfma_f32_16x16x32_bf16 v[2:5], v[172:175], v[216:219], v[2:5]
	v_mfma_f32_16x16x32_bf16 v[46:49], v[168:171], v[184:187], v[46:49]
	v_mfma_f32_16x16x32_bf16 v[42:45], v[176:179], v[184:187], v[42:45]
	v_mfma_f32_16x16x32_bf16 v[30:33], v[168:171], v[192:195], v[30:33]
	v_mfma_f32_16x16x32_bf16 v[26:29], v[176:179], v[192:195], v[26:29]
	v_mfma_f32_16x16x32_bf16 v[14:17], v[168:171], v[200:203], v[14:17]
	v_mfma_f32_16x16x32_bf16 v[10:13], v[176:179], v[200:203], v[10:13]
	v_mfma_f32_16x16x32_bf16 v[6:9], v[168:171], v[220:223], v[6:9]
	v_mfma_f32_16x16x32_bf16 v[2:5], v[176:179], v[220:223], v[2:5]
	s_setprio 0
	s_barrier
	s_add_i32 s22, 0, 0x18000
	s_add_i32 s23, 0, 0x1c000
	v_add_u32_e32 v160, s22, v143
	v_add_u32_e32 v176, s23, v143
	ds_read_b128 v[148:151], v160
	ds_read_b128 v[152:155], v160 offset:1024
	ds_read_b128 v[156:159], v160 offset:2048
	ds_read_b128 v[160:163], v160 offset:3072
	ds_read_b128 v[164:167], v176
	ds_read_b128 v[168:171], v176 offset:1024
	ds_read_b128 v[172:175], v176 offset:2048
	ds_read_b128 v[176:179], v176 offset:3072
	s_add_u32 s20, s30, 0x80000
	s_addc_u32 s21, s31, 0
	s_mov_b32 m0, s27
	v_lshl_add_u64 v[224:225], s[20:21], 0, v[130:131]
	ds_read_b128 v[180:183], v147 offset:32768
	ds_read_b128 v[184:187], v147 offset:33792
	ds_read_b128 v[188:191], v147 offset:34816
	ds_read_b128 v[192:195], v147 offset:35840
	ds_read_b128 v[196:199], v147 offset:36864
	ds_read_b128 v[200:203], v147 offset:37888
	ds_read_b128 v[216:219], v147 offset:38912
	ds_read_b128 v[220:223], v147 offset:39936
	global_load_lds_dwordx4 v[224:225], off
	v_lshl_add_u64 v[224:225], s[20:21], 0, v[134:135]
	s_mov_b32 m0, s48
	s_nop 0
	global_load_lds_dwordx4 v[224:225], off
	s_waitcnt vmcnt(8)
	s_waitcnt lgkmcnt(0)
	s_barrier
	s_setprio 1
	s_waitcnt lgkmcnt(0)
	v_mfma_f32_16x16x32_bf16 v[126:129], v[148:151], v[180:183], v[126:129]
	v_mfma_f32_16x16x32_bf16 v[122:125], v[156:159], v[180:183], v[122:125]
	v_mfma_f32_16x16x32_bf16 v[118:121], v[148:151], v[188:191], v[118:121]
	v_mfma_f32_16x16x32_bf16 v[114:117], v[156:159], v[188:191], v[114:117]
	v_mfma_f32_16x16x32_bf16 v[102:105], v[148:151], v[196:199], v[102:105]
	v_mfma_f32_16x16x32_bf16 v[98:101], v[156:159], v[196:199], v[98:101]
	v_mfma_f32_16x16x32_bf16 v[86:89], v[148:151], v[216:219], v[86:89]
	v_mfma_f32_16x16x32_bf16 v[82:85], v[156:159], v[216:219], v[82:85]
	v_mfma_f32_16x16x32_bf16 v[126:129], v[152:155], v[184:187], v[126:129]
	v_mfma_f32_16x16x32_bf16 v[122:125], v[160:163], v[184:187], v[122:125]
	v_mfma_f32_16x16x32_bf16 v[118:121], v[152:155], v[192:195], v[118:121]
	v_mfma_f32_16x16x32_bf16 v[114:117], v[160:163], v[192:195], v[114:117]
	v_mfma_f32_16x16x32_bf16 v[102:105], v[152:155], v[200:203], v[102:105]
	v_mfma_f32_16x16x32_bf16 v[98:101], v[160:163], v[200:203], v[98:101]
	v_mfma_f32_16x16x32_bf16 v[86:89], v[152:155], v[220:223], v[86:89]
	v_mfma_f32_16x16x32_bf16 v[82:85], v[160:163], v[220:223], v[82:85]
	v_mfma_f32_16x16x32_bf16 v[110:113], v[164:167], v[180:183], v[110:113]
	v_mfma_f32_16x16x32_bf16 v[106:109], v[172:175], v[180:183], v[106:109]
	v_mfma_f32_16x16x32_bf16 v[94:97], v[164:167], v[188:191], v[94:97]
	v_mfma_f32_16x16x32_bf16 v[90:93], v[172:175], v[188:191], v[90:93]
	v_mfma_f32_16x16x32_bf16 v[78:81], v[164:167], v[196:199], v[78:81]
	v_mfma_f32_16x16x32_bf16 v[74:77], v[172:175], v[196:199], v[74:77]
	v_mfma_f32_16x16x32_bf16 v[70:73], v[164:167], v[216:219], v[70:73]
	v_mfma_f32_16x16x32_bf16 v[66:69], v[172:175], v[216:219], v[66:69]
	v_mfma_f32_16x16x32_bf16 v[110:113], v[168:171], v[184:187], v[110:113]
	v_mfma_f32_16x16x32_bf16 v[106:109], v[176:179], v[184:187], v[106:109]
	v_mfma_f32_16x16x32_bf16 v[94:97], v[168:171], v[192:195], v[94:97]
	v_mfma_f32_16x16x32_bf16 v[90:93], v[176:179], v[192:195], v[90:93]
	v_mfma_f32_16x16x32_bf16 v[78:81], v[168:171], v[200:203], v[78:81]
	v_mfma_f32_16x16x32_bf16 v[74:77], v[176:179], v[200:203], v[74:77]
	v_mfma_f32_16x16x32_bf16 v[70:73], v[168:171], v[220:223], v[70:73]
	v_mfma_f32_16x16x32_bf16 v[66:69], v[176:179], v[220:223], v[66:69]
	s_setprio 0
	s_barrier
; #define PG8_STAGE(bufoff, gbase, voff) do { _Pragma("unroll") for (int _i = 0; _i < 2; ++_i) \
;         __builtin_amdgcn_global_load_lds((const unsigned*)((const char*)(gbase) + (voff)[_i]), (LAS unsigned*)(lds + (bufoff) + ldsw + _i * 8192), 16, 0, 0); } while (0)
; #define PG8_STAGE_A(bufoff, kptr, half, VO) do { if constexpr (GATHER) { _Pragma("unroll") for (int _i = 0; _i < 2; ++_i) \
;         __builtin_amdgcn_global_load_lds((const unsigned*)((const char*)(kptr) + (VO)[half][_i]), (LAS unsigned*)(lds + (bufoff) + ldsw + _i * 8192), 16, 0, 0); } \
;         else { PG8_STAGE(bufoff, (kptr) + (half) * hstepA, voffA); } } while (0)
; #define PG8_WAIT_V(n) asm volatile("s_waitcnt vmcnt(" #n ")" ::: "memory")
;     ...
;         for (int t = 0; t < nt; t += 2) {
;             const bool last = (t == nt - 2);
;             const char* a1 = cA + (size_t)(t + 1) * kstep;
;             const char* a2 = last ? nA : cA + (size_t)(t + 2) * kstep; const char* b2 = last ? nB : cB + (size_t)(t + 2) * kstep;
;             const char* a3 = a2 + kstep; const char* b3 = b2 + kstep;
;             unsigned g2[2][2];
;             if constexpr (GATHER) {
; #pragma unroll
;                 for (int _h = 0; _h < 2; ++_h)
; #pragma unroll
;                     for (int _i = 0; _i < 2; ++_i) g2[_h][_i] = last ? gN[_h][_i] : gC[_h][_i]; }
;             if constexpr (SP2) {
;             PG8_LDB(B0, 0, 0); PG8_LDB(B1, 0, 1); PG8_SCHED; PG8_LDA(At, 0, 0); PG8_STAGE_A(PG8_SA(1, 1), a1, 1, gC);
;             PG8_WAIT_V(8); PG8_WAIT_L(0); PG8_BAR; PG8_MMA(0, 0, At, B0); PG8_MMA(0, 1, At, B1); PG8_BAR; PG8_SCHED;
;             PG8_LDA(At, 0, 1); PG8_STAGE(PG8_SB(0, 0), b2, voffB); PG8_STAGE(PG8_SB(0, 1), b2 + hstepB, voffB); PG8_STAGE_A(PG8_SA(0, 0), a2, 0, g2);
;             PG8_WAIT_V(8); PG8_WAIT_L(0); PG8_BAR; PG8_MMA(1, 0, At, B0); PG8_MMA(1, 1, At, B1); PG8_BAR; PG8_SCHED;
;             PG8_LDB(B0, 1, 0); PG8_LDB(B1, 1, 1); PG8_SCHED; PG8_LDA(At, 1, 0); PG8_STAGE_A(PG8_SA(0, 1), a2, 1, g2);
;             PG8_WAIT_V(8); PG8_WAIT_L(0); PG8_BAR; PG8_MMA(0, 0, At, B0); PG8_MMA(0, 1, At, B1); PG8_BAR; PG8_SCHED;
;             PG8_LDA(At, 1, 1); PG8_STAGE(PG8_SB(1, 0), b3, voffB); PG8_STAGE(PG8_SB(1, 1), b3 + hstepB, voffB); PG8_STAGE_A(PG8_SA(1, 0), a3, 0, g2);
;             PG8_WAIT_V(8); PG8_WAIT_L(0); PG8_BAR; PG8_MMA(1, 0, At, B0); PG8_MMA(1, 1, At, B1); PG8_BAR; PG8_SCHED;
	s_add_i32 s20, s22, s12
	v_lshl_add_u64 v[204:205], v[204:205], 0, s[8:9]
	s_mov_b32 m0, s20
	ds_read_b128 v[180:183], v147 offset:49152
	ds_read_b128 v[184:187], v147 offset:50176
	ds_read_b128 v[188:191], v147 offset:51200
	ds_read_b128 v[192:195], v147 offset:52224
	ds_read_b128 v[196:199], v147 offset:53248
	ds_read_b128 v[200:203], v147 offset:54272
	ds_read_b128 v[216:219], v147 offset:55296
	ds_read_b128 v[220:223], v147 offset:56320
	global_load_lds_dwordx4 v[204:205], off
	s_add_i32 m0, s20, 0x2000
	s_add_u32 s0, s0, 0x80080
	v_lshl_add_u64 v[204:205], v[208:209], 0, s[8:9]
	s_addc_u32 s1, s1, 0
	s_add_i32 s20, s23, s12
	global_load_lds_dwordx4 v[204:205], off
	v_lshl_add_u64 v[204:205], s[0:1], 0, v[132:133]
	s_mov_b32 m0, s20
	s_nop 0
	global_load_lds_dwordx4 v[204:205], off
	v_lshl_add_u64 v[204:205], s[0:1], 0, v[136:137]
	s_add_i32 m0, s20, 0x2000
	s_nop 0
	global_load_lds_dwordx4 v[204:205], off
	v_lshl_add_u64 v[204:205], v[210:211], 0, s[8:9]
	s_mov_b32 m0, s49
	s_nop 0
	global_load_lds_dwordx4 v[204:205], off
	v_lshl_add_u64 v[204:205], v[212:213], 0, s[8:9]
	s_mov_b32 m0, s50
	s_nop 0
	global_load_lds_dwordx4 v[204:205], off
	s_waitcnt vmcnt(8)
	s_waitcnt lgkmcnt(0)
	s_barrier
	s_setprio 1
	s_waitcnt lgkmcnt(0)
	v_mfma_f32_16x16x32_bf16 v[62:65], v[148:151], v[180:183], v[62:65]
	v_mfma_f32_16x16x32_bf16 v[58:61], v[156:159], v[180:183], v[58:61]
	v_mfma_f32_16x16x32_bf16 v[54:57], v[148:151], v[188:191], v[54:57]
	v_mfma_f32_16x16x32_bf16 v[50:53], v[156:159], v[188:191], v[50:53]
	v_mfma_f32_16x16x32_bf16 v[38:41], v[148:151], v[196:199], v[38:41]
	v_mfma_f32_16x16x32_bf16 v[34:37], v[156:159], v[196:199], v[34:37]
	v_mfma_f32_16x16x32_bf16 v[22:25], v[148:151], v[216:219], v[22:25]
	v_mfma_f32_16x16x32_bf16 v[18:21], v[156:159], v[216:219], v[18:21]
	v_mfma_f32_16x16x32_bf16 v[62:65], v[152:155], v[184:187], v[62:65]
	v_mfma_f32_16x16x32_bf16 v[58:61], v[160:163], v[184:187], v[58:61]
	v_mfma_f32_16x16x32_bf16 v[54:57], v[152:155], v[192:195], v[54:57]
	v_mfma_f32_16x16x32_bf16 v[50:53], v[160:163], v[192:195], v[50:53]
	v_mfma_f32_16x16x32_bf16 v[38:41], v[152:155], v[200:203], v[38:41]
	v_mfma_f32_16x16x32_bf16 v[34:37], v[160:163], v[200:203], v[34:37]
	v_mfma_f32_16x16x32_bf16 v[22:25], v[152:155], v[220:223], v[22:25]
	v_mfma_f32_16x16x32_bf16 v[18:21], v[160:163], v[220:223], v[18:21]
	v_mfma_f32_16x16x32_bf16 v[46:49], v[164:167], v[180:183], v[46:49]
	v_mfma_f32_16x16x32_bf16 v[42:45], v[172:175], v[180:183], v[42:45]
	v_mfma_f32_16x16x32_bf16 v[30:33], v[164:167], v[188:191], v[30:33]
	v_mfma_f32_16x16x32_bf16 v[26:29], v[172:175], v[188:191], v[26:29]
	v_mfma_f32_16x16x32_bf16 v[14:17], v[164:167], v[196:199], v[14:17]
	v_mfma_f32_16x16x32_bf16 v[10:13], v[172:175], v[196:199], v[10:13]
	v_mfma_f32_16x16x32_bf16 v[6:9], v[164:167], v[216:219], v[6:9]
	v_mfma_f32_16x16x32_bf16 v[2:5], v[172:175], v[216:219], v[2:5]
	v_mfma_f32_16x16x32_bf16 v[46:49], v[168:171], v[184:187], v[46:49]
	v_mfma_f32_16x16x32_bf16 v[42:45], v[176:179], v[184:187], v[42:45]
	v_mfma_f32_16x16x32_bf16 v[30:33], v[168:171], v[192:195], v[30:33]
	v_mfma_f32_16x16x32_bf16 v[26:29], v[176:179], v[192:195], v[26:29]
	v_mfma_f32_16x16x32_bf16 v[14:17], v[168:171], v[200:203], v[14:17]
	v_mfma_f32_16x16x32_bf16 v[10:13], v[176:179], v[200:203], v[10:13]
	v_mfma_f32_16x16x32_bf16 v[6:9], v[168:171], v[220:223], v[6:9]
	v_mfma_f32_16x16x32_bf16 v[2:5], v[176:179], v[220:223], v[2:5]
	s_setprio 0
	s_barrier
	s_add_i32 s19, s19, 2
	s_add_u32 s24, s24, 0x100
	s_addc_u32 s25, s25, 0
	s_add_u32 s17, s17, 0x100
	s_addc_u32 s18, s18, 0
	s_cmp_gt_u32 s19, 29
	s_cbranch_scc0 .LBB0_224
	s_and_b64 vcc, exec, s[36:37]
	s_cbranch_vccz .LBB0_227
	s_barrier

; #define PG8_STAGE(bufoff, gbase, voff) do { _Pragma("unroll") for (int _i = 0; _i < 2; ++_i) \
;         __builtin_amdgcn_global_load_lds((const unsigned*)((const char*)(gbase) + (voff)[_i]), (LAS unsigned*)(lds + (bufoff) + ldsw + _i * 8192), 16, 0, 0); } while (0)
; #define PG8_STAGE_A(bufoff, kptr, half, VO) do { if constexpr (GATHER) { _Pragma("unroll") for (int _i = 0; _i < 2; ++_i) \
;         __builtin_amdgcn_global_load_lds((const unsigned*)((const char*)(kptr) + (VO)[half][_i]), (LAS unsigned*)(lds + (bufoff) + ldsw + _i * 8192), 16, 0, 0); } \
;         else { PG8_STAGE(bufoff, (kptr) + (half) * hstepA, voffA); } } while (0)
; #define PG8_WAIT_V(n) asm volatile("s_waitcnt vmcnt(" #n ")" ::: "memory")
;     ...
;         for (int t = 0; t < nt; t += 2) {
;             const bool last = (t == nt - 2);
;             const char* a1 = cA + (size_t)(t + 1) * kstep;
;             const char* a2 = last ? nA : cA + (size_t)(t + 2) * kstep; const char* b2 = last ? nB : cB + (size_t)(t + 2) * kstep;
;             const char* a3 = a2 + kstep; const char* b3 = b2 + kstep;
;             unsigned g2[2][2];
;             if constexpr (GATHER) {
; #pragma unroll
;                 for (int _h = 0; _h < 2; ++_h)
; #pragma unroll
;                     for (int _i = 0; _i < 2; ++_i) g2[_h][_i] = last ? gN[_h][_i] : gC[_h][_i]; }
;             if constexpr (SP2) {
;             PG8_LDB(B0, 0, 0); PG8_LDB(B1, 0, 1); PG8_SCHED; PG8_LDA(At, 0, 0); PG8_STAGE_A(PG8_SA(1, 1), a1, 1, gC);
;             PG8_WAIT_V(8); PG8_WAIT_L(0); PG8_BAR; PG8_MMA(0, 0, At, B0); PG8_MMA(0, 1, At, B1); PG8_BAR; PG8_SCHED;
;             PG8_LDA(At, 0, 1); PG8_STAGE(PG8_SB(0, 0), b2, voffB); PG8_STAGE(PG8_SB(0, 1), b2 + hstepB, voffB); PG8_STAGE_A(PG8_SA(0, 0), a2, 0, g2);
;             PG8_WAIT_V(8); PG8_WAIT_L(0); PG8_BAR; PG8_MMA(1, 0, At, B0); PG8_MMA(1, 1, At, B1); PG8_BAR; PG8_SCHED;
;             PG8_LDB(B0, 1, 0); PG8_LDB(B1, 1, 1); PG8_SCHED; PG8_LDA(At, 1, 0); PG8_STAGE_A(PG8_SA(0, 1), a2, 1, g2);
;             PG8_WAIT_V(8); PG8_WAIT_L(0); PG8_BAR; PG8_MMA(0, 0, At, B0); PG8_MMA(0, 1, At, B1); PG8_BAR; PG8_SCHED;
;             PG8_LDA(At, 1, 1); PG8_STAGE(PG8_SB(1, 0), b3, voffB); PG8_STAGE(PG8_SB(1, 1), b3 + hstepB, voffB); PG8_STAGE_A(PG8_SA(1, 0), a3, 0, g2);
;             PG8_WAIT_V(8); PG8_WAIT_L(0); PG8_BAR; PG8_MMA(1, 0, At, B0); PG8_MMA(1, 1, At, B1); PG8_BAR; PG8_SCHED;
.LBB0_402:
	s_add_u32 s0, s24, 0xfff80080
	s_addc_u32 s1, s25, -1
	s_add_i32 s16, 0, 0x10000
	s_cmp_eq_u32 s15, 28
	s_cselect_b32 s31, s45, s1
	s_cselect_b32 s30, s44, s0
	s_cselect_b32 s1, s47, s14
	s_cselect_b32 s0, s46, s13
	s_add_i32 s18, 0, 0x14000
	v_add_u32_e32 v160, s16, v143
	v_add_u32_e32 v176, s18, v143
	ds_read_b128 v[148:151], v160
	ds_read_b128 v[152:155], v160 offset:1024
	ds_read_b128 v[156:159], v160 offset:2048
	ds_read_b128 v[160:163], v160 offset:3072
	ds_read_b128 v[164:167], v176
	ds_read_b128 v[168:171], v176 offset:1024
	ds_read_b128 v[172:175], v176 offset:2048
	ds_read_b128 v[176:179], v176 offset:3072
	v_lshl_add_u64 v[204:205], s[24:25], 0, v[138:139]
	s_add_i32 m0, s27, 0xc000
	ds_read_b128 v[180:183], v147
	ds_read_b128 v[184:187], v147 offset:1024
	ds_read_b128 v[188:191], v147 offset:2048
	ds_read_b128 v[192:195], v147 offset:3072
	ds_read_b128 v[196:199], v147 offset:4096
	ds_read_b128 v[200:203], v147 offset:5120
	ds_read_b128 v[216:219], v147 offset:6144
	ds_read_b128 v[220:223], v147 offset:7168
	global_load_lds_dwordx4 v[204:205], off
	v_lshl_add_u64 v[204:205], s[24:25], 0, v[140:141]
	s_add_i32 m0, s27, 0xe000
	s_nop 0
	global_load_lds_dwordx4 v[204:205], off
	s_waitcnt vmcnt(8)
	s_waitcnt lgkmcnt(0)
	s_barrier
	s_setprio 1
	s_waitcnt lgkmcnt(0)
	v_mfma_f32_16x16x32_bf16 v[126:129], v[148:151], v[180:183], v[126:129]
	v_mfma_f32_16x16x32_bf16 v[122:125], v[156:159], v[180:183], v[122:125]
	v_mfma_f32_16x16x32_bf16 v[118:121], v[148:151], v[188:191], v[118:121]
	v_mfma_f32_16x16x32_bf16 v[114:117], v[156:159], v[188:191], v[114:117]
	v_mfma_f32_16x16x32_bf16 v[102:105], v[148:151], v[196:199], v[102:105]
	v_mfma_f32_16x16x32_bf16 v[98:101], v[156:159], v[196:199], v[98:101]
	v_mfma_f32_16x16x32_bf16 v[86:89], v[148:151], v[216:219], v[86:89]
	v_mfma_f32_16x16x32_bf16 v[82:85], v[156:159], v[216:219], v[82:85]
	v_mfma_f32_16x16x32_bf16 v[126:129], v[152:155], v[184:187], v[126:129]
	v_mfma_f32_16x16x32_bf16 v[122:125], v[160:163], v[184:187], v[122:125]
	v_mfma_f32_16x16x32_bf16 v[118:121], v[152:155], v[192:195], v[118:121]
	v_mfma_f32_16x16x32_bf16 v[114:117], v[160:163], v[192:195], v[114:117]
	v_mfma_f32_16x16x32_bf16 v[102:105], v[152:155], v[200:203], v[102:105]
	v_mfma_f32_16x16x32_bf16 v[98:101], v[160:163], v[200:203], v[98:101]
	v_mfma_f32_16x16x32_bf16 v[86:89], v[152:155], v[220:223], v[86:89]
	v_mfma_f32_16x16x32_bf16 v[82:85], v[160:163], v[220:223], v[82:85]
	v_mfma_f32_16x16x32_bf16 v[110:113], v[164:167], v[180:183], v[110:113]
	v_mfma_f32_16x16x32_bf16 v[106:109], v[172:175], v[180:183], v[106:109]
	v_mfma_f32_16x16x32_bf16 v[94:97], v[164:167], v[188:191], v[94:97]
	v_mfma_f32_16x16x32_bf16 v[90:93], v[172:175], v[188:191], v[90:93]
	v_mfma_f32_16x16x32_bf16 v[78:81], v[164:167], v[196:199], v[78:81]
	v_mfma_f32_16x16x32_bf16 v[74:77], v[172:175], v[196:199], v[74:77]
	v_mfma_f32_16x16x32_bf16 v[70:73], v[164:167], v[216:219], v[70:73]
	v_mfma_f32_16x16x32_bf16 v[66:69], v[172:175], v[216:219], v[66:69]
	v_mfma_f32_16x16x32_bf16 v[110:113], v[168:171], v[184:187], v[110:113]
	v_mfma_f32_16x16x32_bf16 v[106:109], v[176:179], v[184:187], v[106:109]
	v_mfma_f32_16x16x32_bf16 v[94:97], v[168:171], v[192:195], v[94:97]
	v_mfma_f32_16x16x32_bf16 v[90:93], v[176:179], v[192:195], v[90:93]
	v_mfma_f32_16x16x32_bf16 v[78:81], v[168:171], v[200:203], v[78:81]
	v_mfma_f32_16x16x32_bf16 v[74:77], v[176:179], v[200:203], v[74:77]
	v_mfma_f32_16x16x32_bf16 v[70:73], v[168:171], v[220:223], v[70:73]
	v_mfma_f32_16x16x32_bf16 v[66:69], v[176:179], v[220:223], v[66:69]
	s_setprio 0
	s_barrier
	s_add_i32 s16, s16, s26
	v_lshl_add_u64 v[204:205], s[0:1], 0, v[132:133]
	s_mov_b32 m0, s16
	ds_read_b128 v[180:183], v147 offset:16384
	ds_read_b128 v[184:187], v147 offset:17408
	ds_read_b128 v[188:191], v147 offset:18432
	ds_read_b128 v[192:195], v147 offset:19456
	ds_read_b128 v[196:199], v147 offset:20480
	ds_read_b128 v[200:203], v147 offset:21504
	ds_read_b128 v[216:219], v147 offset:22528
	ds_read_b128 v[220:223], v147 offset:23552
	global_load_lds_dwordx4 v[204:205], off
	s_add_i32 m0, s16, 0x2000
	s_add_u32 s16, s0, 0x80000
	v_lshl_add_u64 v[208:209], s[0:1], 0, v[136:137]
	s_addc_u32 s17, s1, 0
	s_add_i32 s18, s18, s26
	global_load_lds_dwordx4 v[208:209], off
	v_lshl_add_u64 v[210:211], s[16:17], 0, v[132:133]
	s_mov_b32 m0, s18
	v_lshl_add_u64 v[212:213], s[30:31], 0, v[134:135]
	global_load_lds_dwordx4 v[210:211], off
	v_lshl_add_u64 v[210:211], s[16:17], 0, v[136:137]
	s_add_i32 m0, s18, 0x2000
	s_nop 0
	global_load_lds_dwordx4 v[210:211], off
	v_lshl_add_u64 v[210:211], s[30:31], 0, v[130:131]
	s_mov_b32 m0, s27
	s_nop 0
	global_load_lds_dwordx4 v[210:211], off
	s_mov_b32 m0, s41
	s_nop 0
	global_load_lds_dwordx4 v[212:213], off
	s_waitcnt vmcnt(8)
	s_waitcnt lgkmcnt(0)
	s_barrier
; #define PG8_STAGE(bufoff, gbase, voff) do { _Pragma("unroll") for (int _i = 0; _i < 2; ++_i) \
;         __builtin_amdgcn_global_load_lds((const unsigned*)((const char*)(gbase) + (voff)[_i]), (LAS unsigned*)(lds + (bufoff) + ldsw + _i * 8192), 16, 0, 0); } while (0)
; #define PG8_STAGE_A(bufoff, kptr, half, VO) do { if constexpr (GATHER) { _Pragma("unroll") for (int _i = 0; _i < 2; ++_i) \
;         __builtin_amdgcn_global_load_lds((const unsigned*)((const char*)(kptr) + (VO)[half][_i]), (LAS unsigned*)(lds + (bufoff) + ldsw + _i * 8192), 16, 0, 0); } \
;         else { PG8_STAGE(bufoff, (kptr) + (half) * hstepA, voffA); } } while (0)
; #define PG8_WAIT_V(n) asm volatile("s_waitcnt vmcnt(" #n ")" ::: "memory")
;     ...
;         for (int t = 0; t < nt; t += 2) {
;             const bool last = (t == nt - 2);
;             const char* a1 = cA + (size_t)(t + 1) * kstep;
;             const char* a2 = last ? nA : cA + (size_t)(t + 2) * kstep; const char* b2 = last ? nB : cB + (size_t)(t + 2) * kstep;
;             const char* a3 = a2 + kstep; const char* b3 = b2 + kstep;
;             unsigned g2[2][2];
;             if constexpr (GATHER) {
; #pragma unroll
;                 for (int _h = 0; _h < 2; ++_h)
; #pragma unroll
;                     for (int _i = 0; _i < 2; ++_i) g2[_h][_i] = last ? gN[_h][_i] : gC[_h][_i]; }
;             if constexpr (SP2) {
;             PG8_LDB(B0, 0, 0); PG8_LDB(B1, 0, 1); PG8_SCHED; PG8_LDA(At, 0, 0); PG8_STAGE_A(PG8_SA(1, 1), a1, 1, gC);
;             PG8_WAIT_V(8); PG8_WAIT_L(0); PG8_BAR; PG8_MMA(0, 0, At, B0); PG8_MMA(0, 1, At, B1); PG8_BAR; PG8_SCHED;
;             PG8_LDA(At, 0, 1); PG8_STAGE(PG8_SB(0, 0), b2, voffB); PG8_STAGE(PG8_SB(0, 1), b2 + hstepB, voffB); PG8_STAGE_A(PG8_SA(0, 0), a2, 0, g2);
;             PG8_WAIT_V(8); PG8_WAIT_L(0); PG8_BAR; PG8_MMA(1, 0, At, B0); PG8_MMA(1, 1, At, B1); PG8_BAR; PG8_SCHED;
;             PG8_LDB(B0, 1, 0); PG8_LDB(B1, 1, 1); PG8_SCHED; PG8_LDA(At, 1, 0); PG8_STAGE_A(PG8_SA(0, 1), a2, 1, g2);
;             PG8_WAIT_V(8); PG8_WAIT_L(0); PG8_BAR; PG8_MMA(0, 0, At, B0); PG8_MMA(0, 1, At, B1); PG8_BAR; PG8_SCHED;
;             PG8_LDA(At, 1, 1); PG8_STAGE(PG8_SB(1, 0), b3, voffB); PG8_STAGE(PG8_SB(1, 1), b3 + hstepB, voffB); PG8_STAGE_A(PG8_SA(1, 0), a3, 0, g2);
;             PG8_WAIT_V(8); PG8_WAIT_L(0); PG8_BAR; PG8_MMA(1, 0, At, B0); PG8_MMA(1, 1, At, B1); PG8_BAR; PG8_SCHED;
	s_setprio 1
	s_waitcnt lgkmcnt(0)
	v_mfma_f32_16x16x32_bf16 v[62:65], v[148:151], v[180:183], v[62:65]
	v_mfma_f32_16x16x32_bf16 v[58:61], v[156:159], v[180:183], v[58:61]
	v_mfma_f32_16x16x32_bf16 v[54:57], v[148:151], v[188:191], v[54:57]
	v_mfma_f32_16x16x32_bf16 v[50:53], v[156:159], v[188:191], v[50:53]
	v_mfma_f32_16x16x32_bf16 v[38:41], v[148:151], v[196:199], v[38:41]
	v_mfma_f32_16x16x32_bf16 v[34:37], v[156:159], v[196:199], v[34:37]
	v_mfma_f32_16x16x32_bf16 v[22:25], v[148:151], v[216:219], v[22:25]
	v_mfma_f32_16x16x32_bf16 v[18:21], v[156:159], v[216:219], v[18:21]
	v_mfma_f32_16x16x32_bf16 v[62:65], v[152:155], v[184:187], v[62:65]
	v_mfma_f32_16x16x32_bf16 v[58:61], v[160:163], v[184:187], v[58:61]
	v_mfma_f32_16x16x32_bf16 v[54:57], v[152:155], v[192:195], v[54:57]
	v_mfma_f32_16x16x32_bf16 v[50:53], v[160:163], v[192:195], v[50:53]
	v_mfma_f32_16x16x32_bf16 v[38:41], v[152:155], v[200:203], v[38:41]
	v_mfma_f32_16x16x32_bf16 v[34:37], v[160:163], v[200:203], v[34:37]
	v_mfma_f32_16x16x32_bf16 v[22:25], v[152:155], v[220:223], v[22:25]
	v_mfma_f32_16x16x32_bf16 v[18:21], v[160:163], v[220:223], v[18:21]
	v_mfma_f32_16x16x32_bf16 v[46:49], v[164:167], v[180:183], v[46:49]
	v_mfma_f32_16x16x32_bf16 v[42:45], v[172:175], v[180:183], v[42:45]
	v_mfma_f32_16x16x32_bf16 v[30:33], v[164:167], v[188:191], v[30:33]
	v_mfma_f32_16x16x32_bf16 v[26:29], v[172:175], v[188:191], v[26:29]
	v_mfma_f32_16x16x32_bf16 v[14:17], v[164:167], v[196:199], v[14:17]
	v_mfma_f32_16x16x32_bf16 v[10:13], v[172:175], v[196:199], v[10:13]
	v_mfma_f32_16x16x32_bf16 v[6:9], v[164:167], v[216:219], v[6:9]
	v_mfma_f32_16x16x32_bf16 v[2:5], v[172:175], v[216:219], v[2:5]
	v_mfma_f32_16x16x32_bf16 v[46:49], v[168:171], v[184:187], v[46:49]
	v_mfma_f32_16x16x32_bf16 v[42:45], v[176:179], v[184:187], v[42:45]
	v_mfma_f32_16x16x32_bf16 v[30:33], v[168:171], v[192:195], v[30:33]
	v_mfma_f32_16x16x32_bf16 v[26:29], v[176:179], v[192:195], v[26:29]
	v_mfma_f32_16x16x32_bf16 v[14:17], v[168:171], v[200:203], v[14:17]
	v_mfma_f32_16x16x32_bf16 v[10:13], v[176:179], v[200:203], v[10:13]
	v_mfma_f32_16x16x32_bf16 v[6:9], v[168:171], v[220:223], v[6:9]
	v_mfma_f32_16x16x32_bf16 v[2:5], v[176:179], v[220:223], v[2:5]
	s_setprio 0
	s_barrier
	s_add_i32 s18, 0, 0x18000
	s_add_i32 s19, 0, 0x1c000
	v_add_u32_e32 v160, s18, v143
	v_add_u32_e32 v176, s19, v143
	ds_read_b128 v[148:151], v160
	ds_read_b128 v[152:155], v160 offset:1024
	ds_read_b128 v[156:159], v160 offset:2048
	ds_read_b128 v[160:163], v160 offset:3072
	ds_read_b128 v[164:167], v176
	ds_read_b128 v[168:171], v176 offset:1024
	ds_read_b128 v[172:175], v176 offset:2048
	ds_read_b128 v[176:179], v176 offset:3072
	s_add_u32 s16, s30, 0x80000
	s_addc_u32 s17, s31, 0
	s_mov_b32 m0, s48
	v_lshl_add_u64 v[224:225], s[16:17], 0, v[130:131]
	ds_read_b128 v[180:183], v147 offset:32768
	ds_read_b128 v[184:187], v147 offset:33792
	ds_read_b128 v[188:191], v147 offset:34816
	ds_read_b128 v[192:195], v147 offset:35840
	ds_read_b128 v[196:199], v147 offset:36864
	ds_read_b128 v[200:203], v147 offset:37888
	ds_read_b128 v[216:219], v147 offset:38912
	ds_read_b128 v[220:223], v147 offset:39936
	global_load_lds_dwordx4 v[224:225], off
	v_lshl_add_u64 v[224:225], s[16:17], 0, v[134:135]
	s_mov_b32 m0, s49
	s_nop 0
	global_load_lds_dwordx4 v[224:225], off
	s_waitcnt vmcnt(8)
	s_waitcnt lgkmcnt(0)
	s_barrier
	s_setprio 1
	s_waitcnt lgkmcnt(0)
	v_mfma_f32_16x16x32_bf16 v[126:129], v[148:151], v[180:183], v[126:129]
	v_mfma_f32_16x16x32_bf16 v[122:125], v[156:159], v[180:183], v[122:125]
	v_mfma_f32_16x16x32_bf16 v[118:121], v[148:151], v[188:191], v[118:121]
	v_mfma_f32_16x16x32_bf16 v[114:117], v[156:159], v[188:191], v[114:117]
	v_mfma_f32_16x16x32_bf16 v[102:105], v[148:151], v[196:199], v[102:105]
	v_mfma_f32_16x16x32_bf16 v[98:101], v[156:159], v[196:199], v[98:101]
	v_mfma_f32_16x16x32_bf16 v[86:89], v[148:151], v[216:219], v[86:89]
	v_mfma_f32_16x16x32_bf16 v[82:85], v[156:159], v[216:219], v[82:85]
	v_mfma_f32_16x16x32_bf16 v[126:129], v[152:155], v[184:187], v[126:129]
	v_mfma_f32_16x16x32_bf16 v[122:125], v[160:163], v[184:187], v[122:125]
	v_mfma_f32_16x16x32_bf16 v[118:121], v[152:155], v[192:195], v[118:121]
	v_mfma_f32_16x16x32_bf16 v[114:117], v[160:163], v[192:195], v[114:117]
	v_mfma_f32_16x16x32_bf16 v[102:105], v[152:155], v[200:203], v[102:105]
	v_mfma_f32_16x16x32_bf16 v[98:101], v[160:163], v[200:203], v[98:101]
	v_mfma_f32_16x16x32_bf16 v[86:89], v[152:155], v[220:223], v[86:89]
	v_mfma_f32_16x16x32_bf16 v[82:85], v[160:163], v[220:223], v[82:85]
	v_mfma_f32_16x16x32_bf16 v[110:113], v[164:167], v[180:183], v[110:113]
	v_mfma_f32_16x16x32_bf16 v[106:109], v[172:175], v[180:183], v[106:109]
	v_mfma_f32_16x16x32_bf16 v[94:97], v[164:167], v[188:191], v[94:97]
	v_mfma_f32_16x16x32_bf16 v[90:93], v[172:175], v[188:191], v[90:93]
	v_mfma_f32_16x16x32_bf16 v[78:81], v[164:167], v[196:199], v[78:81]
	v_mfma_f32_16x16x32_bf16 v[74:77], v[172:175], v[196:199], v[74:77]
	v_mfma_f32_16x16x32_bf16 v[70:73], v[164:167], v[216:219], v[70:73]
	v_mfma_f32_16x16x32_bf16 v[66:69], v[172:175], v[216:219], v[66:69]
	v_mfma_f32_16x16x32_bf16 v[110:113], v[168:171], v[184:187], v[110:113]
	v_mfma_f32_16x16x32_bf16 v[106:109], v[176:179], v[184:187], v[106:109]
	v_mfma_f32_16x16x32_bf16 v[94:97], v[168:171], v[192:195], v[94:97]
	v_mfma_f32_16x16x32_bf16 v[90:93], v[176:179], v[192:195], v[90:93]
	v_mfma_f32_16x16x32_bf16 v[78:81], v[168:171], v[200:203], v[78:81]
	v_mfma_f32_16x16x32_bf16 v[74:77], v[176:179], v[200:203], v[74:77]
	v_mfma_f32_16x16x32_bf16 v[70:73], v[168:171], v[220:223], v[70:73]
	v_mfma_f32_16x16x32_bf16 v[66:69], v[176:179], v[220:223], v[66:69]
	s_setprio 0
	s_barrier
; #define PG8_STAGE(bufoff, gbase, voff) do { _Pragma("unroll") for (int _i = 0; _i < 2; ++_i) \
;         __builtin_amdgcn_global_load_lds((const unsigned*)((const char*)(gbase) + (voff)[_i]), (LAS unsigned*)(lds + (bufoff) + ldsw + _i * 8192), 16, 0, 0); } while (0)
; #define PG8_STAGE_A(bufoff, kptr, half, VO) do { if constexpr (GATHER) { _Pragma("unroll") for (int _i = 0; _i < 2; ++_i) \
;         __builtin_amdgcn_global_load_lds((const unsigned*)((const char*)(kptr) + (VO)[half][_i]), (LAS unsigned*)(lds + (bufoff) + ldsw + _i * 8192), 16, 0, 0); } \
;         else { PG8_STAGE(bufoff, (kptr) + (half) * hstepA, voffA); } } while (0)
; #define PG8_WAIT_V(n) asm volatile("s_waitcnt vmcnt(" #n ")" ::: "memory")
;     ...
;         for (int t = 0; t < nt; t += 2) {
;             const bool last = (t == nt - 2);
;             const char* a1 = cA + (size_t)(t + 1) * kstep;
;             const char* a2 = last ? nA : cA + (size_t)(t + 2) * kstep; const char* b2 = last ? nB : cB + (size_t)(t + 2) * kstep;
;             const char* a3 = a2 + kstep; const char* b3 = b2 + kstep;
;             unsigned g2[2][2];
;             if constexpr (GATHER) {
; #pragma unroll
;                 for (int _h = 0; _h < 2; ++_h)
; #pragma unroll
;                     for (int _i = 0; _i < 2; ++_i) g2[_h][_i] = last ? gN[_h][_i] : gC[_h][_i]; }
;             if constexpr (SP2) {
;             PG8_LDB(B0, 0, 0); PG8_LDB(B1, 0, 1); PG8_SCHED; PG8_LDA(At, 0, 0); PG8_STAGE_A(PG8_SA(1, 1), a1, 1, gC);
;             PG8_WAIT_V(8); PG8_WAIT_L(0); PG8_BAR; PG8_MMA(0, 0, At, B0); PG8_MMA(0, 1, At, B1); PG8_BAR; PG8_SCHED;
;             PG8_LDA(At, 0, 1); PG8_STAGE(PG8_SB(0, 0), b2, voffB); PG8_STAGE(PG8_SB(0, 1), b2 + hstepB, voffB); PG8_STAGE_A(PG8_SA(0, 0), a2, 0, g2);
;             PG8_WAIT_V(8); PG8_WAIT_L(0); PG8_BAR; PG8_MMA(1, 0, At, B0); PG8_MMA(1, 1, At, B1); PG8_BAR; PG8_SCHED;
;             PG8_LDB(B0, 1, 0); PG8_LDB(B1, 1, 1); PG8_SCHED; PG8_LDA(At, 1, 0); PG8_STAGE_A(PG8_SA(0, 1), a2, 1, g2);
;             PG8_WAIT_V(8); PG8_WAIT_L(0); PG8_BAR; PG8_MMA(0, 0, At, B0); PG8_MMA(0, 1, At, B1); PG8_BAR; PG8_SCHED;
;             PG8_LDA(At, 1, 1); PG8_STAGE(PG8_SB(1, 0), b3, voffB); PG8_STAGE(PG8_SB(1, 1), b3 + hstepB, voffB); PG8_STAGE_A(PG8_SA(1, 0), a3, 0, g2);
;             PG8_WAIT_V(8); PG8_WAIT_L(0); PG8_BAR; PG8_MMA(1, 0, At, B0); PG8_MMA(1, 1, At, B1); PG8_BAR; PG8_SCHED;
	s_add_i32 s16, s18, s26
	v_lshl_add_u64 v[204:205], v[204:205], 0, s[8:9]
	s_mov_b32 m0, s16
	ds_read_b128 v[180:183], v147 offset:49152
	ds_read_b128 v[184:187], v147 offset:50176
	ds_read_b128 v[188:191], v147 offset:51200
	ds_read_b128 v[192:195], v147 offset:52224
	ds_read_b128 v[196:199], v147 offset:53248
	ds_read_b128 v[200:203], v147 offset:54272
	ds_read_b128 v[216:219], v147 offset:55296
	ds_read_b128 v[220:223], v147 offset:56320
	global_load_lds_dwordx4 v[204:205], off
	s_add_i32 m0, s16, 0x2000
	s_add_u32 s0, s0, 0x80080
	v_lshl_add_u64 v[204:205], v[208:209], 0, s[8:9]
	s_addc_u32 s1, s1, 0
	s_add_i32 s16, s19, s26
	global_load_lds_dwordx4 v[204:205], off
	v_lshl_add_u64 v[204:205], s[0:1], 0, v[132:133]
	s_mov_b32 m0, s16
	s_nop 0
	global_load_lds_dwordx4 v[204:205], off
	v_lshl_add_u64 v[204:205], s[0:1], 0, v[136:137]
	s_add_i32 m0, s16, 0x2000
	s_nop 0
	global_load_lds_dwordx4 v[204:205], off
	v_lshl_add_u64 v[204:205], v[210:211], 0, s[8:9]
	s_mov_b32 m0, s50
	s_nop 0
	global_load_lds_dwordx4 v[204:205], off
	v_lshl_add_u64 v[204:205], v[212:213], 0, s[8:9]
	s_mov_b32 m0, s51
	s_nop 0
	global_load_lds_dwordx4 v[204:205], off
	s_waitcnt vmcnt(8)
	s_waitcnt lgkmcnt(0)
	s_barrier
	s_setprio 1
	s_waitcnt lgkmcnt(0)
	v_mfma_f32_16x16x32_bf16 v[62:65], v[148:151], v[180:183], v[62:65]
	v_mfma_f32_16x16x32_bf16 v[58:61], v[156:159], v[180:183], v[58:61]
	v_mfma_f32_16x16x32_bf16 v[54:57], v[148:151], v[188:191], v[54:57]
	v_mfma_f32_16x16x32_bf16 v[50:53], v[156:159], v[188:191], v[50:53]
	v_mfma_f32_16x16x32_bf16 v[38:41], v[148:151], v[196:199], v[38:41]
	v_mfma_f32_16x16x32_bf16 v[34:37], v[156:159], v[196:199], v[34:37]
	v_mfma_f32_16x16x32_bf16 v[22:25], v[148:151], v[216:219], v[22:25]
	v_mfma_f32_16x16x32_bf16 v[18:21], v[156:159], v[216:219], v[18:21]
	v_mfma_f32_16x16x32_bf16 v[62:65], v[152:155], v[184:187], v[62:65]
	v_mfma_f32_16x16x32_bf16 v[58:61], v[160:163], v[184:187], v[58:61]
	v_mfma_f32_16x16x32_bf16 v[54:57], v[152:155], v[192:195], v[54:57]
	v_mfma_f32_16x16x32_bf16 v[50:53], v[160:163], v[192:195], v[50:53]
	v_mfma_f32_16x16x32_bf16 v[38:41], v[152:155], v[200:203], v[38:41]
	v_mfma_f32_16x16x32_bf16 v[34:37], v[160:163], v[200:203], v[34:37]
	v_mfma_f32_16x16x32_bf16 v[22:25], v[152:155], v[220:223], v[22:25]
	v_mfma_f32_16x16x32_bf16 v[18:21], v[160:163], v[220:223], v[18:21]
	v_mfma_f32_16x16x32_bf16 v[46:49], v[164:167], v[180:183], v[46:49]
	v_mfma_f32_16x16x32_bf16 v[42:45], v[172:175], v[180:183], v[42:45]
	v_mfma_f32_16x16x32_bf16 v[30:33], v[164:167], v[188:191], v[30:33]
	v_mfma_f32_16x16x32_bf16 v[26:29], v[172:175], v[188:191], v[26:29]
	v_mfma_f32_16x16x32_bf16 v[14:17], v[164:167], v[196:199], v[14:17]
	v_mfma_f32_16x16x32_bf16 v[10:13], v[172:175], v[196:199], v[10:13]
	v_mfma_f32_16x16x32_bf16 v[6:9], v[164:167], v[216:219], v[6:9]
	v_mfma_f32_16x16x32_bf16 v[2:5], v[172:175], v[216:219], v[2:5]
	v_mfma_f32_16x16x32_bf16 v[46:49], v[168:171], v[184:187], v[46:49]
	v_mfma_f32_16x16x32_bf16 v[42:45], v[176:179], v[184:187], v[42:45]
	v_mfma_f32_16x16x32_bf16 v[30:33], v[168:171], v[192:195], v[30:33]
	v_mfma_f32_16x16x32_bf16 v[26:29], v[176:179], v[192:195], v[26:29]
	v_mfma_f32_16x16x32_bf16 v[14:17], v[168:171], v[200:203], v[14:17]
	v_mfma_f32_16x16x32_bf16 v[10:13], v[176:179], v[200:203], v[10:13]
	v_mfma_f32_16x16x32_bf16 v[6:9], v[168:171], v[220:223], v[6:9]
	v_mfma_f32_16x16x32_bf16 v[2:5], v[176:179], v[220:223], v[2:5]
	s_setprio 0
	s_barrier
	s_add_i32 s15, s15, 2
	s_add_u32 s24, s24, 0x100
	s_addc_u32 s25, s25, 0
	s_add_u32 s13, s13, 0x100
	s_addc_u32 s14, s14, 0
	s_cmp_gt_u32 s15, 29
	s_cbranch_scc0 .LBB0_402
	s_and_b64 vcc, exec, s[38:39]
	s_cbranch_vccz .LBB0_405
	s_barrier

; #define PG8_STAGE(bufoff, gbase, voff) do { _Pragma("unroll") for (int _i = 0; _i < 2; ++_i) \
;         __builtin_amdgcn_global_load_lds((const unsigned*)((const char*)(gbase) + (voff)[_i]), (LAS unsigned*)(lds + (bufoff) + ldsw + _i * 8192), 16, 0, 0); } while (0)
; #define PG8_STAGE_A(bufoff, kptr, half, VO) do { if constexpr (GATHER) { _Pragma("unroll") for (int _i = 0; _i < 2; ++_i) \
;         __builtin_amdgcn_global_load_lds((const unsigned*)((const char*)(kptr) + (VO)[half][_i]), (LAS unsigned*)(lds + (bufoff) + ldsw + _i * 8192), 16, 0, 0); } \
;         else { PG8_STAGE(bufoff, (kptr) + (half) * hstepA, voffA); } } while (0)
; #define PG8_WAIT_V(n) asm volatile("s_waitcnt vmcnt(" #n ")" ::: "memory")
;     ...
;         for (int t = 0; t < nt; t += 2) {
;             const bool last = (t == nt - 2);
;             const char* a1 = cA + (size_t)(t + 1) * kstep;
;             const char* a2 = last ? nA : cA + (size_t)(t + 2) * kstep; const char* b2 = last ? nB : cB + (size_t)(t + 2) * kstep;
;             const char* a3 = a2 + kstep; const char* b3 = b2 + kstep;
;             unsigned g2[2][2];
;             if constexpr (GATHER) {
; #pragma unroll
;                 for (int _h = 0; _h < 2; ++_h)
; #pragma unroll
;                     for (int _i = 0; _i < 2; ++_i) g2[_h][_i] = last ? gN[_h][_i] : gC[_h][_i]; }
;             if constexpr (SP2) {
;             PG8_LDB(B0, 0, 0); PG8_LDB(B1, 0, 1); PG8_SCHED; PG8_LDA(At, 0, 0); PG8_STAGE_A(PG8_SA(1, 1), a1, 1, gC);
;             PG8_WAIT_V(8); PG8_WAIT_L(0); PG8_BAR; PG8_MMA(0, 0, At, B0); PG8_MMA(0, 1, At, B1); PG8_BAR; PG8_SCHED;
;             PG8_LDA(At, 0, 1); PG8_STAGE(PG8_SB(0, 0), b2, voffB); PG8_STAGE(PG8_SB(0, 1), b2 + hstepB, voffB); PG8_STAGE_A(PG8_SA(0, 0), a2, 0, g2);
;             PG8_WAIT_V(8); PG8_WAIT_L(0); PG8_BAR; PG8_MMA(1, 0, At, B0); PG8_MMA(1, 1, At, B1); PG8_BAR; PG8_SCHED;
;             PG8_LDB(B0, 1, 0); PG8_LDB(B1, 1, 1); PG8_SCHED; PG8_LDA(At, 1, 0); PG8_STAGE_A(PG8_SA(0, 1), a2, 1, g2);
;             PG8_WAIT_V(8); PG8_WAIT_L(0); PG8_BAR; PG8_MMA(0, 0, At, B0); PG8_MMA(0, 1, At, B1); PG8_BAR; PG8_SCHED;
;             PG8_LDA(At, 1, 1); PG8_STAGE(PG8_SB(1, 0), b3, voffB); PG8_STAGE(PG8_SB(1, 1), b3 + hstepB, voffB); PG8_STAGE_A(PG8_SA(1, 0), a3, 0, g2);
;             PG8_WAIT_V(8); PG8_WAIT_L(0); PG8_BAR; PG8_MMA(1, 0, At, B0); PG8_MMA(1, 1, At, B1); PG8_BAR; PG8_SCHED;
.LBB0_615:
	s_add_u32 s0, s38, 0x100
	s_addc_u32 s1, s39, 0
	s_add_i32 s15, 0, 0x10000
	s_cmp_eq_u32 s14, 2
	s_cselect_b32 s31, s45, s1
	s_cselect_b32 s30, s44, s0
	s_cselect_b32 s25, s47, s13
	s_cselect_b32 s24, s46, s12
	s_add_i32 s18, 0, 0x14000
	s_waitcnt vmcnt(0)
	v_add_u32_e32 v106, s15, v217
	v_add_u32_e32 v150, s18, v217
	ds_read_b128 v[82:85], v106
	ds_read_b128 v[86:89], v106 offset:1024
	ds_read_b128 v[102:105], v106 offset:2048
	ds_read_b128 v[106:109], v106 offset:3072
	ds_read_b128 v[122:125], v150
	ds_read_b128 v[126:129], v150 offset:1024
	ds_read_b128 v[146:149], v150 offset:2048
	ds_read_b128 v[150:153], v150 offset:3072
	v_lshl_add_u64 v[208:209], s[38:39], 0, v[202:203]
	s_add_i32 m0, s61, 0xc000
	ds_read_b128 v[162:165], v221
	ds_read_b128 v[166:169], v221 offset:1024
	ds_read_b128 v[170:173], v221 offset:2048
	ds_read_b128 v[174:177], v221 offset:3072
	ds_read_b128 v[178:181], v221 offset:4096
	ds_read_b128 v[182:185], v221 offset:5120
	ds_read_b128 v[186:189], v221 offset:6144
	ds_read_b128 v[190:193], v221 offset:7168
	global_load_lds_dwordx4 v[208:209], off
	v_lshl_add_u64 v[208:209], s[38:39], 0, v[204:205]
	s_add_i32 m0, s61, 0xe000
	s_nop 0
	global_load_lds_dwordx4 v[208:209], off
	s_waitcnt vmcnt(8)
	s_waitcnt lgkmcnt(0)
	s_barrier
	s_setprio 1
	s_waitcnt lgkmcnt(0)
	v_mfma_f32_16x16x32_bf16 v[158:161], v[82:85], v[162:165], v[158:161]
	v_mfma_f32_16x16x32_bf16 v[154:157], v[102:105], v[162:165], v[154:157]
	v_mfma_f32_16x16x32_bf16 v[134:137], v[82:85], v[170:173], v[134:137]
	v_mfma_f32_16x16x32_bf16 v[130:133], v[102:105], v[170:173], v[130:133]
	v_mfma_f32_16x16x32_bf16 v[110:113], v[82:85], v[178:181], v[110:113]
	v_mfma_f32_16x16x32_bf16 v[98:101], v[102:105], v[178:181], v[98:101]
	v_mfma_f32_16x16x32_bf16 v[78:81], v[82:85], v[186:189], v[78:81]
	v_mfma_f32_16x16x32_bf16 v[74:77], v[102:105], v[186:189], v[74:77]
	v_mfma_f32_16x16x32_bf16 v[158:161], v[86:89], v[166:169], v[158:161]
	v_mfma_f32_16x16x32_bf16 v[154:157], v[106:109], v[166:169], v[154:157]
	v_mfma_f32_16x16x32_bf16 v[134:137], v[86:89], v[174:177], v[134:137]
	v_mfma_f32_16x16x32_bf16 v[130:133], v[106:109], v[174:177], v[130:133]
	v_mfma_f32_16x16x32_bf16 v[110:113], v[86:89], v[182:185], v[110:113]
	v_mfma_f32_16x16x32_bf16 v[98:101], v[106:109], v[182:185], v[98:101]
	v_mfma_f32_16x16x32_bf16 v[78:81], v[86:89], v[190:193], v[78:81]
	v_mfma_f32_16x16x32_bf16 v[74:77], v[106:109], v[190:193], v[74:77]
	v_mfma_f32_16x16x32_bf16 v[142:145], v[122:125], v[162:165], v[142:145]
	v_mfma_f32_16x16x32_bf16 v[138:141], v[146:149], v[162:165], v[138:141]
	v_mfma_f32_16x16x32_bf16 v[118:121], v[122:125], v[170:173], v[118:121]
	v_mfma_f32_16x16x32_bf16 v[114:117], v[146:149], v[170:173], v[114:117]
	v_mfma_f32_16x16x32_bf16 v[94:97], v[122:125], v[178:181], v[94:97]
	v_mfma_f32_16x16x32_bf16 v[90:93], v[146:149], v[178:181], v[90:93]
	v_mfma_f32_16x16x32_bf16 v[70:73], v[122:125], v[186:189], v[70:73]
	v_mfma_f32_16x16x32_bf16 v[66:69], v[146:149], v[186:189], v[66:69]
	v_mfma_f32_16x16x32_bf16 v[142:145], v[126:129], v[166:169], v[142:145]
	v_mfma_f32_16x16x32_bf16 v[138:141], v[150:153], v[166:169], v[138:141]
	v_mfma_f32_16x16x32_bf16 v[118:121], v[126:129], v[174:177], v[118:121]
	v_mfma_f32_16x16x32_bf16 v[114:117], v[150:153], v[174:177], v[114:117]
	v_mfma_f32_16x16x32_bf16 v[94:97], v[126:129], v[182:185], v[94:97]
	v_mfma_f32_16x16x32_bf16 v[90:93], v[150:153], v[182:185], v[90:93]
	v_mfma_f32_16x16x32_bf16 v[70:73], v[126:129], v[190:193], v[70:73]
	v_mfma_f32_16x16x32_bf16 v[66:69], v[150:153], v[190:193], v[66:69]
	s_setprio 0
	s_barrier
	s_add_i32 s15, s15, s60
	v_lshl_add_u64 v[208:209], s[24:25], 0, v[194:195]
	s_mov_b32 m0, s15
	ds_read_b128 v[162:165], v221 offset:16384
	ds_read_b128 v[166:169], v221 offset:17408
	ds_read_b128 v[170:173], v221 offset:18432
	ds_read_b128 v[174:177], v221 offset:19456
	ds_read_b128 v[178:181], v221 offset:20480
	ds_read_b128 v[182:185], v221 offset:21504
	ds_read_b128 v[186:189], v221 offset:22528
	ds_read_b128 v[190:193], v221 offset:23552
	global_load_lds_dwordx4 v[208:209], off
	s_add_i32 m0, s15, 0x2000
	s_add_u32 s16, s24, 0x18000
	v_lshl_add_u64 v[210:211], s[24:25], 0, v[196:197]
	s_addc_u32 s17, s25, 0
	s_add_i32 s15, s18, s60
	global_load_lds_dwordx4 v[210:211], off
	v_lshl_add_u64 v[212:213], s[16:17], 0, v[194:195]
	s_mov_b32 m0, s15
	v_lshl_add_u64 v[222:223], s[30:31], 0, v[196:197]
	global_load_lds_dwordx4 v[212:213], off
	v_lshl_add_u64 v[212:213], s[16:17], 0, v[196:197]
	s_add_i32 m0, s15, 0x2000
	s_nop 0
	global_load_lds_dwordx4 v[212:213], off
	v_lshl_add_u64 v[212:213], s[30:31], 0, v[194:195]
	s_mov_b32 m0, s61
	s_nop 0
	global_load_lds_dwordx4 v[212:213], off
	s_mov_b32 m0, s63
	s_nop 0
	global_load_lds_dwordx4 v[222:223], off
	s_waitcnt vmcnt(8)
	s_waitcnt lgkmcnt(0)
	s_barrier
; #define PG8_STAGE(bufoff, gbase, voff) do { _Pragma("unroll") for (int _i = 0; _i < 2; ++_i) \
;         __builtin_amdgcn_global_load_lds((const unsigned*)((const char*)(gbase) + (voff)[_i]), (LAS unsigned*)(lds + (bufoff) + ldsw + _i * 8192), 16, 0, 0); } while (0)
; #define PG8_STAGE_A(bufoff, kptr, half, VO) do { if constexpr (GATHER) { _Pragma("unroll") for (int _i = 0; _i < 2; ++_i) \
;         __builtin_amdgcn_global_load_lds((const unsigned*)((const char*)(kptr) + (VO)[half][_i]), (LAS unsigned*)(lds + (bufoff) + ldsw + _i * 8192), 16, 0, 0); } \
;         else { PG8_STAGE(bufoff, (kptr) + (half) * hstepA, voffA); } } while (0)
; #define PG8_WAIT_V(n) asm volatile("s_waitcnt vmcnt(" #n ")" ::: "memory")
;     ...
;         for (int t = 0; t < nt; t += 2) {
;             const bool last = (t == nt - 2);
;             const char* a1 = cA + (size_t)(t + 1) * kstep;
;             const char* a2 = last ? nA : cA + (size_t)(t + 2) * kstep; const char* b2 = last ? nB : cB + (size_t)(t + 2) * kstep;
;             const char* a3 = a2 + kstep; const char* b3 = b2 + kstep;
;             unsigned g2[2][2];
;             if constexpr (GATHER) {
; #pragma unroll
;                 for (int _h = 0; _h < 2; ++_h)
; #pragma unroll
;                     for (int _i = 0; _i < 2; ++_i) g2[_h][_i] = last ? gN[_h][_i] : gC[_h][_i]; }
;             if constexpr (SP2) {
;             PG8_LDB(B0, 0, 0); PG8_LDB(B1, 0, 1); PG8_SCHED; PG8_LDA(At, 0, 0); PG8_STAGE_A(PG8_SA(1, 1), a1, 1, gC);
;             PG8_WAIT_V(8); PG8_WAIT_L(0); PG8_BAR; PG8_MMA(0, 0, At, B0); PG8_MMA(0, 1, At, B1); PG8_BAR; PG8_SCHED;
;             PG8_LDA(At, 0, 1); PG8_STAGE(PG8_SB(0, 0), b2, voffB); PG8_STAGE(PG8_SB(0, 1), b2 + hstepB, voffB); PG8_STAGE_A(PG8_SA(0, 0), a2, 0, g2);
;             PG8_WAIT_V(8); PG8_WAIT_L(0); PG8_BAR; PG8_MMA(1, 0, At, B0); PG8_MMA(1, 1, At, B1); PG8_BAR; PG8_SCHED;
;             PG8_LDB(B0, 1, 0); PG8_LDB(B1, 1, 1); PG8_SCHED; PG8_LDA(At, 1, 0); PG8_STAGE_A(PG8_SA(0, 1), a2, 1, g2);
;             PG8_WAIT_V(8); PG8_WAIT_L(0); PG8_BAR; PG8_MMA(0, 0, At, B0); PG8_MMA(0, 1, At, B1); PG8_BAR; PG8_SCHED;
;             PG8_LDA(At, 1, 1); PG8_STAGE(PG8_SB(1, 0), b3, voffB); PG8_STAGE(PG8_SB(1, 1), b3 + hstepB, voffB); PG8_STAGE_A(PG8_SA(1, 0), a3, 0, g2);
;             PG8_WAIT_V(8); PG8_WAIT_L(0); PG8_BAR; PG8_MMA(1, 0, At, B0); PG8_MMA(1, 1, At, B1); PG8_BAR; PG8_SCHED;
	s_setprio 1
	s_waitcnt lgkmcnt(0)
	v_mfma_f32_16x16x32_bf16 v[62:65], v[82:85], v[162:165], v[62:65]
	v_mfma_f32_16x16x32_bf16 v[58:61], v[102:105], v[162:165], v[58:61]
	v_mfma_f32_16x16x32_bf16 v[46:49], v[82:85], v[170:173], v[46:49]
	v_mfma_f32_16x16x32_bf16 v[42:45], v[102:105], v[170:173], v[42:45]
	v_mfma_f32_16x16x32_bf16 v[30:33], v[82:85], v[178:181], v[30:33]
	v_mfma_f32_16x16x32_bf16 v[26:29], v[102:105], v[178:181], v[26:29]
	v_mfma_f32_16x16x32_bf16 v[14:17], v[82:85], v[186:189], v[14:17]
	v_mfma_f32_16x16x32_bf16 v[10:13], v[102:105], v[186:189], v[10:13]
	v_mfma_f32_16x16x32_bf16 v[62:65], v[86:89], v[166:169], v[62:65]
	v_mfma_f32_16x16x32_bf16 v[58:61], v[106:109], v[166:169], v[58:61]
	v_mfma_f32_16x16x32_bf16 v[46:49], v[86:89], v[174:177], v[46:49]
	v_mfma_f32_16x16x32_bf16 v[42:45], v[106:109], v[174:177], v[42:45]
	v_mfma_f32_16x16x32_bf16 v[30:33], v[86:89], v[182:185], v[30:33]
	v_mfma_f32_16x16x32_bf16 v[26:29], v[106:109], v[182:185], v[26:29]
	v_mfma_f32_16x16x32_bf16 v[14:17], v[86:89], v[190:193], v[14:17]
	v_mfma_f32_16x16x32_bf16 v[10:13], v[106:109], v[190:193], v[10:13]
	v_mfma_f32_16x16x32_bf16 v[54:57], v[122:125], v[162:165], v[54:57]
	v_mfma_f32_16x16x32_bf16 v[50:53], v[146:149], v[162:165], v[50:53]
	v_mfma_f32_16x16x32_bf16 v[38:41], v[122:125], v[170:173], v[38:41]
	v_mfma_f32_16x16x32_bf16 v[34:37], v[146:149], v[170:173], v[34:37]
	v_mfma_f32_16x16x32_bf16 v[22:25], v[122:125], v[178:181], v[22:25]
	v_mfma_f32_16x16x32_bf16 v[18:21], v[146:149], v[178:181], v[18:21]
	v_mfma_f32_16x16x32_bf16 v[6:9], v[122:125], v[186:189], v[6:9]
	v_mfma_f32_16x16x32_bf16 v[2:5], v[146:149], v[186:189], v[2:5]
	v_mfma_f32_16x16x32_bf16 v[54:57], v[126:129], v[166:169], v[54:57]
	v_mfma_f32_16x16x32_bf16 v[50:53], v[150:153], v[166:169], v[50:53]
	v_mfma_f32_16x16x32_bf16 v[38:41], v[126:129], v[174:177], v[38:41]
	v_mfma_f32_16x16x32_bf16 v[34:37], v[150:153], v[174:177], v[34:37]
	v_mfma_f32_16x16x32_bf16 v[22:25], v[126:129], v[182:185], v[22:25]
	v_mfma_f32_16x16x32_bf16 v[18:21], v[150:153], v[182:185], v[18:21]
	v_mfma_f32_16x16x32_bf16 v[6:9], v[126:129], v[190:193], v[6:9]
	v_mfma_f32_16x16x32_bf16 v[2:5], v[150:153], v[190:193], v[2:5]
	s_setprio 0
	s_barrier
	s_add_i32 s15, 0, 0x18000
	s_add_i32 s18, 0, 0x1c000
	v_add_u32_e32 v106, s15, v217
	v_add_u32_e32 v150, s18, v217
	ds_read_b128 v[82:85], v106
	ds_read_b128 v[86:89], v106 offset:1024
	ds_read_b128 v[102:105], v106 offset:2048
	ds_read_b128 v[106:109], v106 offset:3072
	ds_read_b128 v[122:125], v150
	ds_read_b128 v[126:129], v150 offset:1024
	ds_read_b128 v[146:149], v150 offset:2048
	ds_read_b128 v[150:153], v150 offset:3072
	s_add_u32 s16, s30, 0x18000
	s_addc_u32 s17, s31, 0
	s_mov_b32 m0, s64
	v_lshl_add_u64 v[224:225], s[16:17], 0, v[194:195]
	ds_read_b128 v[162:165], v221 offset:32768
	ds_read_b128 v[166:169], v221 offset:33792
	ds_read_b128 v[170:173], v221 offset:34816
	ds_read_b128 v[174:177], v221 offset:35840
	ds_read_b128 v[178:181], v221 offset:36864
	ds_read_b128 v[182:185], v221 offset:37888
	ds_read_b128 v[186:189], v221 offset:38912
	ds_read_b128 v[190:193], v221 offset:39936
	global_load_lds_dwordx4 v[224:225], off
	v_lshl_add_u64 v[224:225], s[16:17], 0, v[196:197]
	s_mov_b32 m0, s65
	s_nop 0
	global_load_lds_dwordx4 v[224:225], off
	s_waitcnt vmcnt(8)
	s_waitcnt lgkmcnt(0)
	s_barrier
	s_setprio 1
	s_waitcnt lgkmcnt(0)
	v_mfma_f32_16x16x32_bf16 v[158:161], v[82:85], v[162:165], v[158:161]
	v_mfma_f32_16x16x32_bf16 v[154:157], v[102:105], v[162:165], v[154:157]
	v_mfma_f32_16x16x32_bf16 v[134:137], v[82:85], v[170:173], v[134:137]
	v_mfma_f32_16x16x32_bf16 v[130:133], v[102:105], v[170:173], v[130:133]
	v_mfma_f32_16x16x32_bf16 v[110:113], v[82:85], v[178:181], v[110:113]
	v_mfma_f32_16x16x32_bf16 v[98:101], v[102:105], v[178:181], v[98:101]
	v_mfma_f32_16x16x32_bf16 v[78:81], v[82:85], v[186:189], v[78:81]
	v_mfma_f32_16x16x32_bf16 v[74:77], v[102:105], v[186:189], v[74:77]
	v_mfma_f32_16x16x32_bf16 v[158:161], v[86:89], v[166:169], v[158:161]
	v_mfma_f32_16x16x32_bf16 v[154:157], v[106:109], v[166:169], v[154:157]
	v_mfma_f32_16x16x32_bf16 v[134:137], v[86:89], v[174:177], v[134:137]
	v_mfma_f32_16x16x32_bf16 v[130:133], v[106:109], v[174:177], v[130:133]
	v_mfma_f32_16x16x32_bf16 v[110:113], v[86:89], v[182:185], v[110:113]
	v_mfma_f32_16x16x32_bf16 v[98:101], v[106:109], v[182:185], v[98:101]
	v_mfma_f32_16x16x32_bf16 v[78:81], v[86:89], v[190:193], v[78:81]
	v_mfma_f32_16x16x32_bf16 v[74:77], v[106:109], v[190:193], v[74:77]
	v_mfma_f32_16x16x32_bf16 v[142:145], v[122:125], v[162:165], v[142:145]
	v_mfma_f32_16x16x32_bf16 v[138:141], v[146:149], v[162:165], v[138:141]
	v_mfma_f32_16x16x32_bf16 v[118:121], v[122:125], v[170:173], v[118:121]
	v_mfma_f32_16x16x32_bf16 v[114:117], v[146:149], v[170:173], v[114:117]
	v_mfma_f32_16x16x32_bf16 v[94:97], v[122:125], v[178:181], v[94:97]
	v_mfma_f32_16x16x32_bf16 v[90:93], v[146:149], v[178:181], v[90:93]
	v_mfma_f32_16x16x32_bf16 v[70:73], v[122:125], v[186:189], v[70:73]
	v_mfma_f32_16x16x32_bf16 v[66:69], v[146:149], v[186:189], v[66:69]
	v_mfma_f32_16x16x32_bf16 v[142:145], v[126:129], v[166:169], v[142:145]
	v_mfma_f32_16x16x32_bf16 v[138:141], v[150:153], v[166:169], v[138:141]
	v_mfma_f32_16x16x32_bf16 v[118:121], v[126:129], v[174:177], v[118:121]
	v_mfma_f32_16x16x32_bf16 v[114:117], v[150:153], v[174:177], v[114:117]
	v_mfma_f32_16x16x32_bf16 v[94:97], v[126:129], v[182:185], v[94:97]
	v_mfma_f32_16x16x32_bf16 v[90:93], v[150:153], v[182:185], v[90:93]
	v_mfma_f32_16x16x32_bf16 v[70:73], v[126:129], v[190:193], v[70:73]
	v_mfma_f32_16x16x32_bf16 v[66:69], v[150:153], v[190:193], v[66:69]
	s_setprio 0
	s_barrier
; #define PG8_STAGE(bufoff, gbase, voff) do { _Pragma("unroll") for (int _i = 0; _i < 2; ++_i) \
;         __builtin_amdgcn_global_load_lds((const unsigned*)((const char*)(gbase) + (voff)[_i]), (LAS unsigned*)(lds + (bufoff) + ldsw + _i * 8192), 16, 0, 0); } while (0)
; #define PG8_STAGE_A(bufoff, kptr, half, VO) do { if constexpr (GATHER) { _Pragma("unroll") for (int _i = 0; _i < 2; ++_i) \
;         __builtin_amdgcn_global_load_lds((const unsigned*)((const char*)(kptr) + (VO)[half][_i]), (LAS unsigned*)(lds + (bufoff) + ldsw + _i * 8192), 16, 0, 0); } \
;         else { PG8_STAGE(bufoff, (kptr) + (half) * hstepA, voffA); } } while (0)
; #define PG8_WAIT_V(n) asm volatile("s_waitcnt vmcnt(" #n ")" ::: "memory")
;     ...
;         for (int t = 0; t < nt; t += 2) {
;             const bool last = (t == nt - 2);
;             const char* a1 = cA + (size_t)(t + 1) * kstep;
;             const char* a2 = last ? nA : cA + (size_t)(t + 2) * kstep; const char* b2 = last ? nB : cB + (size_t)(t + 2) * kstep;
;             const char* a3 = a2 + kstep; const char* b3 = b2 + kstep;
;             unsigned g2[2][2];
;             if constexpr (GATHER) {
; #pragma unroll
;                 for (int _h = 0; _h < 2; ++_h)
; #pragma unroll
;                     for (int _i = 0; _i < 2; ++_i) g2[_h][_i] = last ? gN[_h][_i] : gC[_h][_i]; }
;             if constexpr (SP2) {
;             PG8_LDB(B0, 0, 0); PG8_LDB(B1, 0, 1); PG8_SCHED; PG8_LDA(At, 0, 0); PG8_STAGE_A(PG8_SA(1, 1), a1, 1, gC);
;             PG8_WAIT_V(8); PG8_WAIT_L(0); PG8_BAR; PG8_MMA(0, 0, At, B0); PG8_MMA(0, 1, At, B1); PG8_BAR; PG8_SCHED;
;             PG8_LDA(At, 0, 1); PG8_STAGE(PG8_SB(0, 0), b2, voffB); PG8_STAGE(PG8_SB(0, 1), b2 + hstepB, voffB); PG8_STAGE_A(PG8_SA(0, 0), a2, 0, g2);
;             PG8_WAIT_V(8); PG8_WAIT_L(0); PG8_BAR; PG8_MMA(1, 0, At, B0); PG8_MMA(1, 1, At, B1); PG8_BAR; PG8_SCHED;
;             PG8_LDB(B0, 1, 0); PG8_LDB(B1, 1, 1); PG8_SCHED; PG8_LDA(At, 1, 0); PG8_STAGE_A(PG8_SA(0, 1), a2, 1, g2);
;             PG8_WAIT_V(8); PG8_WAIT_L(0); PG8_BAR; PG8_MMA(0, 0, At, B0); PG8_MMA(0, 1, At, B1); PG8_BAR; PG8_SCHED;
;             PG8_LDA(At, 1, 1); PG8_STAGE(PG8_SB(1, 0), b3, voffB); PG8_STAGE(PG8_SB(1, 1), b3 + hstepB, voffB); PG8_STAGE_A(PG8_SA(1, 0), a3, 0, g2);
;             PG8_WAIT_V(8); PG8_WAIT_L(0); PG8_BAR; PG8_MMA(1, 0, At, B0); PG8_MMA(1, 1, At, B1); PG8_BAR; PG8_SCHED;
	s_add_i32 s15, s15, s60
	v_lshl_add_u64 v[208:209], v[208:209], 0, s[8:9]
	s_mov_b32 m0, s15
	ds_read_b128 v[162:165], v221 offset:49152
	ds_read_b128 v[166:169], v221 offset:50176
	ds_read_b128 v[170:173], v221 offset:51200
	ds_read_b128 v[174:177], v221 offset:52224
	ds_read_b128 v[178:181], v221 offset:53248
	ds_read_b128 v[182:185], v221 offset:54272
	ds_read_b128 v[186:189], v221 offset:55296
	ds_read_b128 v[190:193], v221 offset:56320
	global_load_lds_dwordx4 v[208:209], off
	s_add_i32 m0, s15, 0x2000
	s_add_u32 s16, s24, 0x18080
	v_lshl_add_u64 v[208:209], v[210:211], 0, s[8:9]
	s_addc_u32 s17, s25, 0
	s_add_i32 s15, s18, s60
	global_load_lds_dwordx4 v[208:209], off
	v_lshl_add_u64 v[208:209], s[16:17], 0, v[194:195]
	s_mov_b32 m0, s15
	s_nop 0
	global_load_lds_dwordx4 v[208:209], off
	v_lshl_add_u64 v[208:209], s[16:17], 0, v[196:197]
	s_add_i32 m0, s15, 0x2000
	s_nop 0
	global_load_lds_dwordx4 v[208:209], off
	v_lshl_add_u64 v[208:209], v[212:213], 0, s[8:9]
	s_mov_b32 m0, s67
	s_nop 0
	global_load_lds_dwordx4 v[208:209], off
	v_lshl_add_u64 v[208:209], v[222:223], 0, s[8:9]
	s_mov_b32 m0, s68
	s_nop 0
	global_load_lds_dwordx4 v[208:209], off
	s_waitcnt vmcnt(8)
	s_waitcnt lgkmcnt(0)
	s_barrier
	s_setprio 1
	s_waitcnt lgkmcnt(0)
	v_mfma_f32_16x16x32_bf16 v[62:65], v[82:85], v[162:165], v[62:65]
	v_mfma_f32_16x16x32_bf16 v[58:61], v[102:105], v[162:165], v[58:61]
	v_mfma_f32_16x16x32_bf16 v[46:49], v[82:85], v[170:173], v[46:49]
	v_mfma_f32_16x16x32_bf16 v[42:45], v[102:105], v[170:173], v[42:45]
	v_mfma_f32_16x16x32_bf16 v[30:33], v[82:85], v[178:181], v[30:33]
	v_mfma_f32_16x16x32_bf16 v[26:29], v[102:105], v[178:181], v[26:29]
	v_mfma_f32_16x16x32_bf16 v[14:17], v[82:85], v[186:189], v[14:17]
	v_mfma_f32_16x16x32_bf16 v[10:13], v[102:105], v[186:189], v[10:13]
	v_mfma_f32_16x16x32_bf16 v[62:65], v[86:89], v[166:169], v[62:65]
	v_mfma_f32_16x16x32_bf16 v[58:61], v[106:109], v[166:169], v[58:61]
	v_mfma_f32_16x16x32_bf16 v[46:49], v[86:89], v[174:177], v[46:49]
	v_mfma_f32_16x16x32_bf16 v[42:45], v[106:109], v[174:177], v[42:45]
	v_mfma_f32_16x16x32_bf16 v[30:33], v[86:89], v[182:185], v[30:33]
	v_mfma_f32_16x16x32_bf16 v[26:29], v[106:109], v[182:185], v[26:29]
	v_mfma_f32_16x16x32_bf16 v[14:17], v[86:89], v[190:193], v[14:17]
	v_mfma_f32_16x16x32_bf16 v[10:13], v[106:109], v[190:193], v[10:13]
	v_mfma_f32_16x16x32_bf16 v[54:57], v[122:125], v[162:165], v[54:57]
	v_mfma_f32_16x16x32_bf16 v[50:53], v[146:149], v[162:165], v[50:53]
	v_mfma_f32_16x16x32_bf16 v[38:41], v[122:125], v[170:173], v[38:41]
	v_mfma_f32_16x16x32_bf16 v[34:37], v[146:149], v[170:173], v[34:37]
	v_mfma_f32_16x16x32_bf16 v[22:25], v[122:125], v[178:181], v[22:25]
	v_mfma_f32_16x16x32_bf16 v[18:21], v[146:149], v[178:181], v[18:21]
	v_mfma_f32_16x16x32_bf16 v[6:9], v[122:125], v[186:189], v[6:9]
	v_mfma_f32_16x16x32_bf16 v[2:5], v[146:149], v[186:189], v[2:5]
	v_mfma_f32_16x16x32_bf16 v[54:57], v[126:129], v[166:169], v[54:57]
	v_mfma_f32_16x16x32_bf16 v[50:53], v[150:153], v[166:169], v[50:53]
	v_mfma_f32_16x16x32_bf16 v[38:41], v[126:129], v[174:177], v[38:41]
	v_mfma_f32_16x16x32_bf16 v[34:37], v[150:153], v[174:177], v[34:37]
	v_mfma_f32_16x16x32_bf16 v[22:25], v[126:129], v[182:185], v[22:25]
	v_mfma_f32_16x16x32_bf16 v[18:21], v[150:153], v[182:185], v[18:21]
	v_mfma_f32_16x16x32_bf16 v[6:9], v[126:129], v[190:193], v[6:9]
	v_mfma_f32_16x16x32_bf16 v[2:5], v[150:153], v[190:193], v[2:5]
	s_setprio 0
	s_barrier
	s_add_i32 s14, s14, 2
	s_add_u32 s12, s12, 0x100
	s_addc_u32 s13, s13, 0
	s_cmp_gt_u32 s14, 3
	s_mov_b64 s[38:39], s[0:1]
	s_cbranch_scc0 .LBB0_615
	s_and_b64 vcc, exec, s[42:43]
	s_cbranch_vccz .LBB0_618
	s_barrier

; #define PG8_STAGE(bufoff, gbase, voff) do { _Pragma("unroll") for (int _i = 0; _i < 2; ++_i) \
;         __builtin_amdgcn_global_load_lds((const unsigned*)((const char*)(gbase) + (voff)[_i]), (LAS unsigned*)(lds + (bufoff) + ldsw + _i * 8192), 16, 0, 0); } while (0)
; #define PG8_STAGE_A(bufoff, kptr, half, VO) do { if constexpr (GATHER) { _Pragma("unroll") for (int _i = 0; _i < 2; ++_i) \
;         __builtin_amdgcn_global_load_lds((const unsigned*)((const char*)(kptr) + (VO)[half][_i]), (LAS unsigned*)(lds + (bufoff) + ldsw + _i * 8192), 16, 0, 0); } \
;         else { PG8_STAGE(bufoff, (kptr) + (half) * hstepA, voffA); } } while (0)
; #define PG8_LDA(dst, b, h) do { _Pragma("unroll") for (int m = 0; m < 4; ++m) _Pragma("unroll") for (int k = 0; k < 2; ++k) dst[m][k] = *(const LAS bf16x8*)(lds + PG8_SA(b, h) + aoff + m * 2048 + k * 1024); } while (0)
; #define PG8_LDB(dst, b, h) do { _Pragma("unroll") for (int n = 0; n < 2; ++n) _Pragma("unroll") for (int k = 0; k < 2; ++k) dst[n][k] = *(const LAS bf16x8*)(lds + PG8_SB(b, h) + boff + n * 2048 + k * 1024); } while (0)
; #define PG8_WAIT_V(n) asm volatile("s_waitcnt vmcnt(" #n ")" ::: "memory")
; #define PG8_WAIT_L(n) asm volatile("s_waitcnt lgkmcnt(" #n ")" ::: "memory")
; #define PG8_BAR __builtin_amdgcn_s_barrier()
;     ...
;             const char* a1 = cA + (size_t)(t + 1) * kstep;
;             const char* a2 = last ? nA : cA + (size_t)(t + 2) * kstep; const char* b2 = last ? nB : cB + (size_t)(t + 2) * kstep;
;             const char* a3 = a2 + kstep; const char* b3 = b2 + kstep;
;             unsigned g2[2][2];
;             if constexpr (GATHER) {
; #pragma unroll
;                 for (int _h = 0; _h < 2; ++_h)
; #pragma unroll
;                     for (int _i = 0; _i < 2; ++_i) g2[_h][_i] = last ? gN[_h][_i] : gC[_h][_i]; }
;             if constexpr (SP2) {
;             PG8_LDB(B0, 0, 0); PG8_LDB(B1, 0, 1); PG8_SCHED; PG8_LDA(At, 0, 0); PG8_STAGE_A(PG8_SA(1, 1), a1, 1, gC);
;             PG8_WAIT_V(8); PG8_WAIT_L(0); PG8_BAR; PG8_MMA(0, 0, At, B0); PG8_MMA(0, 1, At, B1); PG8_BAR; PG8_SCHED;
;             PG8_LDA(At, 0, 1); PG8_STAGE(PG8_SB(0, 0), b2, voffB); PG8_STAGE(PG8_SB(0, 1), b2 + hstepB, voffB); PG8_STAGE_A(PG8_SA(0, 0), a2, 0, g2);
;             PG8_WAIT_V(8); PG8_WAIT_L(0); PG8_BAR; PG8_MMA(1, 0, At, B0); PG8_MMA(1, 1, At, B1); PG8_BAR; PG8_SCHED;
.LBB0_668:
	s_add_u32 s16, s48, s30
	s_addc_u32 s17, s49, s31
	s_add_u32 s18, s16, 0x100
	s_addc_u32 s19, s17, 0
	s_and_b64 s[14:15], s[0:1], exec
	s_cselect_b32 s51, s43, s19
	s_cselect_b32 s50, s42, s18
	s_add_u32 s14, s46, s30
	s_addc_u32 s15, s47, s31
	s_add_u32 s14, s14, 0x100
	s_addc_u32 s15, s15, 0
	s_add_i32 s22, 0, 0x10000
	s_and_b64 s[0:1], s[0:1], exec
	s_cselect_b32 s55, s45, s15
	s_cselect_b32 s54, s44, s14
	s_add_i32 s1, 0, 0x14000
	s_add_u32 s58, s16, 0x10080
	s_addc_u32 s59, s17, 0
	s_add_i32 s21, s22, s26
	s_add_i32 m0, s27, 0xc000
	s_add_i32 s34, s27, 0xe000
	s_add_i32 s18, s21, 0x2000
	s_add_u32 s56, s54, 0x10000
	v_add_u32_e32 v152, s22, v138
	v_add_u32_e32 v168, s1, v138
	s_addc_u32 s57, s55, 0
	s_add_i32 s20, s1, s26
	ds_read_b128 v[140:143], v152
	ds_read_b128 v[144:147], v152 offset:1024
	ds_read_b128 v[148:151], v152 offset:2048
	ds_read_b128 v[152:155], v152 offset:3072
	ds_read_b128 v[156:159], v168
	ds_read_b128 v[160:163], v168 offset:1024
	ds_read_b128 v[164:167], v168 offset:2048
	ds_read_b128 v[168:171], v168 offset:3072
	s_add_i32 s19, s20, 0x2000
	s_add_i32 s17, 0, 0x18000
	s_add_i32 s16, 0, 0x1c000
	s_add_u32 s30, s50, 0x10000
	s_addc_u32 s31, s51, 0
	s_add_i32 s15, s17, s26
	s_add_i32 s14, s15, 0x2000
	s_add_u32 s0, s54, 0x10080
	s_addc_u32 s1, s55, 0
	s_add_i32 s23, s16, s26
	s_add_i32 s22, s23, 0x2000
	v_lshl_add_u64 v[204:205], s[58:59], 0, v[134:135]
	ds_read_b128 v[172:175], v139
	ds_read_b128 v[176:179], v139 offset:1024
	ds_read_b128 v[180:183], v139 offset:2048
	ds_read_b128 v[184:187], v139 offset:3072
	ds_read_b128 v[188:191], v139 offset:4096
	ds_read_b128 v[192:195], v139 offset:5120
	ds_read_b128 v[196:199], v139 offset:6144
	ds_read_b128 v[200:203], v139 offset:7168
	global_load_lds_dwordx4 v[204:205], off
	v_lshl_add_u64 v[204:205], s[58:59], 0, v[132:133]
	s_mov_b32 m0, s34
	s_nop 0
	global_load_lds_dwordx4 v[204:205], off
	s_waitcnt vmcnt(8)
	s_waitcnt lgkmcnt(0)
	s_barrier
	s_setprio 1
	s_waitcnt lgkmcnt(0)
	v_mfma_f32_16x16x32_bf16 v[126:129], v[140:143], v[172:175], v[126:129]
	v_mfma_f32_16x16x32_bf16 v[122:125], v[148:151], v[172:175], v[122:125]
	v_mfma_f32_16x16x32_bf16 v[118:121], v[140:143], v[180:183], v[118:121]
	v_mfma_f32_16x16x32_bf16 v[114:117], v[148:151], v[180:183], v[114:117]
	v_mfma_f32_16x16x32_bf16 v[102:105], v[140:143], v[188:191], v[102:105]
	v_mfma_f32_16x16x32_bf16 v[98:101], v[148:151], v[188:191], v[98:101]
	v_mfma_f32_16x16x32_bf16 v[86:89], v[140:143], v[196:199], v[86:89]
	v_mfma_f32_16x16x32_bf16 v[82:85], v[148:151], v[196:199], v[82:85]
	v_mfma_f32_16x16x32_bf16 v[126:129], v[144:147], v[176:179], v[126:129]
	v_mfma_f32_16x16x32_bf16 v[122:125], v[152:155], v[176:179], v[122:125]
	v_mfma_f32_16x16x32_bf16 v[118:121], v[144:147], v[184:187], v[118:121]
	v_mfma_f32_16x16x32_bf16 v[114:117], v[152:155], v[184:187], v[114:117]
	v_mfma_f32_16x16x32_bf16 v[102:105], v[144:147], v[192:195], v[102:105]
	v_mfma_f32_16x16x32_bf16 v[98:101], v[152:155], v[192:195], v[98:101]
	v_mfma_f32_16x16x32_bf16 v[86:89], v[144:147], v[200:203], v[86:89]
	v_mfma_f32_16x16x32_bf16 v[82:85], v[152:155], v[200:203], v[82:85]
	v_mfma_f32_16x16x32_bf16 v[110:113], v[156:159], v[172:175], v[110:113]
	v_mfma_f32_16x16x32_bf16 v[106:109], v[164:167], v[172:175], v[106:109]
	v_mfma_f32_16x16x32_bf16 v[94:97], v[156:159], v[180:183], v[94:97]
	v_mfma_f32_16x16x32_bf16 v[90:93], v[164:167], v[180:183], v[90:93]
	v_mfma_f32_16x16x32_bf16 v[78:81], v[156:159], v[188:191], v[78:81]
	v_mfma_f32_16x16x32_bf16 v[74:77], v[164:167], v[188:191], v[74:77]
	v_mfma_f32_16x16x32_bf16 v[70:73], v[156:159], v[196:199], v[70:73]
	v_mfma_f32_16x16x32_bf16 v[66:69], v[164:167], v[196:199], v[66:69]
	v_mfma_f32_16x16x32_bf16 v[110:113], v[160:163], v[176:179], v[110:113]
	v_mfma_f32_16x16x32_bf16 v[106:109], v[168:171], v[176:179], v[106:109]
	v_mfma_f32_16x16x32_bf16 v[94:97], v[160:163], v[184:187], v[94:97]
	v_mfma_f32_16x16x32_bf16 v[90:93], v[168:171], v[184:187], v[90:93]
	v_mfma_f32_16x16x32_bf16 v[78:81], v[160:163], v[192:195], v[78:81]
	v_mfma_f32_16x16x32_bf16 v[74:77], v[168:171], v[192:195], v[74:77]
	v_mfma_f32_16x16x32_bf16 v[70:73], v[160:163], v[200:203], v[70:73]
	v_mfma_f32_16x16x32_bf16 v[66:69], v[168:171], v[200:203], v[66:69]
	s_setprio 0
	s_barrier
	s_mov_b32 m0, s21
	v_lshl_add_u64 v[204:205], s[54:55], 0, v[206:207]
	ds_read_b128 v[172:175], v139 offset:16384
	ds_read_b128 v[176:179], v139 offset:17408
	ds_read_b128 v[180:183], v139 offset:18432
	ds_read_b128 v[184:187], v139 offset:19456
	ds_read_b128 v[188:191], v139 offset:20480
	ds_read_b128 v[192:195], v139 offset:21504
	ds_read_b128 v[196:199], v139 offset:22528
	ds_read_b128 v[200:203], v139 offset:23552
	global_load_lds_dwordx4 v[204:205], off
	v_lshl_add_u64 v[208:209], s[54:55], 0, v[130:131]
	s_mov_b32 m0, s18
	v_lshl_add_u64 v[210:211], s[56:57], 0, v[206:207]
	global_load_lds_dwordx4 v[208:209], off
	s_mov_b32 m0, s20
	v_lshl_add_u64 v[212:213], s[50:51], 0, v[132:133]
	global_load_lds_dwordx4 v[210:211], off
	v_lshl_add_u64 v[210:211], s[56:57], 0, v[130:131]
	s_mov_b32 m0, s19
	s_nop 0
	global_load_lds_dwordx4 v[210:211], off
	v_lshl_add_u64 v[210:211], s[50:51], 0, v[134:135]
	s_mov_b32 m0, s27
	s_nop 0
	global_load_lds_dwordx4 v[210:211], off
	s_mov_b32 m0, s60
	s_nop 0
	global_load_lds_dwordx4 v[212:213], off
	s_waitcnt vmcnt(8)
	s_waitcnt lgkmcnt(0)
	s_barrier
; #define PG8_STAGE_A(bufoff, kptr, half, VO) do { if constexpr (GATHER) { _Pragma("unroll") for (int _i = 0; _i < 2; ++_i) \
;         __builtin_amdgcn_global_load_lds((const unsigned*)((const char*)(kptr) + (VO)[half][_i]), (LAS unsigned*)(lds + (bufoff) + ldsw + _i * 8192), 16, 0, 0); } \
;         else { PG8_STAGE(bufoff, (kptr) + (half) * hstepA, voffA); } } while (0)
; #define PG8_LDA(dst, b, h) do { _Pragma("unroll") for (int m = 0; m < 4; ++m) _Pragma("unroll") for (int k = 0; k < 2; ++k) dst[m][k] = *(const LAS bf16x8*)(lds + PG8_SA(b, h) + aoff + m * 2048 + k * 1024); } while (0)
; #define PG8_LDB(dst, b, h) do { _Pragma("unroll") for (int n = 0; n < 2; ++n) _Pragma("unroll") for (int k = 0; k < 2; ++k) dst[n][k] = *(const LAS bf16x8*)(lds + PG8_SB(b, h) + boff + n * 2048 + k * 1024); } while (0)
; #define PG8_MMA(ai, bj, At, Bt) do { __builtin_amdgcn_s_setprio(1); _Pragma("unroll") for (int m = 0; m < 4; ++m) _Pragma("unroll") for (int n = 0; n < 2; ++n) _Pragma("unroll") for (int k = 0; k < 2; ++k) \
;         acc[ai][bj][m][n] = __builtin_amdgcn_mfma_f32_16x16x32_bf16(Bt[n][k], At[m][k], acc[ai][bj][m][n], 0, 0, 0); __builtin_amdgcn_s_setprio(0); } while (0)
; #define PG8_WAIT_V(n) asm volatile("s_waitcnt vmcnt(" #n ")" ::: "memory")
; #define PG8_WAIT_L(n) asm volatile("s_waitcnt lgkmcnt(" #n ")" ::: "memory")
; #define PG8_BAR __builtin_amdgcn_s_barrier()
; #define PG8_SCHED __builtin_amdgcn_sched_barrier(0)
;     ...
;             PG8_WAIT_V(8); PG8_WAIT_L(0); PG8_BAR; PG8_MMA(1, 0, At, B0); PG8_MMA(1, 1, At, B1); PG8_BAR; PG8_SCHED;
;             PG8_LDB(B0, 1, 0); PG8_LDB(B1, 1, 1); PG8_SCHED; PG8_LDA(At, 1, 0); PG8_STAGE_A(PG8_SA(0, 1), a2, 1, g2);
;             PG8_WAIT_V(8); PG8_WAIT_L(0); PG8_BAR; PG8_MMA(0, 0, At, B0); PG8_MMA(0, 1, At, B1); PG8_BAR; PG8_SCHED;
	s_setprio 1
	s_waitcnt lgkmcnt(0)
	v_mfma_f32_16x16x32_bf16 v[62:65], v[140:143], v[172:175], v[62:65]
	v_mfma_f32_16x16x32_bf16 v[58:61], v[148:151], v[172:175], v[58:61]
	v_mfma_f32_16x16x32_bf16 v[54:57], v[140:143], v[180:183], v[54:57]
	v_mfma_f32_16x16x32_bf16 v[50:53], v[148:151], v[180:183], v[50:53]
	v_mfma_f32_16x16x32_bf16 v[38:41], v[140:143], v[188:191], v[38:41]
	v_mfma_f32_16x16x32_bf16 v[34:37], v[148:151], v[188:191], v[34:37]
	v_mfma_f32_16x16x32_bf16 v[22:25], v[140:143], v[196:199], v[22:25]
	v_mfma_f32_16x16x32_bf16 v[18:21], v[148:151], v[196:199], v[18:21]
	v_mfma_f32_16x16x32_bf16 v[62:65], v[144:147], v[176:179], v[62:65]
	v_mfma_f32_16x16x32_bf16 v[58:61], v[152:155], v[176:179], v[58:61]
	v_mfma_f32_16x16x32_bf16 v[54:57], v[144:147], v[184:187], v[54:57]
	v_mfma_f32_16x16x32_bf16 v[50:53], v[152:155], v[184:187], v[50:53]
	v_mfma_f32_16x16x32_bf16 v[38:41], v[144:147], v[192:195], v[38:41]
	v_mfma_f32_16x16x32_bf16 v[34:37], v[152:155], v[192:195], v[34:37]
	v_mfma_f32_16x16x32_bf16 v[22:25], v[144:147], v[200:203], v[22:25]
	v_mfma_f32_16x16x32_bf16 v[18:21], v[152:155], v[200:203], v[18:21]
	v_mfma_f32_16x16x32_bf16 v[46:49], v[156:159], v[172:175], v[46:49]
	v_mfma_f32_16x16x32_bf16 v[42:45], v[164:167], v[172:175], v[42:45]
	v_mfma_f32_16x16x32_bf16 v[30:33], v[156:159], v[180:183], v[30:33]
	v_mfma_f32_16x16x32_bf16 v[26:29], v[164:167], v[180:183], v[26:29]
	v_mfma_f32_16x16x32_bf16 v[14:17], v[156:159], v[188:191], v[14:17]
	v_mfma_f32_16x16x32_bf16 v[10:13], v[164:167], v[188:191], v[10:13]
	v_mfma_f32_16x16x32_bf16 v[6:9], v[156:159], v[196:199], v[6:9]
	v_mfma_f32_16x16x32_bf16 v[2:5], v[164:167], v[196:199], v[2:5]
	v_mfma_f32_16x16x32_bf16 v[46:49], v[160:163], v[176:179], v[46:49]
	v_mfma_f32_16x16x32_bf16 v[42:45], v[168:171], v[176:179], v[42:45]
	v_mfma_f32_16x16x32_bf16 v[30:33], v[160:163], v[184:187], v[30:33]
	v_mfma_f32_16x16x32_bf16 v[26:29], v[168:171], v[184:187], v[26:29]
	v_mfma_f32_16x16x32_bf16 v[14:17], v[160:163], v[192:195], v[14:17]
	v_mfma_f32_16x16x32_bf16 v[10:13], v[168:171], v[192:195], v[10:13]
	v_mfma_f32_16x16x32_bf16 v[6:9], v[160:163], v[200:203], v[6:9]
	v_mfma_f32_16x16x32_bf16 v[2:5], v[168:171], v[200:203], v[2:5]
	s_setprio 0
	s_barrier
	v_add_u32_e32 v152, s17, v138
	v_add_u32_e32 v168, s16, v138
	ds_read_b128 v[140:143], v152
	ds_read_b128 v[144:147], v152 offset:1024
	ds_read_b128 v[148:151], v152 offset:2048
	ds_read_b128 v[152:155], v152 offset:3072
	ds_read_b128 v[156:159], v168
	ds_read_b128 v[160:163], v168 offset:1024
	ds_read_b128 v[164:167], v168 offset:2048
	ds_read_b128 v[168:171], v168 offset:3072
	s_mov_b32 m0, s61
	v_lshl_add_u64 v[216:217], s[30:31], 0, v[134:135]
	ds_read_b128 v[172:175], v139 offset:32768
	ds_read_b128 v[176:179], v139 offset:33792
	ds_read_b128 v[180:183], v139 offset:34816
	ds_read_b128 v[184:187], v139 offset:35840
	ds_read_b128 v[188:191], v139 offset:36864
	ds_read_b128 v[192:195], v139 offset:37888
	ds_read_b128 v[196:199], v139 offset:38912
	ds_read_b128 v[200:203], v139 offset:39936
	global_load_lds_dwordx4 v[216:217], off
	v_lshl_add_u64 v[216:217], s[30:31], 0, v[132:133]
	s_mov_b32 m0, s63
	s_nop 0
	global_load_lds_dwordx4 v[216:217], off
	s_waitcnt vmcnt(8)
	s_waitcnt lgkmcnt(0)
	s_barrier
	s_setprio 1
	s_waitcnt lgkmcnt(0)
	v_mfma_f32_16x16x32_bf16 v[126:129], v[140:143], v[172:175], v[126:129]
	v_mfma_f32_16x16x32_bf16 v[122:125], v[148:151], v[172:175], v[122:125]
	v_mfma_f32_16x16x32_bf16 v[118:121], v[140:143], v[180:183], v[118:121]
	v_mfma_f32_16x16x32_bf16 v[114:117], v[148:151], v[180:183], v[114:117]
	v_mfma_f32_16x16x32_bf16 v[102:105], v[140:143], v[188:191], v[102:105]
	v_mfma_f32_16x16x32_bf16 v[98:101], v[148:151], v[188:191], v[98:101]
	v_mfma_f32_16x16x32_bf16 v[86:89], v[140:143], v[196:199], v[86:89]
	v_mfma_f32_16x16x32_bf16 v[82:85], v[148:151], v[196:199], v[82:85]
	v_mfma_f32_16x16x32_bf16 v[126:129], v[144:147], v[176:179], v[126:129]
	v_mfma_f32_16x16x32_bf16 v[122:125], v[152:155], v[176:179], v[122:125]
	v_mfma_f32_16x16x32_bf16 v[118:121], v[144:147], v[184:187], v[118:121]
	v_mfma_f32_16x16x32_bf16 v[114:117], v[152:155], v[184:187], v[114:117]
	v_mfma_f32_16x16x32_bf16 v[102:105], v[144:147], v[192:195], v[102:105]
	v_mfma_f32_16x16x32_bf16 v[98:101], v[152:155], v[192:195], v[98:101]
	v_mfma_f32_16x16x32_bf16 v[86:89], v[144:147], v[200:203], v[86:89]
	v_mfma_f32_16x16x32_bf16 v[82:85], v[152:155], v[200:203], v[82:85]
	v_mfma_f32_16x16x32_bf16 v[110:113], v[156:159], v[172:175], v[110:113]
	v_mfma_f32_16x16x32_bf16 v[106:109], v[164:167], v[172:175], v[106:109]
	v_mfma_f32_16x16x32_bf16 v[94:97], v[156:159], v[180:183], v[94:97]
	v_mfma_f32_16x16x32_bf16 v[90:93], v[164:167], v[180:183], v[90:93]
	v_mfma_f32_16x16x32_bf16 v[78:81], v[156:159], v[188:191], v[78:81]
	v_mfma_f32_16x16x32_bf16 v[74:77], v[164:167], v[188:191], v[74:77]
	v_mfma_f32_16x16x32_bf16 v[70:73], v[156:159], v[196:199], v[70:73]
	v_mfma_f32_16x16x32_bf16 v[66:69], v[164:167], v[196:199], v[66:69]
	v_mfma_f32_16x16x32_bf16 v[110:113], v[160:163], v[176:179], v[110:113]
	v_mfma_f32_16x16x32_bf16 v[106:109], v[168:171], v[176:179], v[106:109]
	v_mfma_f32_16x16x32_bf16 v[94:97], v[160:163], v[184:187], v[94:97]
	v_mfma_f32_16x16x32_bf16 v[90:93], v[168:171], v[184:187], v[90:93]
	v_mfma_f32_16x16x32_bf16 v[78:81], v[160:163], v[192:195], v[78:81]
	v_mfma_f32_16x16x32_bf16 v[74:77], v[168:171], v[192:195], v[74:77]
	v_mfma_f32_16x16x32_bf16 v[70:73], v[160:163], v[200:203], v[70:73]
	v_mfma_f32_16x16x32_bf16 v[66:69], v[168:171], v[200:203], v[66:69]
	s_setprio 0
	s_barrier
; #define PG8_STAGE(bufoff, gbase, voff) do { _Pragma("unroll") for (int _i = 0; _i < 2; ++_i) \
;         __builtin_amdgcn_global_load_lds((const unsigned*)((const char*)(gbase) + (voff)[_i]), (LAS unsigned*)(lds + (bufoff) + ldsw + _i * 8192), 16, 0, 0); } while (0)
; #define PG8_STAGE_A(bufoff, kptr, half, VO) do { if constexpr (GATHER) { _Pragma("unroll") for (int _i = 0; _i < 2; ++_i) \
;         __builtin_amdgcn_global_load_lds((const unsigned*)((const char*)(kptr) + (VO)[half][_i]), (LAS unsigned*)(lds + (bufoff) + ldsw + _i * 8192), 16, 0, 0); } \
;         else { PG8_STAGE(bufoff, (kptr) + (half) * hstepA, voffA); } } while (0)
; #define PG8_LDA(dst, b, h) do { _Pragma("unroll") for (int m = 0; m < 4; ++m) _Pragma("unroll") for (int k = 0; k < 2; ++k) dst[m][k] = *(const LAS bf16x8*)(lds + PG8_SA(b, h) + aoff + m * 2048 + k * 1024); } while (0)
; #define PG8_MMA(ai, bj, At, Bt) do { __builtin_amdgcn_s_setprio(1); _Pragma("unroll") for (int m = 0; m < 4; ++m) _Pragma("unroll") for (int n = 0; n < 2; ++n) _Pragma("unroll") for (int k = 0; k < 2; ++k) \
;         acc[ai][bj][m][n] = __builtin_amdgcn_mfma_f32_16x16x32_bf16(Bt[n][k], At[m][k], acc[ai][bj][m][n], 0, 0, 0); __builtin_amdgcn_s_setprio(0); } while (0)
; #define PG8_WAIT_V(n) asm volatile("s_waitcnt vmcnt(" #n ")" ::: "memory")
; #define PG8_WAIT_L(n) asm volatile("s_waitcnt lgkmcnt(" #n ")" ::: "memory")
; #define PG8_BAR __builtin_amdgcn_s_barrier()
; #define PG8_SCHED __builtin_amdgcn_sched_barrier(0)
;     ...
;             PG8_LDA(At, 1, 1); PG8_STAGE(PG8_SB(1, 0), b3, voffB); PG8_STAGE(PG8_SB(1, 1), b3 + hstepB, voffB); PG8_STAGE_A(PG8_SA(1, 0), a3, 0, g2);
;             PG8_WAIT_V(8); PG8_WAIT_L(0); PG8_BAR; PG8_MMA(1, 0, At, B0); PG8_MMA(1, 1, At, B1); PG8_BAR; PG8_SCHED;
	s_mov_b32 m0, s15
	v_lshl_add_u64 v[204:205], v[204:205], 0, s[8:9]
	ds_read_b128 v[172:175], v139 offset:49152
	ds_read_b128 v[176:179], v139 offset:50176
	ds_read_b128 v[180:183], v139 offset:51200
	ds_read_b128 v[184:187], v139 offset:52224
	ds_read_b128 v[188:191], v139 offset:53248
	ds_read_b128 v[192:195], v139 offset:54272
	ds_read_b128 v[196:199], v139 offset:55296
	ds_read_b128 v[200:203], v139 offset:56320
	global_load_lds_dwordx4 v[204:205], off
	v_lshl_add_u64 v[204:205], v[208:209], 0, s[8:9]
	s_mov_b32 m0, s14
	s_nop 0
	global_load_lds_dwordx4 v[204:205], off
	v_lshl_add_u64 v[204:205], s[0:1], 0, v[206:207]
	s_mov_b32 m0, s23
	s_nop 0
	global_load_lds_dwordx4 v[204:205], off
	v_lshl_add_u64 v[204:205], s[0:1], 0, v[130:131]
	s_mov_b32 m0, s22
	s_nop 0
	global_load_lds_dwordx4 v[204:205], off
	v_lshl_add_u64 v[204:205], v[210:211], 0, s[8:9]
	s_mov_b32 m0, s64
	s_nop 0
	global_load_lds_dwordx4 v[204:205], off
	v_lshl_add_u64 v[204:205], v[212:213], 0, s[8:9]
	s_mov_b32 m0, s65
	s_nop 0
	global_load_lds_dwordx4 v[204:205], off
	s_waitcnt vmcnt(8)
	s_waitcnt lgkmcnt(0)
	s_barrier
	s_setprio 1
	s_waitcnt lgkmcnt(0)
	v_mfma_f32_16x16x32_bf16 v[62:65], v[140:143], v[172:175], v[62:65]
	v_mfma_f32_16x16x32_bf16 v[58:61], v[148:151], v[172:175], v[58:61]
	v_mfma_f32_16x16x32_bf16 v[54:57], v[140:143], v[180:183], v[54:57]
	v_mfma_f32_16x16x32_bf16 v[50:53], v[148:151], v[180:183], v[50:53]
	v_mfma_f32_16x16x32_bf16 v[38:41], v[140:143], v[188:191], v[38:41]
	v_mfma_f32_16x16x32_bf16 v[34:37], v[148:151], v[188:191], v[34:37]
	v_mfma_f32_16x16x32_bf16 v[22:25], v[140:143], v[196:199], v[22:25]
	v_mfma_f32_16x16x32_bf16 v[18:21], v[148:151], v[196:199], v[18:21]
	v_mfma_f32_16x16x32_bf16 v[62:65], v[144:147], v[176:179], v[62:65]
	v_mfma_f32_16x16x32_bf16 v[58:61], v[152:155], v[176:179], v[58:61]
	v_mfma_f32_16x16x32_bf16 v[54:57], v[144:147], v[184:187], v[54:57]
	v_mfma_f32_16x16x32_bf16 v[50:53], v[152:155], v[184:187], v[50:53]
	v_mfma_f32_16x16x32_bf16 v[38:41], v[144:147], v[192:195], v[38:41]
	v_mfma_f32_16x16x32_bf16 v[34:37], v[152:155], v[192:195], v[34:37]
	v_mfma_f32_16x16x32_bf16 v[22:25], v[144:147], v[200:203], v[22:25]
	v_mfma_f32_16x16x32_bf16 v[18:21], v[152:155], v[200:203], v[18:21]
	v_mfma_f32_16x16x32_bf16 v[46:49], v[156:159], v[172:175], v[46:49]
	v_mfma_f32_16x16x32_bf16 v[42:45], v[164:167], v[172:175], v[42:45]
	v_mfma_f32_16x16x32_bf16 v[30:33], v[156:159], v[180:183], v[30:33]
	v_mfma_f32_16x16x32_bf16 v[26:29], v[164:167], v[180:183], v[26:29]
	v_mfma_f32_16x16x32_bf16 v[14:17], v[156:159], v[188:191], v[14:17]
	v_mfma_f32_16x16x32_bf16 v[10:13], v[164:167], v[188:191], v[10:13]
	v_mfma_f32_16x16x32_bf16 v[6:9], v[156:159], v[196:199], v[6:9]
	v_mfma_f32_16x16x32_bf16 v[2:5], v[164:167], v[196:199], v[2:5]
	v_mfma_f32_16x16x32_bf16 v[46:49], v[160:163], v[176:179], v[46:49]
	v_mfma_f32_16x16x32_bf16 v[42:45], v[168:171], v[176:179], v[42:45]
	v_mfma_f32_16x16x32_bf16 v[30:33], v[160:163], v[184:187], v[30:33]
	v_mfma_f32_16x16x32_bf16 v[26:29], v[168:171], v[184:187], v[26:29]
	v_mfma_f32_16x16x32_bf16 v[14:17], v[160:163], v[192:195], v[14:17]
	v_mfma_f32_16x16x32_bf16 v[10:13], v[168:171], v[192:195], v[10:13]
	v_mfma_f32_16x16x32_bf16 v[6:9], v[160:163], v[200:203], v[6:9]
	v_mfma_f32_16x16x32_bf16 v[2:5], v[168:171], v[200:203], v[2:5]
	s_setprio 0
	s_barrier
	s_andn2_b64 vcc, exec, s[24:25]
	s_mov_b64 s[0:1], -1
	s_mov_b64 s[24:25], 0
	s_mov_b64 s[30:31], 0x100
	s_cbranch_vccz .LBB0_668
	s_and_b64 vcc, exec, s[38:39]
	s_cbranch_vccz .LBB0_671
	s_barrier

; #define PG8_STAGE(bufoff, gbase, voff) do { _Pragma("unroll") for (int _i = 0; _i < 2; ++_i) \
;         __builtin_amdgcn_global_load_lds((const unsigned*)((const char*)(gbase) + (voff)[_i]), (LAS unsigned*)(lds + (bufoff) + ldsw + _i * 8192), 16, 0, 0); } while (0)
; #define PG8_STAGE_A(bufoff, kptr, half, VO) do { if constexpr (GATHER) { _Pragma("unroll") for (int _i = 0; _i < 2; ++_i) \
;         __builtin_amdgcn_global_load_lds((const unsigned*)((const char*)(kptr) + (VO)[half][_i]), (LAS unsigned*)(lds + (bufoff) + ldsw + _i * 8192), 16, 0, 0); } \
;         else { PG8_STAGE(bufoff, (kptr) + (half) * hstepA, voffA); } } while (0)
; #define PG8_LDA(dst, b, h) do { _Pragma("unroll") for (int m = 0; m < 4; ++m) _Pragma("unroll") for (int k = 0; k < 2; ++k) dst[m][k] = *(const LAS bf16x8*)(lds + PG8_SA(b, h) + aoff + m * 2048 + k * 1024); } while (0)
; #define PG8_LDB(dst, b, h) do { _Pragma("unroll") for (int n = 0; n < 2; ++n) _Pragma("unroll") for (int k = 0; k < 2; ++k) dst[n][k] = *(const LAS bf16x8*)(lds + PG8_SB(b, h) + boff + n * 2048 + k * 1024); } while (0)
; #define PG8_WAIT_V(n) asm volatile("s_waitcnt vmcnt(" #n ")" ::: "memory")
; #define PG8_WAIT_L(n) asm volatile("s_waitcnt lgkmcnt(" #n ")" ::: "memory")
; #define PG8_BAR __builtin_amdgcn_s_barrier()
;     ...
;             const char* a1 = cA + (size_t)(t + 1) * kstep;
;             const char* a2 = last ? nA : cA + (size_t)(t + 2) * kstep; const char* b2 = last ? nB : cB + (size_t)(t + 2) * kstep;
;             const char* a3 = a2 + kstep; const char* b3 = b2 + kstep;
;             unsigned g2[2][2];
;             if constexpr (GATHER) {
; #pragma unroll
;                 for (int _h = 0; _h < 2; ++_h)
; #pragma unroll
;                     for (int _i = 0; _i < 2; ++_i) g2[_h][_i] = last ? gN[_h][_i] : gC[_h][_i]; }
;             if constexpr (SP2) {
;             PG8_LDB(B0, 0, 0); PG8_LDB(B1, 0, 1); PG8_SCHED; PG8_LDA(At, 0, 0); PG8_STAGE_A(PG8_SA(1, 1), a1, 1, gC);
;             PG8_WAIT_V(8); PG8_WAIT_L(0); PG8_BAR; PG8_MMA(0, 0, At, B0); PG8_MMA(0, 1, At, B1); PG8_BAR; PG8_SCHED;
;             PG8_LDA(At, 0, 1); PG8_STAGE(PG8_SB(0, 0), b2, voffB); PG8_STAGE(PG8_SB(0, 1), b2 + hstepB, voffB); PG8_STAGE_A(PG8_SA(0, 0), a2, 0, g2);
;             PG8_WAIT_V(8); PG8_WAIT_L(0); PG8_BAR; PG8_MMA(1, 0, At, B0); PG8_MMA(1, 1, At, B1); PG8_BAR; PG8_SCHED;
.LBB0_684:
	s_add_u32 s16, s46, s48
	s_addc_u32 s17, s47, s49
	s_add_u32 s18, s16, 0x100
	s_addc_u32 s19, s17, 0
	s_and_b64 s[14:15], s[0:1], exec
	s_cselect_b32 s51, s43, s19
	s_cselect_b32 s50, s42, s18
	s_add_u32 s14, s24, s48
	s_addc_u32 s15, s25, s49
	s_add_u32 s14, s14, 0x100
	s_addc_u32 s15, s15, 0
	s_add_i32 s22, 0, 0x10000
	s_and_b64 s[0:1], s[0:1], exec
	s_cselect_b32 s55, s45, s15
	s_cselect_b32 s54, s44, s14
	s_add_i32 s1, 0, 0x14000
	s_add_u32 s58, s16, 0x10080
	s_addc_u32 s59, s17, 0
	s_add_i32 s21, s22, s26
	s_add_i32 m0, s27, 0xc000
	s_add_i32 s35, s27, 0xe000
	s_add_i32 s18, s21, 0x2000
	v_add_u32_e32 v143, s22, v144
	s_add_u32 s56, s54, 0x10000
	ds_read_b128 v[146:149], v143
	ds_read_b128 v[150:153], v143 offset:1024
	ds_read_b128 v[154:157], v143 offset:2048
	ds_read_b128 v[158:161], v143 offset:3072
	v_add_u32_e32 v143, s1, v144
	s_addc_u32 s57, s55, 0
	s_add_i32 s20, s1, s26
	ds_read_b128 v[162:165], v143
	ds_read_b128 v[166:169], v143 offset:1024
	ds_read_b128 v[170:173], v143 offset:2048
	ds_read_b128 v[174:177], v143 offset:3072
	s_add_i32 s19, s20, 0x2000
	s_add_i32 s17, 0, 0x18000
	s_add_i32 s16, 0, 0x1c000
	s_add_u32 s48, s50, 0x10000
	s_addc_u32 s49, s51, 0
	s_add_i32 s15, s17, s26
	s_add_i32 s14, s15, 0x2000
	s_add_u32 s0, s54, 0x10080
	s_addc_u32 s1, s55, 0
	s_add_i32 s23, s16, s26
	s_add_i32 s22, s23, 0x2000
	v_lshl_add_u64 v[208:209], s[58:59], 0, v[136:137]
	ds_read_b128 v[178:181], v145
	ds_read_b128 v[182:185], v145 offset:1024
	ds_read_b128 v[186:189], v145 offset:2048
	ds_read_b128 v[190:193], v145 offset:3072
	ds_read_b128 v[194:197], v145 offset:4096
	ds_read_b128 v[198:201], v145 offset:5120
	ds_read_b128 v[202:205], v145 offset:6144
	ds_read_b128 v[216:219], v145 offset:7168
	global_load_lds_dwordx4 v[208:209], off
	v_lshl_add_u64 v[208:209], s[58:59], 0, v[132:133]
	s_mov_b32 m0, s35
	s_nop 0
	global_load_lds_dwordx4 v[208:209], off
	s_waitcnt vmcnt(8)
	s_waitcnt lgkmcnt(0)
	s_barrier
	s_setprio 1
	s_waitcnt lgkmcnt(0)
	v_mfma_f32_16x16x32_bf16 v[126:129], v[146:149], v[178:181], v[126:129]
	v_mfma_f32_16x16x32_bf16 v[122:125], v[154:157], v[178:181], v[122:125]
	v_mfma_f32_16x16x32_bf16 v[118:121], v[146:149], v[186:189], v[118:121]
	v_mfma_f32_16x16x32_bf16 v[114:117], v[154:157], v[186:189], v[114:117]
	v_mfma_f32_16x16x32_bf16 v[102:105], v[146:149], v[194:197], v[102:105]
	v_mfma_f32_16x16x32_bf16 v[98:101], v[154:157], v[194:197], v[98:101]
	v_mfma_f32_16x16x32_bf16 v[86:89], v[146:149], v[202:205], v[86:89]
	v_mfma_f32_16x16x32_bf16 v[82:85], v[154:157], v[202:205], v[82:85]
	v_mfma_f32_16x16x32_bf16 v[126:129], v[150:153], v[182:185], v[126:129]
	v_mfma_f32_16x16x32_bf16 v[122:125], v[158:161], v[182:185], v[122:125]
	v_mfma_f32_16x16x32_bf16 v[118:121], v[150:153], v[190:193], v[118:121]
	v_mfma_f32_16x16x32_bf16 v[114:117], v[158:161], v[190:193], v[114:117]
	v_mfma_f32_16x16x32_bf16 v[102:105], v[150:153], v[198:201], v[102:105]
	v_mfma_f32_16x16x32_bf16 v[98:101], v[158:161], v[198:201], v[98:101]
	v_mfma_f32_16x16x32_bf16 v[86:89], v[150:153], v[216:219], v[86:89]
	v_mfma_f32_16x16x32_bf16 v[82:85], v[158:161], v[216:219], v[82:85]
	v_mfma_f32_16x16x32_bf16 v[110:113], v[162:165], v[178:181], v[110:113]
	v_mfma_f32_16x16x32_bf16 v[106:109], v[170:173], v[178:181], v[106:109]
	v_mfma_f32_16x16x32_bf16 v[94:97], v[162:165], v[186:189], v[94:97]
	v_mfma_f32_16x16x32_bf16 v[90:93], v[170:173], v[186:189], v[90:93]
	v_mfma_f32_16x16x32_bf16 v[78:81], v[162:165], v[194:197], v[78:81]
	v_mfma_f32_16x16x32_bf16 v[74:77], v[170:173], v[194:197], v[74:77]
	v_mfma_f32_16x16x32_bf16 v[70:73], v[162:165], v[202:205], v[70:73]
	v_mfma_f32_16x16x32_bf16 v[66:69], v[170:173], v[202:205], v[66:69]
	v_mfma_f32_16x16x32_bf16 v[110:113], v[166:169], v[182:185], v[110:113]
	v_mfma_f32_16x16x32_bf16 v[106:109], v[174:177], v[182:185], v[106:109]
	v_mfma_f32_16x16x32_bf16 v[94:97], v[166:169], v[190:193], v[94:97]
	v_mfma_f32_16x16x32_bf16 v[90:93], v[174:177], v[190:193], v[90:93]
	v_mfma_f32_16x16x32_bf16 v[78:81], v[166:169], v[198:201], v[78:81]
	v_mfma_f32_16x16x32_bf16 v[74:77], v[174:177], v[198:201], v[74:77]
	v_mfma_f32_16x16x32_bf16 v[70:73], v[166:169], v[216:219], v[70:73]
	v_mfma_f32_16x16x32_bf16 v[66:69], v[174:177], v[216:219], v[66:69]
	s_setprio 0
	s_barrier
	s_mov_b32 m0, s21
	v_lshl_add_u64 v[208:209], s[54:55], 0, v[134:135]
	ds_read_b128 v[178:181], v145 offset:16384
	ds_read_b128 v[182:185], v145 offset:17408
	ds_read_b128 v[186:189], v145 offset:18432
	ds_read_b128 v[190:193], v145 offset:19456
	ds_read_b128 v[194:197], v145 offset:20480
	ds_read_b128 v[198:201], v145 offset:21504
	ds_read_b128 v[202:205], v145 offset:22528
	ds_read_b128 v[216:219], v145 offset:23552
	global_load_lds_dwordx4 v[208:209], off
	v_lshl_add_u64 v[210:211], s[54:55], 0, v[130:131]
	s_mov_b32 m0, s18
	v_lshl_add_u64 v[212:213], s[56:57], 0, v[134:135]
	global_load_lds_dwordx4 v[210:211], off
	s_mov_b32 m0, s20
	v_lshl_add_u64 v[220:221], s[50:51], 0, v[132:133]
	global_load_lds_dwordx4 v[212:213], off
	v_lshl_add_u64 v[212:213], s[56:57], 0, v[130:131]
	s_mov_b32 m0, s19
	s_nop 0
	global_load_lds_dwordx4 v[212:213], off
	v_lshl_add_u64 v[212:213], s[50:51], 0, v[136:137]
	s_mov_b32 m0, s27
	s_nop 0
	global_load_lds_dwordx4 v[212:213], off
	s_mov_b32 m0, s60
	s_nop 0
	global_load_lds_dwordx4 v[220:221], off
	s_waitcnt vmcnt(8)
	s_waitcnt lgkmcnt(0)
	s_barrier
; #define PG8_STAGE_A(bufoff, kptr, half, VO) do { if constexpr (GATHER) { _Pragma("unroll") for (int _i = 0; _i < 2; ++_i) \
;         __builtin_amdgcn_global_load_lds((const unsigned*)((const char*)(kptr) + (VO)[half][_i]), (LAS unsigned*)(lds + (bufoff) + ldsw + _i * 8192), 16, 0, 0); } \
;         else { PG8_STAGE(bufoff, (kptr) + (half) * hstepA, voffA); } } while (0)
; #define PG8_LDA(dst, b, h) do { _Pragma("unroll") for (int m = 0; m < 4; ++m) _Pragma("unroll") for (int k = 0; k < 2; ++k) dst[m][k] = *(const LAS bf16x8*)(lds + PG8_SA(b, h) + aoff + m * 2048 + k * 1024); } while (0)
; #define PG8_LDB(dst, b, h) do { _Pragma("unroll") for (int n = 0; n < 2; ++n) _Pragma("unroll") for (int k = 0; k < 2; ++k) dst[n][k] = *(const LAS bf16x8*)(lds + PG8_SB(b, h) + boff + n * 2048 + k * 1024); } while (0)
; #define PG8_MMA(ai, bj, At, Bt) do { __builtin_amdgcn_s_setprio(1); _Pragma("unroll") for (int m = 0; m < 4; ++m) _Pragma("unroll") for (int n = 0; n < 2; ++n) _Pragma("unroll") for (int k = 0; k < 2; ++k) \
;         acc[ai][bj][m][n] = __builtin_amdgcn_mfma_f32_16x16x32_bf16(Bt[n][k], At[m][k], acc[ai][bj][m][n], 0, 0, 0); __builtin_amdgcn_s_setprio(0); } while (0)
; #define PG8_WAIT_V(n) asm volatile("s_waitcnt vmcnt(" #n ")" ::: "memory")
; #define PG8_WAIT_L(n) asm volatile("s_waitcnt lgkmcnt(" #n ")" ::: "memory")
; #define PG8_BAR __builtin_amdgcn_s_barrier()
; #define PG8_SCHED __builtin_amdgcn_sched_barrier(0)
;     ...
;             PG8_WAIT_V(8); PG8_WAIT_L(0); PG8_BAR; PG8_MMA(1, 0, At, B0); PG8_MMA(1, 1, At, B1); PG8_BAR; PG8_SCHED;
;             PG8_LDB(B0, 1, 0); PG8_LDB(B1, 1, 1); PG8_SCHED; PG8_LDA(At, 1, 0); PG8_STAGE_A(PG8_SA(0, 1), a2, 1, g2);
;             PG8_WAIT_V(8); PG8_WAIT_L(0); PG8_BAR; PG8_MMA(0, 0, At, B0); PG8_MMA(0, 1, At, B1); PG8_BAR; PG8_SCHED;
	s_setprio 1
	s_waitcnt lgkmcnt(0)
	v_mfma_f32_16x16x32_bf16 v[62:65], v[146:149], v[178:181], v[62:65]
	v_mfma_f32_16x16x32_bf16 v[58:61], v[154:157], v[178:181], v[58:61]
	v_mfma_f32_16x16x32_bf16 v[54:57], v[146:149], v[186:189], v[54:57]
	v_mfma_f32_16x16x32_bf16 v[50:53], v[154:157], v[186:189], v[50:53]
	v_mfma_f32_16x16x32_bf16 v[38:41], v[146:149], v[194:197], v[38:41]
	v_mfma_f32_16x16x32_bf16 v[34:37], v[154:157], v[194:197], v[34:37]
	v_mfma_f32_16x16x32_bf16 v[22:25], v[146:149], v[202:205], v[22:25]
	v_mfma_f32_16x16x32_bf16 v[18:21], v[154:157], v[202:205], v[18:21]
	v_mfma_f32_16x16x32_bf16 v[62:65], v[150:153], v[182:185], v[62:65]
	v_mfma_f32_16x16x32_bf16 v[58:61], v[158:161], v[182:185], v[58:61]
	v_mfma_f32_16x16x32_bf16 v[54:57], v[150:153], v[190:193], v[54:57]
	v_mfma_f32_16x16x32_bf16 v[50:53], v[158:161], v[190:193], v[50:53]
	v_mfma_f32_16x16x32_bf16 v[38:41], v[150:153], v[198:201], v[38:41]
	v_mfma_f32_16x16x32_bf16 v[34:37], v[158:161], v[198:201], v[34:37]
	v_mfma_f32_16x16x32_bf16 v[22:25], v[150:153], v[216:219], v[22:25]
	v_mfma_f32_16x16x32_bf16 v[18:21], v[158:161], v[216:219], v[18:21]
	v_mfma_f32_16x16x32_bf16 v[46:49], v[162:165], v[178:181], v[46:49]
	v_mfma_f32_16x16x32_bf16 v[42:45], v[170:173], v[178:181], v[42:45]
	v_mfma_f32_16x16x32_bf16 v[30:33], v[162:165], v[186:189], v[30:33]
	v_mfma_f32_16x16x32_bf16 v[26:29], v[170:173], v[186:189], v[26:29]
	v_mfma_f32_16x16x32_bf16 v[14:17], v[162:165], v[194:197], v[14:17]
	v_mfma_f32_16x16x32_bf16 v[10:13], v[170:173], v[194:197], v[10:13]
	v_mfma_f32_16x16x32_bf16 v[6:9], v[162:165], v[202:205], v[6:9]
	v_mfma_f32_16x16x32_bf16 v[2:5], v[170:173], v[202:205], v[2:5]
	v_mfma_f32_16x16x32_bf16 v[46:49], v[166:169], v[182:185], v[46:49]
	v_mfma_f32_16x16x32_bf16 v[42:45], v[174:177], v[182:185], v[42:45]
	v_mfma_f32_16x16x32_bf16 v[30:33], v[166:169], v[190:193], v[30:33]
	v_mfma_f32_16x16x32_bf16 v[26:29], v[174:177], v[190:193], v[26:29]
	v_mfma_f32_16x16x32_bf16 v[14:17], v[166:169], v[198:201], v[14:17]
	v_mfma_f32_16x16x32_bf16 v[10:13], v[174:177], v[198:201], v[10:13]
	v_mfma_f32_16x16x32_bf16 v[6:9], v[166:169], v[216:219], v[6:9]
	v_mfma_f32_16x16x32_bf16 v[2:5], v[174:177], v[216:219], v[2:5]
	s_setprio 0
	s_barrier
	v_add_u32_e32 v143, s17, v144
	ds_read_b128 v[146:149], v143
	ds_read_b128 v[150:153], v143 offset:1024
	ds_read_b128 v[154:157], v143 offset:2048
	ds_read_b128 v[158:161], v143 offset:3072
	v_add_u32_e32 v143, s16, v144
	ds_read_b128 v[162:165], v143
	ds_read_b128 v[166:169], v143 offset:1024
	ds_read_b128 v[170:173], v143 offset:2048
	ds_read_b128 v[174:177], v143 offset:3072
	s_mov_b32 m0, s61
	v_lshl_add_u64 v[222:223], s[48:49], 0, v[136:137]
	ds_read_b128 v[178:181], v145 offset:32768
	ds_read_b128 v[182:185], v145 offset:33792
	ds_read_b128 v[186:189], v145 offset:34816
	ds_read_b128 v[190:193], v145 offset:35840
	ds_read_b128 v[194:197], v145 offset:36864
	ds_read_b128 v[198:201], v145 offset:37888
	ds_read_b128 v[202:205], v145 offset:38912
	ds_read_b128 v[216:219], v145 offset:39936
	global_load_lds_dwordx4 v[222:223], off
	v_lshl_add_u64 v[222:223], s[48:49], 0, v[132:133]
	s_mov_b32 m0, s63
	s_nop 0
	global_load_lds_dwordx4 v[222:223], off
	s_waitcnt vmcnt(8)
	s_waitcnt lgkmcnt(0)
	s_barrier
	s_setprio 1
	s_waitcnt lgkmcnt(0)
	v_mfma_f32_16x16x32_bf16 v[126:129], v[146:149], v[178:181], v[126:129]
	v_mfma_f32_16x16x32_bf16 v[122:125], v[154:157], v[178:181], v[122:125]
	v_mfma_f32_16x16x32_bf16 v[118:121], v[146:149], v[186:189], v[118:121]
	v_mfma_f32_16x16x32_bf16 v[114:117], v[154:157], v[186:189], v[114:117]
	v_mfma_f32_16x16x32_bf16 v[102:105], v[146:149], v[194:197], v[102:105]
	v_mfma_f32_16x16x32_bf16 v[98:101], v[154:157], v[194:197], v[98:101]
	v_mfma_f32_16x16x32_bf16 v[86:89], v[146:149], v[202:205], v[86:89]
	v_mfma_f32_16x16x32_bf16 v[82:85], v[154:157], v[202:205], v[82:85]
	v_mfma_f32_16x16x32_bf16 v[126:129], v[150:153], v[182:185], v[126:129]
	v_mfma_f32_16x16x32_bf16 v[122:125], v[158:161], v[182:185], v[122:125]
	v_mfma_f32_16x16x32_bf16 v[118:121], v[150:153], v[190:193], v[118:121]
	v_mfma_f32_16x16x32_bf16 v[114:117], v[158:161], v[190:193], v[114:117]
	v_mfma_f32_16x16x32_bf16 v[102:105], v[150:153], v[198:201], v[102:105]
	v_mfma_f32_16x16x32_bf16 v[98:101], v[158:161], v[198:201], v[98:101]
	v_mfma_f32_16x16x32_bf16 v[86:89], v[150:153], v[216:219], v[86:89]
	v_mfma_f32_16x16x32_bf16 v[82:85], v[158:161], v[216:219], v[82:85]
	v_mfma_f32_16x16x32_bf16 v[110:113], v[162:165], v[178:181], v[110:113]
	v_mfma_f32_16x16x32_bf16 v[106:109], v[170:173], v[178:181], v[106:109]
	v_mfma_f32_16x16x32_bf16 v[94:97], v[162:165], v[186:189], v[94:97]
	v_mfma_f32_16x16x32_bf16 v[90:93], v[170:173], v[186:189], v[90:93]
	v_mfma_f32_16x16x32_bf16 v[78:81], v[162:165], v[194:197], v[78:81]
	v_mfma_f32_16x16x32_bf16 v[74:77], v[170:173], v[194:197], v[74:77]
	v_mfma_f32_16x16x32_bf16 v[70:73], v[162:165], v[202:205], v[70:73]
	v_mfma_f32_16x16x32_bf16 v[66:69], v[170:173], v[202:205], v[66:69]
	v_mfma_f32_16x16x32_bf16 v[110:113], v[166:169], v[182:185], v[110:113]
	v_mfma_f32_16x16x32_bf16 v[106:109], v[174:177], v[182:185], v[106:109]
	v_mfma_f32_16x16x32_bf16 v[94:97], v[166:169], v[190:193], v[94:97]
	v_mfma_f32_16x16x32_bf16 v[90:93], v[174:177], v[190:193], v[90:93]
	v_mfma_f32_16x16x32_bf16 v[78:81], v[166:169], v[198:201], v[78:81]
	v_mfma_f32_16x16x32_bf16 v[74:77], v[174:177], v[198:201], v[74:77]
	v_mfma_f32_16x16x32_bf16 v[70:73], v[166:169], v[216:219], v[70:73]
	v_mfma_f32_16x16x32_bf16 v[66:69], v[174:177], v[216:219], v[66:69]
	s_setprio 0
	s_barrier
; #define PG8_STAGE(bufoff, gbase, voff) do { _Pragma("unroll") for (int _i = 0; _i < 2; ++_i) \
;         __builtin_amdgcn_global_load_lds((const unsigned*)((const char*)(gbase) + (voff)[_i]), (LAS unsigned*)(lds + (bufoff) + ldsw + _i * 8192), 16, 0, 0); } while (0)
; #define PG8_STAGE_A(bufoff, kptr, half, VO) do { if constexpr (GATHER) { _Pragma("unroll") for (int _i = 0; _i < 2; ++_i) \
;         __builtin_amdgcn_global_load_lds((const unsigned*)((const char*)(kptr) + (VO)[half][_i]), (LAS unsigned*)(lds + (bufoff) + ldsw + _i * 8192), 16, 0, 0); } \
;         else { PG8_STAGE(bufoff, (kptr) + (half) * hstepA, voffA); } } while (0)
; #define PG8_LDA(dst, b, h) do { _Pragma("unroll") for (int m = 0; m < 4; ++m) _Pragma("unroll") for (int k = 0; k < 2; ++k) dst[m][k] = *(const LAS bf16x8*)(lds + PG8_SA(b, h) + aoff + m * 2048 + k * 1024); } while (0)
; #define PG8_MMA(ai, bj, At, Bt) do { __builtin_amdgcn_s_setprio(1); _Pragma("unroll") for (int m = 0; m < 4; ++m) _Pragma("unroll") for (int n = 0; n < 2; ++n) _Pragma("unroll") for (int k = 0; k < 2; ++k) \
;         acc[ai][bj][m][n] = __builtin_amdgcn_mfma_f32_16x16x32_bf16(Bt[n][k], At[m][k], acc[ai][bj][m][n], 0, 0, 0); __builtin_amdgcn_s_setprio(0); } while (0)
; #define PG8_WAIT_V(n) asm volatile("s_waitcnt vmcnt(" #n ")" ::: "memory")
; #define PG8_WAIT_L(n) asm volatile("s_waitcnt lgkmcnt(" #n ")" ::: "memory")
; #define PG8_BAR __builtin_amdgcn_s_barrier()
; #define PG8_SCHED __builtin_amdgcn_sched_barrier(0)
;     ...
;             PG8_LDA(At, 1, 1); PG8_STAGE(PG8_SB(1, 0), b3, voffB); PG8_STAGE(PG8_SB(1, 1), b3 + hstepB, voffB); PG8_STAGE_A(PG8_SA(1, 0), a3, 0, g2);
;             PG8_WAIT_V(8); PG8_WAIT_L(0); PG8_BAR; PG8_MMA(1, 0, At, B0); PG8_MMA(1, 1, At, B1); PG8_BAR; PG8_SCHED;
	s_mov_b32 m0, s15
	v_lshl_add_u64 v[208:209], v[208:209], 0, s[8:9]
	ds_read_b128 v[178:181], v145 offset:49152
	ds_read_b128 v[182:185], v145 offset:50176
	ds_read_b128 v[186:189], v145 offset:51200
	ds_read_b128 v[190:193], v145 offset:52224
	ds_read_b128 v[194:197], v145 offset:53248
	ds_read_b128 v[198:201], v145 offset:54272
	ds_read_b128 v[202:205], v145 offset:55296
	ds_read_b128 v[216:219], v145 offset:56320
	global_load_lds_dwordx4 v[208:209], off
	v_lshl_add_u64 v[208:209], v[210:211], 0, s[8:9]
	s_mov_b32 m0, s14
	s_nop 0
	global_load_lds_dwordx4 v[208:209], off
	v_lshl_add_u64 v[208:209], s[0:1], 0, v[134:135]
	s_mov_b32 m0, s23
	s_nop 0
	global_load_lds_dwordx4 v[208:209], off
	v_lshl_add_u64 v[208:209], s[0:1], 0, v[130:131]
	s_mov_b32 m0, s22
	s_nop 0
	global_load_lds_dwordx4 v[208:209], off
	v_lshl_add_u64 v[208:209], v[212:213], 0, s[8:9]
	s_mov_b32 m0, s64
	s_nop 0
	global_load_lds_dwordx4 v[208:209], off
	v_lshl_add_u64 v[208:209], v[220:221], 0, s[8:9]
	s_mov_b32 m0, s65
	s_nop 0
	global_load_lds_dwordx4 v[208:209], off
	s_waitcnt vmcnt(8)
	s_waitcnt lgkmcnt(0)
	s_barrier
	s_setprio 1
	s_waitcnt lgkmcnt(0)
	v_mfma_f32_16x16x32_bf16 v[62:65], v[146:149], v[178:181], v[62:65]
	v_mfma_f32_16x16x32_bf16 v[58:61], v[154:157], v[178:181], v[58:61]
	v_mfma_f32_16x16x32_bf16 v[54:57], v[146:149], v[186:189], v[54:57]
	v_mfma_f32_16x16x32_bf16 v[50:53], v[154:157], v[186:189], v[50:53]
	v_mfma_f32_16x16x32_bf16 v[38:41], v[146:149], v[194:197], v[38:41]
	v_mfma_f32_16x16x32_bf16 v[34:37], v[154:157], v[194:197], v[34:37]
	v_mfma_f32_16x16x32_bf16 v[22:25], v[146:149], v[202:205], v[22:25]
	v_mfma_f32_16x16x32_bf16 v[18:21], v[154:157], v[202:205], v[18:21]
	v_mfma_f32_16x16x32_bf16 v[62:65], v[150:153], v[182:185], v[62:65]
	v_mfma_f32_16x16x32_bf16 v[58:61], v[158:161], v[182:185], v[58:61]
	v_mfma_f32_16x16x32_bf16 v[54:57], v[150:153], v[190:193], v[54:57]
	v_mfma_f32_16x16x32_bf16 v[50:53], v[158:161], v[190:193], v[50:53]
	v_mfma_f32_16x16x32_bf16 v[38:41], v[150:153], v[198:201], v[38:41]
	v_mfma_f32_16x16x32_bf16 v[34:37], v[158:161], v[198:201], v[34:37]
	v_mfma_f32_16x16x32_bf16 v[22:25], v[150:153], v[216:219], v[22:25]
	v_mfma_f32_16x16x32_bf16 v[18:21], v[158:161], v[216:219], v[18:21]
	v_mfma_f32_16x16x32_bf16 v[46:49], v[162:165], v[178:181], v[46:49]
	v_mfma_f32_16x16x32_bf16 v[42:45], v[170:173], v[178:181], v[42:45]
	v_mfma_f32_16x16x32_bf16 v[30:33], v[162:165], v[186:189], v[30:33]
	v_mfma_f32_16x16x32_bf16 v[26:29], v[170:173], v[186:189], v[26:29]
	v_mfma_f32_16x16x32_bf16 v[14:17], v[162:165], v[194:197], v[14:17]
	v_mfma_f32_16x16x32_bf16 v[10:13], v[170:173], v[194:197], v[10:13]
	v_mfma_f32_16x16x32_bf16 v[6:9], v[162:165], v[202:205], v[6:9]
	v_mfma_f32_16x16x32_bf16 v[2:5], v[170:173], v[202:205], v[2:5]
	v_mfma_f32_16x16x32_bf16 v[46:49], v[166:169], v[182:185], v[46:49]
	v_mfma_f32_16x16x32_bf16 v[42:45], v[174:177], v[182:185], v[42:45]
	v_mfma_f32_16x16x32_bf16 v[30:33], v[166:169], v[190:193], v[30:33]
	v_mfma_f32_16x16x32_bf16 v[26:29], v[174:177], v[190:193], v[26:29]
	v_mfma_f32_16x16x32_bf16 v[14:17], v[166:169], v[198:201], v[14:17]
	v_mfma_f32_16x16x32_bf16 v[10:13], v[174:177], v[198:201], v[10:13]
	v_mfma_f32_16x16x32_bf16 v[6:9], v[166:169], v[216:219], v[6:9]
	v_mfma_f32_16x16x32_bf16 v[2:5], v[174:177], v[216:219], v[2:5]
	s_setprio 0
	s_barrier
	s_andn2_b64 vcc, exec, s[30:31]
	s_mov_b64 s[0:1], -1
	s_mov_b64 s[30:31], 0
	s_mov_b64 s[48:49], 0x100
	s_cbranch_vccz .LBB0_684
	s_and_b64 vcc, exec, s[38:39]
	s_cbranch_vccz .LBB0_687
	s_barrier

; #define PG8_STAGE(bufoff, gbase, voff) do { _Pragma("unroll") for (int _i = 0; _i < 2; ++_i) \
;         __builtin_amdgcn_global_load_lds((const unsigned*)((const char*)(gbase) + (voff)[_i]), (LAS unsigned*)(lds + (bufoff) + ldsw + _i * 8192), 16, 0, 0); } while (0)
; #define PG8_STAGE_A(bufoff, kptr, half, VO) do { if constexpr (GATHER) { _Pragma("unroll") for (int _i = 0; _i < 2; ++_i) \
;         __builtin_amdgcn_global_load_lds((const unsigned*)((const char*)(kptr) + (VO)[half][_i]), (LAS unsigned*)(lds + (bufoff) + ldsw + _i * 8192), 16, 0, 0); } \
;         else { PG8_STAGE(bufoff, (kptr) + (half) * hstepA, voffA); } } while (0)
; #define PG8_LDA(dst, b, h) do { _Pragma("unroll") for (int m = 0; m < 4; ++m) _Pragma("unroll") for (int k = 0; k < 2; ++k) dst[m][k] = *(const LAS bf16x8*)(lds + PG8_SA(b, h) + aoff + m * 2048 + k * 1024); } while (0)
; #define PG8_LDB(dst, b, h) do { _Pragma("unroll") for (int n = 0; n < 2; ++n) _Pragma("unroll") for (int k = 0; k < 2; ++k) dst[n][k] = *(const LAS bf16x8*)(lds + PG8_SB(b, h) + boff + n * 2048 + k * 1024); } while (0)
; #define PG8_WAIT_V(n) asm volatile("s_waitcnt vmcnt(" #n ")" ::: "memory")
; #define PG8_WAIT_L(n) asm volatile("s_waitcnt lgkmcnt(" #n ")" ::: "memory")
; #define PG8_BAR __builtin_amdgcn_s_barrier()
;     ...
;             const char* a1 = cA + (size_t)(t + 1) * kstep;
;             const char* a2 = last ? nA : cA + (size_t)(t + 2) * kstep; const char* b2 = last ? nB : cB + (size_t)(t + 2) * kstep;
;             const char* a3 = a2 + kstep; const char* b3 = b2 + kstep;
;             unsigned g2[2][2];
;             if constexpr (GATHER) {
; #pragma unroll
;                 for (int _h = 0; _h < 2; ++_h)
; #pragma unroll
;                     for (int _i = 0; _i < 2; ++_i) g2[_h][_i] = last ? gN[_h][_i] : gC[_h][_i]; }
;             if constexpr (SP2) {
;             PG8_LDB(B0, 0, 0); PG8_LDB(B1, 0, 1); PG8_SCHED; PG8_LDA(At, 0, 0); PG8_STAGE_A(PG8_SA(1, 1), a1, 1, gC);
;             PG8_WAIT_V(8); PG8_WAIT_L(0); PG8_BAR; PG8_MMA(0, 0, At, B0); PG8_MMA(0, 1, At, B1); PG8_BAR; PG8_SCHED;
;             PG8_LDA(At, 0, 1); PG8_STAGE(PG8_SB(0, 0), b2, voffB); PG8_STAGE(PG8_SB(0, 1), b2 + hstepB, voffB); PG8_STAGE_A(PG8_SA(0, 0), a2, 0, g2);
;             PG8_WAIT_V(8); PG8_WAIT_L(0); PG8_BAR; PG8_MMA(1, 0, At, B0); PG8_MMA(1, 1, At, B1); PG8_BAR; PG8_SCHED;
.LBB0_702:
	s_add_u32 s16, s40, s30
	s_addc_u32 s17, s41, s31
	s_add_u32 s18, s16, 0x100
	s_addc_u32 s19, s17, 0
	s_and_b64 s[14:15], s[0:1], exec
	s_cselect_b32 s55, s49, s19
	s_cselect_b32 s54, s48, s18
	s_add_u32 s14, s38, s30
	s_addc_u32 s15, s39, s31
	s_add_u32 s14, s14, 0x100
	s_addc_u32 s15, s15, 0
	s_add_i32 s22, 0, 0x10000
	s_and_b64 s[0:1], s[0:1], exec
	s_cselect_b32 s57, s51, s15
	s_cselect_b32 s56, s50, s14
	s_add_i32 s1, 0, 0x14000
	s_add_u32 s60, s16, 0x20080
	s_addc_u32 s61, s17, 0
	s_add_i32 s21, s22, s27
	s_add_i32 m0, s63, 0xc000
	s_add_i32 s34, s63, 0xe000
	s_add_i32 s18, s21, 0x2000
	v_add_u32_e32 v138, s22, v141
	s_add_u32 s58, s56, 0x10000
	ds_read_b128 v[144:147], v138
	ds_read_b128 v[148:151], v138 offset:1024
	ds_read_b128 v[152:155], v138 offset:2048
	ds_read_b128 v[156:159], v138 offset:3072
	v_add_u32_e32 v138, s1, v141
	s_addc_u32 s59, s57, 0
	s_add_i32 s20, s1, s27
	ds_read_b128 v[160:163], v138
	ds_read_b128 v[164:167], v138 offset:1024
	ds_read_b128 v[168:171], v138 offset:2048
	ds_read_b128 v[172:175], v138 offset:3072
	s_add_i32 s19, s20, 0x2000
	s_add_i32 s17, 0, 0x18000
	s_add_i32 s16, 0, 0x1c000
	s_add_u32 s30, s54, 0x20000
	s_addc_u32 s31, s55, 0
	s_add_i32 s15, s17, s27
	s_add_i32 s14, s15, 0x2000
	s_add_u32 s0, s56, 0x10080
	s_addc_u32 s1, s57, 0
	s_add_i32 s23, s16, s27
	s_add_i32 s22, s23, 0x2000
	v_lshl_add_u64 v[138:139], s[60:61], 0, v[130:131]
	ds_read_b128 v[176:179], v142
	ds_read_b128 v[180:183], v142 offset:1024
	ds_read_b128 v[184:187], v142 offset:2048
	ds_read_b128 v[188:191], v142 offset:3072
	ds_read_b128 v[192:195], v142 offset:4096
	ds_read_b128 v[196:199], v142 offset:5120
	ds_read_b128 v[200:203], v142 offset:6144
	ds_read_b128 v[216:219], v142 offset:7168
	global_load_lds_dwordx4 v[138:139], off
	v_lshl_add_u64 v[138:139], s[60:61], 0, v[132:133]
	s_mov_b32 m0, s34
	s_nop 0
	global_load_lds_dwordx4 v[138:139], off
	s_waitcnt vmcnt(8)
	s_waitcnt lgkmcnt(0)
	s_barrier
	s_setprio 1
	s_waitcnt lgkmcnt(0)
	v_mfma_f32_16x16x32_bf16 v[126:129], v[144:147], v[176:179], v[126:129]
	v_mfma_f32_16x16x32_bf16 v[122:125], v[152:155], v[176:179], v[122:125]
	v_mfma_f32_16x16x32_bf16 v[118:121], v[144:147], v[184:187], v[118:121]
	v_mfma_f32_16x16x32_bf16 v[114:117], v[152:155], v[184:187], v[114:117]
	v_mfma_f32_16x16x32_bf16 v[102:105], v[144:147], v[192:195], v[102:105]
	v_mfma_f32_16x16x32_bf16 v[98:101], v[152:155], v[192:195], v[98:101]
	v_mfma_f32_16x16x32_bf16 v[86:89], v[144:147], v[200:203], v[86:89]
	v_mfma_f32_16x16x32_bf16 v[82:85], v[152:155], v[200:203], v[82:85]
	v_mfma_f32_16x16x32_bf16 v[126:129], v[148:151], v[180:183], v[126:129]
	v_mfma_f32_16x16x32_bf16 v[122:125], v[156:159], v[180:183], v[122:125]
	v_mfma_f32_16x16x32_bf16 v[118:121], v[148:151], v[188:191], v[118:121]
	v_mfma_f32_16x16x32_bf16 v[114:117], v[156:159], v[188:191], v[114:117]
	v_mfma_f32_16x16x32_bf16 v[102:105], v[148:151], v[196:199], v[102:105]
	v_mfma_f32_16x16x32_bf16 v[98:101], v[156:159], v[196:199], v[98:101]
	v_mfma_f32_16x16x32_bf16 v[86:89], v[148:151], v[216:219], v[86:89]
	v_mfma_f32_16x16x32_bf16 v[82:85], v[156:159], v[216:219], v[82:85]
	v_mfma_f32_16x16x32_bf16 v[110:113], v[160:163], v[176:179], v[110:113]
	v_mfma_f32_16x16x32_bf16 v[106:109], v[168:171], v[176:179], v[106:109]
	v_mfma_f32_16x16x32_bf16 v[94:97], v[160:163], v[184:187], v[94:97]
	v_mfma_f32_16x16x32_bf16 v[90:93], v[168:171], v[184:187], v[90:93]
	v_mfma_f32_16x16x32_bf16 v[78:81], v[160:163], v[192:195], v[78:81]
	v_mfma_f32_16x16x32_bf16 v[74:77], v[168:171], v[192:195], v[74:77]
	v_mfma_f32_16x16x32_bf16 v[70:73], v[160:163], v[200:203], v[70:73]
	v_mfma_f32_16x16x32_bf16 v[66:69], v[168:171], v[200:203], v[66:69]
	v_mfma_f32_16x16x32_bf16 v[110:113], v[164:167], v[180:183], v[110:113]
	v_mfma_f32_16x16x32_bf16 v[106:109], v[172:175], v[180:183], v[106:109]
	v_mfma_f32_16x16x32_bf16 v[94:97], v[164:167], v[188:191], v[94:97]
	v_mfma_f32_16x16x32_bf16 v[90:93], v[172:175], v[188:191], v[90:93]
	v_mfma_f32_16x16x32_bf16 v[78:81], v[164:167], v[196:199], v[78:81]
	v_mfma_f32_16x16x32_bf16 v[74:77], v[172:175], v[196:199], v[74:77]
	v_mfma_f32_16x16x32_bf16 v[70:73], v[164:167], v[216:219], v[70:73]
	v_mfma_f32_16x16x32_bf16 v[66:69], v[172:175], v[216:219], v[66:69]
	s_setprio 0
	s_barrier
	s_mov_b32 m0, s21
	v_lshl_add_u64 v[138:139], s[56:57], 0, v[206:207]
	ds_read_b128 v[176:179], v142 offset:16384
	ds_read_b128 v[180:183], v142 offset:17408
	ds_read_b128 v[184:187], v142 offset:18432
	ds_read_b128 v[188:191], v142 offset:19456
	ds_read_b128 v[192:195], v142 offset:20480
	ds_read_b128 v[196:199], v142 offset:21504
	ds_read_b128 v[200:203], v142 offset:22528
	ds_read_b128 v[216:219], v142 offset:23552
	global_load_lds_dwordx4 v[138:139], off
	v_lshl_add_u64 v[204:205], s[56:57], 0, v[134:135]
	s_mov_b32 m0, s18
	v_lshl_add_u64 v[208:209], s[58:59], 0, v[206:207]
	global_load_lds_dwordx4 v[204:205], off
	s_mov_b32 m0, s20
	v_lshl_add_u64 v[210:211], s[54:55], 0, v[132:133]
	global_load_lds_dwordx4 v[208:209], off
	v_lshl_add_u64 v[208:209], s[58:59], 0, v[134:135]
	s_mov_b32 m0, s19
	s_nop 0
	global_load_lds_dwordx4 v[208:209], off
	v_lshl_add_u64 v[208:209], s[54:55], 0, v[130:131]
	s_mov_b32 m0, s63
	s_nop 0
	global_load_lds_dwordx4 v[208:209], off
	s_mov_b32 m0, s64
	s_nop 0
	global_load_lds_dwordx4 v[210:211], off
	s_waitcnt vmcnt(8)
	s_waitcnt lgkmcnt(0)
	s_barrier
; #define PG8_STAGE_A(bufoff, kptr, half, VO) do { if constexpr (GATHER) { _Pragma("unroll") for (int _i = 0; _i < 2; ++_i) \
;         __builtin_amdgcn_global_load_lds((const unsigned*)((const char*)(kptr) + (VO)[half][_i]), (LAS unsigned*)(lds + (bufoff) + ldsw + _i * 8192), 16, 0, 0); } \
;         else { PG8_STAGE(bufoff, (kptr) + (half) * hstepA, voffA); } } while (0)
; #define PG8_LDA(dst, b, h) do { _Pragma("unroll") for (int m = 0; m < 4; ++m) _Pragma("unroll") for (int k = 0; k < 2; ++k) dst[m][k] = *(const LAS bf16x8*)(lds + PG8_SA(b, h) + aoff + m * 2048 + k * 1024); } while (0)
; #define PG8_LDB(dst, b, h) do { _Pragma("unroll") for (int n = 0; n < 2; ++n) _Pragma("unroll") for (int k = 0; k < 2; ++k) dst[n][k] = *(const LAS bf16x8*)(lds + PG8_SB(b, h) + boff + n * 2048 + k * 1024); } while (0)
; #define PG8_MMA(ai, bj, At, Bt) do { __builtin_amdgcn_s_setprio(1); _Pragma("unroll") for (int m = 0; m < 4; ++m) _Pragma("unroll") for (int n = 0; n < 2; ++n) _Pragma("unroll") for (int k = 0; k < 2; ++k) \
;         acc[ai][bj][m][n] = __builtin_amdgcn_mfma_f32_16x16x32_bf16(Bt[n][k], At[m][k], acc[ai][bj][m][n], 0, 0, 0); __builtin_amdgcn_s_setprio(0); } while (0)
; #define PG8_WAIT_V(n) asm volatile("s_waitcnt vmcnt(" #n ")" ::: "memory")
; #define PG8_WAIT_L(n) asm volatile("s_waitcnt lgkmcnt(" #n ")" ::: "memory")
; #define PG8_BAR __builtin_amdgcn_s_barrier()
; #define PG8_SCHED __builtin_amdgcn_sched_barrier(0)
;     ...
;             PG8_WAIT_V(8); PG8_WAIT_L(0); PG8_BAR; PG8_MMA(1, 0, At, B0); PG8_MMA(1, 1, At, B1); PG8_BAR; PG8_SCHED;
;             PG8_LDB(B0, 1, 0); PG8_LDB(B1, 1, 1); PG8_SCHED; PG8_LDA(At, 1, 0); PG8_STAGE_A(PG8_SA(0, 1), a2, 1, g2);
;             PG8_WAIT_V(8); PG8_WAIT_L(0); PG8_BAR; PG8_MMA(0, 0, At, B0); PG8_MMA(0, 1, At, B1); PG8_BAR; PG8_SCHED;
	s_setprio 1
	s_waitcnt lgkmcnt(0)
	v_mfma_f32_16x16x32_bf16 v[62:65], v[144:147], v[176:179], v[62:65]
	v_mfma_f32_16x16x32_bf16 v[58:61], v[152:155], v[176:179], v[58:61]
	v_mfma_f32_16x16x32_bf16 v[54:57], v[144:147], v[184:187], v[54:57]
	v_mfma_f32_16x16x32_bf16 v[50:53], v[152:155], v[184:187], v[50:53]
	v_mfma_f32_16x16x32_bf16 v[38:41], v[144:147], v[192:195], v[38:41]
	v_mfma_f32_16x16x32_bf16 v[34:37], v[152:155], v[192:195], v[34:37]
	v_mfma_f32_16x16x32_bf16 v[22:25], v[144:147], v[200:203], v[22:25]
	v_mfma_f32_16x16x32_bf16 v[18:21], v[152:155], v[200:203], v[18:21]
	v_mfma_f32_16x16x32_bf16 v[62:65], v[148:151], v[180:183], v[62:65]
	v_mfma_f32_16x16x32_bf16 v[58:61], v[156:159], v[180:183], v[58:61]
	v_mfma_f32_16x16x32_bf16 v[54:57], v[148:151], v[188:191], v[54:57]
	v_mfma_f32_16x16x32_bf16 v[50:53], v[156:159], v[188:191], v[50:53]
	v_mfma_f32_16x16x32_bf16 v[38:41], v[148:151], v[196:199], v[38:41]
	v_mfma_f32_16x16x32_bf16 v[34:37], v[156:159], v[196:199], v[34:37]
	v_mfma_f32_16x16x32_bf16 v[22:25], v[148:151], v[216:219], v[22:25]
	v_mfma_f32_16x16x32_bf16 v[18:21], v[156:159], v[216:219], v[18:21]
	v_mfma_f32_16x16x32_bf16 v[46:49], v[160:163], v[176:179], v[46:49]
	v_mfma_f32_16x16x32_bf16 v[42:45], v[168:171], v[176:179], v[42:45]
	v_mfma_f32_16x16x32_bf16 v[30:33], v[160:163], v[184:187], v[30:33]
	v_mfma_f32_16x16x32_bf16 v[26:29], v[168:171], v[184:187], v[26:29]
	v_mfma_f32_16x16x32_bf16 v[14:17], v[160:163], v[192:195], v[14:17]
	v_mfma_f32_16x16x32_bf16 v[10:13], v[168:171], v[192:195], v[10:13]
	v_mfma_f32_16x16x32_bf16 v[6:9], v[160:163], v[200:203], v[6:9]
	v_mfma_f32_16x16x32_bf16 v[2:5], v[168:171], v[200:203], v[2:5]
	v_mfma_f32_16x16x32_bf16 v[46:49], v[164:167], v[180:183], v[46:49]
	v_mfma_f32_16x16x32_bf16 v[42:45], v[172:175], v[180:183], v[42:45]
	v_mfma_f32_16x16x32_bf16 v[30:33], v[164:167], v[188:191], v[30:33]
	v_mfma_f32_16x16x32_bf16 v[26:29], v[172:175], v[188:191], v[26:29]
	v_mfma_f32_16x16x32_bf16 v[14:17], v[164:167], v[196:199], v[14:17]
	v_mfma_f32_16x16x32_bf16 v[10:13], v[172:175], v[196:199], v[10:13]
	v_mfma_f32_16x16x32_bf16 v[6:9], v[164:167], v[216:219], v[6:9]
	v_mfma_f32_16x16x32_bf16 v[2:5], v[172:175], v[216:219], v[2:5]
	s_setprio 0
	s_barrier
	v_add_u32_e32 v143, s17, v141
	ds_read_b128 v[144:147], v143
	ds_read_b128 v[148:151], v143 offset:1024
	ds_read_b128 v[152:155], v143 offset:2048
	ds_read_b128 v[156:159], v143 offset:3072
	v_add_u32_e32 v143, s16, v141
	ds_read_b128 v[160:163], v143
	ds_read_b128 v[164:167], v143 offset:1024
	ds_read_b128 v[168:171], v143 offset:2048
	ds_read_b128 v[172:175], v143 offset:3072
	s_mov_b32 m0, s65
	v_lshl_add_u64 v[212:213], s[30:31], 0, v[130:131]
	ds_read_b128 v[176:179], v142 offset:32768
	ds_read_b128 v[180:183], v142 offset:33792
	ds_read_b128 v[184:187], v142 offset:34816
	ds_read_b128 v[188:191], v142 offset:35840
	ds_read_b128 v[192:195], v142 offset:36864
	ds_read_b128 v[196:199], v142 offset:37888
	ds_read_b128 v[200:203], v142 offset:38912
	ds_read_b128 v[216:219], v142 offset:39936
	global_load_lds_dwordx4 v[212:213], off
	v_lshl_add_u64 v[212:213], s[30:31], 0, v[132:133]
	s_mov_b32 m0, s66
	s_nop 0
	global_load_lds_dwordx4 v[212:213], off
	s_waitcnt vmcnt(8)
	s_waitcnt lgkmcnt(0)
	s_barrier
	s_setprio 1
	s_waitcnt lgkmcnt(0)
	v_mfma_f32_16x16x32_bf16 v[126:129], v[144:147], v[176:179], v[126:129]
	v_mfma_f32_16x16x32_bf16 v[122:125], v[152:155], v[176:179], v[122:125]
	v_mfma_f32_16x16x32_bf16 v[118:121], v[144:147], v[184:187], v[118:121]
	v_mfma_f32_16x16x32_bf16 v[114:117], v[152:155], v[184:187], v[114:117]
	v_mfma_f32_16x16x32_bf16 v[102:105], v[144:147], v[192:195], v[102:105]
	v_mfma_f32_16x16x32_bf16 v[98:101], v[152:155], v[192:195], v[98:101]
	v_mfma_f32_16x16x32_bf16 v[86:89], v[144:147], v[200:203], v[86:89]
	v_mfma_f32_16x16x32_bf16 v[82:85], v[152:155], v[200:203], v[82:85]
	v_mfma_f32_16x16x32_bf16 v[126:129], v[148:151], v[180:183], v[126:129]
	v_mfma_f32_16x16x32_bf16 v[122:125], v[156:159], v[180:183], v[122:125]
	v_mfma_f32_16x16x32_bf16 v[118:121], v[148:151], v[188:191], v[118:121]
	v_mfma_f32_16x16x32_bf16 v[114:117], v[156:159], v[188:191], v[114:117]
	v_mfma_f32_16x16x32_bf16 v[102:105], v[148:151], v[196:199], v[102:105]
	v_mfma_f32_16x16x32_bf16 v[98:101], v[156:159], v[196:199], v[98:101]
	v_mfma_f32_16x16x32_bf16 v[86:89], v[148:151], v[216:219], v[86:89]
	v_mfma_f32_16x16x32_bf16 v[82:85], v[156:159], v[216:219], v[82:85]
	v_mfma_f32_16x16x32_bf16 v[110:113], v[160:163], v[176:179], v[110:113]
	v_mfma_f32_16x16x32_bf16 v[106:109], v[168:171], v[176:179], v[106:109]
	v_mfma_f32_16x16x32_bf16 v[94:97], v[160:163], v[184:187], v[94:97]
	v_mfma_f32_16x16x32_bf16 v[90:93], v[168:171], v[184:187], v[90:93]
	v_mfma_f32_16x16x32_bf16 v[78:81], v[160:163], v[192:195], v[78:81]
	v_mfma_f32_16x16x32_bf16 v[74:77], v[168:171], v[192:195], v[74:77]
	v_mfma_f32_16x16x32_bf16 v[70:73], v[160:163], v[200:203], v[70:73]
	v_mfma_f32_16x16x32_bf16 v[66:69], v[168:171], v[200:203], v[66:69]
	v_mfma_f32_16x16x32_bf16 v[110:113], v[164:167], v[180:183], v[110:113]
	v_mfma_f32_16x16x32_bf16 v[106:109], v[172:175], v[180:183], v[106:109]
	v_mfma_f32_16x16x32_bf16 v[94:97], v[164:167], v[188:191], v[94:97]
	v_mfma_f32_16x16x32_bf16 v[90:93], v[172:175], v[188:191], v[90:93]
	v_mfma_f32_16x16x32_bf16 v[78:81], v[164:167], v[196:199], v[78:81]
	v_mfma_f32_16x16x32_bf16 v[74:77], v[172:175], v[196:199], v[74:77]
	v_mfma_f32_16x16x32_bf16 v[70:73], v[164:167], v[216:219], v[70:73]
	v_mfma_f32_16x16x32_bf16 v[66:69], v[172:175], v[216:219], v[66:69]
	s_setprio 0
	s_barrier
; #define PG8_STAGE(bufoff, gbase, voff) do { _Pragma("unroll") for (int _i = 0; _i < 2; ++_i) \
;         __builtin_amdgcn_global_load_lds((const unsigned*)((const char*)(gbase) + (voff)[_i]), (LAS unsigned*)(lds + (bufoff) + ldsw + _i * 8192), 16, 0, 0); } while (0)
; #define PG8_STAGE_A(bufoff, kptr, half, VO) do { if constexpr (GATHER) { _Pragma("unroll") for (int _i = 0; _i < 2; ++_i) \
;         __builtin_amdgcn_global_load_lds((const unsigned*)((const char*)(kptr) + (VO)[half][_i]), (LAS unsigned*)(lds + (bufoff) + ldsw + _i * 8192), 16, 0, 0); } \
;         else { PG8_STAGE(bufoff, (kptr) + (half) * hstepA, voffA); } } while (0)
; #define PG8_LDA(dst, b, h) do { _Pragma("unroll") for (int m = 0; m < 4; ++m) _Pragma("unroll") for (int k = 0; k < 2; ++k) dst[m][k] = *(const LAS bf16x8*)(lds + PG8_SA(b, h) + aoff + m * 2048 + k * 1024); } while (0)
; #define PG8_MMA(ai, bj, At, Bt) do { __builtin_amdgcn_s_setprio(1); _Pragma("unroll") for (int m = 0; m < 4; ++m) _Pragma("unroll") for (int n = 0; n < 2; ++n) _Pragma("unroll") for (int k = 0; k < 2; ++k) \
;         acc[ai][bj][m][n] = __builtin_amdgcn_mfma_f32_16x16x32_bf16(Bt[n][k], At[m][k], acc[ai][bj][m][n], 0, 0, 0); __builtin_amdgcn_s_setprio(0); } while (0)
; #define PG8_WAIT_V(n) asm volatile("s_waitcnt vmcnt(" #n ")" ::: "memory")
; #define PG8_WAIT_L(n) asm volatile("s_waitcnt lgkmcnt(" #n ")" ::: "memory")
; #define PG8_BAR __builtin_amdgcn_s_barrier()
; #define PG8_SCHED __builtin_amdgcn_sched_barrier(0)
;     ...
;             PG8_LDA(At, 1, 1); PG8_STAGE(PG8_SB(1, 0), b3, voffB); PG8_STAGE(PG8_SB(1, 1), b3 + hstepB, voffB); PG8_STAGE_A(PG8_SA(1, 0), a3, 0, g2);
;             PG8_WAIT_V(8); PG8_WAIT_L(0); PG8_BAR; PG8_MMA(1, 0, At, B0); PG8_MMA(1, 1, At, B1); PG8_BAR; PG8_SCHED;
	s_mov_b32 m0, s15
	v_lshl_add_u64 v[138:139], v[138:139], 0, s[8:9]
	ds_read_b128 v[176:179], v142 offset:49152
	ds_read_b128 v[180:183], v142 offset:50176
	ds_read_b128 v[184:187], v142 offset:51200
	ds_read_b128 v[188:191], v142 offset:52224
	ds_read_b128 v[192:195], v142 offset:53248
	ds_read_b128 v[196:199], v142 offset:54272
	ds_read_b128 v[200:203], v142 offset:55296
	ds_read_b128 v[216:219], v142 offset:56320
	global_load_lds_dwordx4 v[138:139], off
	v_lshl_add_u64 v[138:139], v[204:205], 0, s[8:9]
	s_mov_b32 m0, s14
	s_nop 0
	global_load_lds_dwordx4 v[138:139], off
	v_lshl_add_u64 v[138:139], s[0:1], 0, v[206:207]
	s_mov_b32 m0, s23
	s_nop 0
	global_load_lds_dwordx4 v[138:139], off
	v_lshl_add_u64 v[138:139], s[0:1], 0, v[134:135]
	s_mov_b32 m0, s22
	s_nop 0
	global_load_lds_dwordx4 v[138:139], off
	v_lshl_add_u64 v[138:139], v[208:209], 0, s[8:9]
	s_mov_b32 m0, s67
	s_nop 0
	global_load_lds_dwordx4 v[138:139], off
	v_lshl_add_u64 v[138:139], v[210:211], 0, s[8:9]
	s_mov_b32 m0, s68
	s_nop 0
	global_load_lds_dwordx4 v[138:139], off
	s_waitcnt vmcnt(8)
	s_waitcnt lgkmcnt(0)
	s_barrier
	s_setprio 1
	s_waitcnt lgkmcnt(0)
	v_mfma_f32_16x16x32_bf16 v[62:65], v[144:147], v[176:179], v[62:65]
	v_mfma_f32_16x16x32_bf16 v[58:61], v[152:155], v[176:179], v[58:61]
	v_mfma_f32_16x16x32_bf16 v[54:57], v[144:147], v[184:187], v[54:57]
	v_mfma_f32_16x16x32_bf16 v[50:53], v[152:155], v[184:187], v[50:53]
	v_mfma_f32_16x16x32_bf16 v[38:41], v[144:147], v[192:195], v[38:41]
	v_mfma_f32_16x16x32_bf16 v[34:37], v[152:155], v[192:195], v[34:37]
	v_mfma_f32_16x16x32_bf16 v[22:25], v[144:147], v[200:203], v[22:25]
	v_mfma_f32_16x16x32_bf16 v[18:21], v[152:155], v[200:203], v[18:21]
	v_mfma_f32_16x16x32_bf16 v[62:65], v[148:151], v[180:183], v[62:65]
	v_mfma_f32_16x16x32_bf16 v[58:61], v[156:159], v[180:183], v[58:61]
	v_mfma_f32_16x16x32_bf16 v[54:57], v[148:151], v[188:191], v[54:57]
	v_mfma_f32_16x16x32_bf16 v[50:53], v[156:159], v[188:191], v[50:53]
	v_mfma_f32_16x16x32_bf16 v[38:41], v[148:151], v[196:199], v[38:41]
	v_mfma_f32_16x16x32_bf16 v[34:37], v[156:159], v[196:199], v[34:37]
	v_mfma_f32_16x16x32_bf16 v[22:25], v[148:151], v[216:219], v[22:25]
	v_mfma_f32_16x16x32_bf16 v[18:21], v[156:159], v[216:219], v[18:21]
	v_mfma_f32_16x16x32_bf16 v[46:49], v[160:163], v[176:179], v[46:49]
	v_mfma_f32_16x16x32_bf16 v[42:45], v[168:171], v[176:179], v[42:45]
	v_mfma_f32_16x16x32_bf16 v[30:33], v[160:163], v[184:187], v[30:33]
	v_mfma_f32_16x16x32_bf16 v[26:29], v[168:171], v[184:187], v[26:29]
	v_mfma_f32_16x16x32_bf16 v[14:17], v[160:163], v[192:195], v[14:17]
	v_mfma_f32_16x16x32_bf16 v[10:13], v[168:171], v[192:195], v[10:13]
	v_mfma_f32_16x16x32_bf16 v[6:9], v[160:163], v[200:203], v[6:9]
	v_mfma_f32_16x16x32_bf16 v[2:5], v[168:171], v[200:203], v[2:5]
	v_mfma_f32_16x16x32_bf16 v[46:49], v[164:167], v[180:183], v[46:49]
	v_mfma_f32_16x16x32_bf16 v[42:45], v[172:175], v[180:183], v[42:45]
	v_mfma_f32_16x16x32_bf16 v[30:33], v[164:167], v[188:191], v[30:33]
	v_mfma_f32_16x16x32_bf16 v[26:29], v[172:175], v[188:191], v[26:29]
	v_mfma_f32_16x16x32_bf16 v[14:17], v[164:167], v[196:199], v[14:17]
	v_mfma_f32_16x16x32_bf16 v[10:13], v[172:175], v[196:199], v[10:13]
	v_mfma_f32_16x16x32_bf16 v[6:9], v[164:167], v[216:219], v[6:9]
	v_mfma_f32_16x16x32_bf16 v[2:5], v[172:175], v[216:219], v[2:5]
	s_setprio 0
	s_barrier
	s_andn2_b64 vcc, exec, s[24:25]
	s_mov_b64 s[0:1], -1
	s_mov_b64 s[24:25], 0
	s_mov_b64 s[30:31], 0x100
	s_cbranch_vccz .LBB0_702
	s_and_b64 vcc, exec, s[42:43]
	s_cbranch_vccz .LBB0_705
	s_barrier

; #define PG8_STAGE(bufoff, gbase, voff) do { _Pragma("unroll") for (int _i = 0; _i < 2; ++_i) \
;         __builtin_amdgcn_global_load_lds((const unsigned*)((const char*)(gbase) + (voff)[_i]), (LAS unsigned*)(lds + (bufoff) + ldsw + _i * 8192), 16, 0, 0); } while (0)
; #define PG8_STAGE_A(bufoff, kptr, half, VO) do { if constexpr (GATHER) { _Pragma("unroll") for (int _i = 0; _i < 2; ++_i) \
;         __builtin_amdgcn_global_load_lds((const unsigned*)((const char*)(kptr) + (VO)[half][_i]), (LAS unsigned*)(lds + (bufoff) + ldsw + _i * 8192), 16, 0, 0); } \
;         else { PG8_STAGE(bufoff, (kptr) + (half) * hstepA, voffA); } } while (0)
; #define PG8_LDA(dst, b, h) do { _Pragma("unroll") for (int m = 0; m < 4; ++m) _Pragma("unroll") for (int k = 0; k < 2; ++k) dst[m][k] = *(const LAS bf16x8*)(lds + PG8_SA(b, h) + aoff + m * 2048 + k * 1024); } while (0)
; #define PG8_LDB(dst, b, h) do { _Pragma("unroll") for (int n = 0; n < 2; ++n) _Pragma("unroll") for (int k = 0; k < 2; ++k) dst[n][k] = *(const LAS bf16x8*)(lds + PG8_SB(b, h) + boff + n * 2048 + k * 1024); } while (0)
; #define PG8_WAIT_V(n) asm volatile("s_waitcnt vmcnt(" #n ")" ::: "memory")
; #define PG8_WAIT_L(n) asm volatile("s_waitcnt lgkmcnt(" #n ")" ::: "memory")
; #define PG8_BAR __builtin_amdgcn_s_barrier()
;     ...
;             const char* a1 = cA + (size_t)(t + 1) * kstep;
;             const char* a2 = last ? nA : cA + (size_t)(t + 2) * kstep; const char* b2 = last ? nB : cB + (size_t)(t + 2) * kstep;
;             const char* a3 = a2 + kstep; const char* b3 = b2 + kstep;
;             unsigned g2[2][2];
;             if constexpr (GATHER) {
; #pragma unroll
;                 for (int _h = 0; _h < 2; ++_h)
; #pragma unroll
;                     for (int _i = 0; _i < 2; ++_i) g2[_h][_i] = last ? gN[_h][_i] : gC[_h][_i]; }
;             if constexpr (SP2) {
;             PG8_LDB(B0, 0, 0); PG8_LDB(B1, 0, 1); PG8_SCHED; PG8_LDA(At, 0, 0); PG8_STAGE_A(PG8_SA(1, 1), a1, 1, gC);
;             PG8_WAIT_V(8); PG8_WAIT_L(0); PG8_BAR; PG8_MMA(0, 0, At, B0); PG8_MMA(0, 1, At, B1); PG8_BAR; PG8_SCHED;
;             PG8_LDA(At, 0, 1); PG8_STAGE(PG8_SB(0, 0), b2, voffB); PG8_STAGE(PG8_SB(0, 1), b2 + hstepB, voffB); PG8_STAGE_A(PG8_SA(0, 0), a2, 0, g2);
;             PG8_WAIT_V(8); PG8_WAIT_L(0); PG8_BAR; PG8_MMA(1, 0, At, B0); PG8_MMA(1, 1, At, B1); PG8_BAR; PG8_SCHED;
.LBB0_1318:
	s_add_u32 s0, s24, 0xfffe0080
	s_addc_u32 s1, s25, -1
	s_add_i32 s17, 0, 0x10000
	s_cmp_eq_u32 s16, 4
	s_cselect_b32 s31, s45, s1
	s_cselect_b32 s30, s44, s0
	v_add_u32_e32 v147, s17, v144
	s_cselect_b32 s1, s47, s15
	s_cselect_b32 s0, s46, s14
	s_add_i32 s20, 0, 0x14000
	ds_read_b128 v[148:151], v147
	ds_read_b128 v[152:155], v147 offset:1024
	ds_read_b128 v[156:159], v147 offset:2048
	ds_read_b128 v[160:163], v147 offset:3072
	v_add_u32_e32 v147, s20, v144
	ds_read_b128 v[164:167], v147
	ds_read_b128 v[168:171], v147 offset:1024
	ds_read_b128 v[172:175], v147 offset:2048
	ds_read_b128 v[176:179], v147 offset:3072
	v_lshl_add_u64 v[204:205], s[24:25], 0, v[140:141]
	s_add_i32 m0, s51, 0xc000
	ds_read_b128 v[180:183], v146
	ds_read_b128 v[184:187], v146 offset:1024
	ds_read_b128 v[188:191], v146 offset:2048
	ds_read_b128 v[192:195], v146 offset:3072
	ds_read_b128 v[196:199], v146 offset:4096
	ds_read_b128 v[200:203], v146 offset:5120
	ds_read_b128 v[216:219], v146 offset:6144
	ds_read_b128 v[220:223], v146 offset:7168
	global_load_lds_dwordx4 v[204:205], off
	v_lshl_add_u64 v[204:205], s[24:25], 0, v[142:143]
	s_add_i32 m0, s51, 0xe000
	s_nop 0
	global_load_lds_dwordx4 v[204:205], off
	s_waitcnt vmcnt(8)
	s_waitcnt lgkmcnt(0)
	s_barrier
	s_setprio 1
	s_waitcnt lgkmcnt(0)
	v_mfma_f32_16x16x32_bf16 v[126:129], v[148:151], v[180:183], v[126:129]
	v_mfma_f32_16x16x32_bf16 v[122:125], v[156:159], v[180:183], v[122:125]
	v_mfma_f32_16x16x32_bf16 v[110:113], v[148:151], v[188:191], v[110:113]
	v_mfma_f32_16x16x32_bf16 v[106:109], v[156:159], v[188:191], v[106:109]
	v_mfma_f32_16x16x32_bf16 v[94:97], v[148:151], v[196:199], v[94:97]
	v_mfma_f32_16x16x32_bf16 v[90:93], v[156:159], v[196:199], v[90:93]
	v_mfma_f32_16x16x32_bf16 v[78:81], v[148:151], v[216:219], v[78:81]
	v_mfma_f32_16x16x32_bf16 v[74:77], v[156:159], v[216:219], v[74:77]
	v_mfma_f32_16x16x32_bf16 v[126:129], v[152:155], v[184:187], v[126:129]
	v_mfma_f32_16x16x32_bf16 v[122:125], v[160:163], v[184:187], v[122:125]
	v_mfma_f32_16x16x32_bf16 v[110:113], v[152:155], v[192:195], v[110:113]
	v_mfma_f32_16x16x32_bf16 v[106:109], v[160:163], v[192:195], v[106:109]
	v_mfma_f32_16x16x32_bf16 v[94:97], v[152:155], v[200:203], v[94:97]
	v_mfma_f32_16x16x32_bf16 v[90:93], v[160:163], v[200:203], v[90:93]
	v_mfma_f32_16x16x32_bf16 v[78:81], v[152:155], v[220:223], v[78:81]
	v_mfma_f32_16x16x32_bf16 v[74:77], v[160:163], v[220:223], v[74:77]
	v_mfma_f32_16x16x32_bf16 v[118:121], v[164:167], v[180:183], v[118:121]
	v_mfma_f32_16x16x32_bf16 v[114:117], v[172:175], v[180:183], v[114:117]
	v_mfma_f32_16x16x32_bf16 v[102:105], v[164:167], v[188:191], v[102:105]
	v_mfma_f32_16x16x32_bf16 v[98:101], v[172:175], v[188:191], v[98:101]
	v_mfma_f32_16x16x32_bf16 v[86:89], v[164:167], v[196:199], v[86:89]
	v_mfma_f32_16x16x32_bf16 v[82:85], v[172:175], v[196:199], v[82:85]
	v_mfma_f32_16x16x32_bf16 v[70:73], v[164:167], v[216:219], v[70:73]
	v_mfma_f32_16x16x32_bf16 v[66:69], v[172:175], v[216:219], v[66:69]
	v_mfma_f32_16x16x32_bf16 v[118:121], v[168:171], v[184:187], v[118:121]
	v_mfma_f32_16x16x32_bf16 v[114:117], v[176:179], v[184:187], v[114:117]
	v_mfma_f32_16x16x32_bf16 v[102:105], v[168:171], v[192:195], v[102:105]
	v_mfma_f32_16x16x32_bf16 v[98:101], v[176:179], v[192:195], v[98:101]
	v_mfma_f32_16x16x32_bf16 v[86:89], v[168:171], v[200:203], v[86:89]
	v_mfma_f32_16x16x32_bf16 v[82:85], v[176:179], v[200:203], v[82:85]
	v_mfma_f32_16x16x32_bf16 v[70:73], v[168:171], v[220:223], v[70:73]
	v_mfma_f32_16x16x32_bf16 v[66:69], v[176:179], v[220:223], v[66:69]
	s_setprio 0
	s_barrier
	s_add_i32 s17, s17, s27
	v_lshl_add_u64 v[204:205], s[0:1], 0, v[132:133]
	s_mov_b32 m0, s17
	ds_read_b128 v[180:183], v146 offset:16384
	ds_read_b128 v[184:187], v146 offset:17408
	ds_read_b128 v[188:191], v146 offset:18432
	ds_read_b128 v[192:195], v146 offset:19456
	ds_read_b128 v[196:199], v146 offset:20480
	ds_read_b128 v[200:203], v146 offset:21504
	ds_read_b128 v[216:219], v146 offset:22528
	ds_read_b128 v[220:223], v146 offset:23552
	global_load_lds_dwordx4 v[204:205], off
	s_add_i32 m0, s17, 0x2000
	s_add_u32 s18, s0, 0x20000
	v_lshl_add_u64 v[208:209], s[0:1], 0, v[136:137]
	s_addc_u32 s19, s1, 0
	s_add_i32 s17, s20, s27
	global_load_lds_dwordx4 v[208:209], off
	v_lshl_add_u64 v[210:211], s[18:19], 0, v[132:133]
	s_mov_b32 m0, s17
	v_lshl_add_u64 v[212:213], s[30:31], 0, v[134:135]
	global_load_lds_dwordx4 v[210:211], off
	v_lshl_add_u64 v[210:211], s[18:19], 0, v[136:137]
	s_add_i32 m0, s17, 0x2000
	s_nop 0
	global_load_lds_dwordx4 v[210:211], off
	v_lshl_add_u64 v[210:211], s[30:31], 0, v[130:131]
	s_mov_b32 m0, s51
	s_nop 0
	global_load_lds_dwordx4 v[210:211], off
	s_mov_b32 m0, s54
	s_nop 0
	global_load_lds_dwordx4 v[212:213], off
	s_waitcnt vmcnt(8)
	s_waitcnt lgkmcnt(0)
	s_barrier
; #define PG8_STAGE_A(bufoff, kptr, half, VO) do { if constexpr (GATHER) { _Pragma("unroll") for (int _i = 0; _i < 2; ++_i) \
;         __builtin_amdgcn_global_load_lds((const unsigned*)((const char*)(kptr) + (VO)[half][_i]), (LAS unsigned*)(lds + (bufoff) + ldsw + _i * 8192), 16, 0, 0); } \
;         else { PG8_STAGE(bufoff, (kptr) + (half) * hstepA, voffA); } } while (0)
; #define PG8_LDA(dst, b, h) do { _Pragma("unroll") for (int m = 0; m < 4; ++m) _Pragma("unroll") for (int k = 0; k < 2; ++k) dst[m][k] = *(const LAS bf16x8*)(lds + PG8_SA(b, h) + aoff + m * 2048 + k * 1024); } while (0)
; #define PG8_LDB(dst, b, h) do { _Pragma("unroll") for (int n = 0; n < 2; ++n) _Pragma("unroll") for (int k = 0; k < 2; ++k) dst[n][k] = *(const LAS bf16x8*)(lds + PG8_SB(b, h) + boff + n * 2048 + k * 1024); } while (0)
; #define PG8_MMA(ai, bj, At, Bt) do { __builtin_amdgcn_s_setprio(1); _Pragma("unroll") for (int m = 0; m < 4; ++m) _Pragma("unroll") for (int n = 0; n < 2; ++n) _Pragma("unroll") for (int k = 0; k < 2; ++k) \
;         acc[ai][bj][m][n] = __builtin_amdgcn_mfma_f32_16x16x32_bf16(Bt[n][k], At[m][k], acc[ai][bj][m][n], 0, 0, 0); __builtin_amdgcn_s_setprio(0); } while (0)
; #define PG8_WAIT_V(n) asm volatile("s_waitcnt vmcnt(" #n ")" ::: "memory")
; #define PG8_WAIT_L(n) asm volatile("s_waitcnt lgkmcnt(" #n ")" ::: "memory")
; #define PG8_BAR __builtin_amdgcn_s_barrier()
; #define PG8_SCHED __builtin_amdgcn_sched_barrier(0)
;     ...
;             PG8_WAIT_V(8); PG8_WAIT_L(0); PG8_BAR; PG8_MMA(1, 0, At, B0); PG8_MMA(1, 1, At, B1); PG8_BAR; PG8_SCHED;
;             PG8_LDB(B0, 1, 0); PG8_LDB(B1, 1, 1); PG8_SCHED; PG8_LDA(At, 1, 0); PG8_STAGE_A(PG8_SA(0, 1), a2, 1, g2);
;             PG8_WAIT_V(8); PG8_WAIT_L(0); PG8_BAR; PG8_MMA(0, 0, At, B0); PG8_MMA(0, 1, At, B1); PG8_BAR; PG8_SCHED;
	s_setprio 1
	s_waitcnt lgkmcnt(0)
	v_mfma_f32_16x16x32_bf16 v[62:65], v[148:151], v[180:183], v[62:65]
	v_mfma_f32_16x16x32_bf16 v[58:61], v[156:159], v[180:183], v[58:61]
	v_mfma_f32_16x16x32_bf16 v[46:49], v[148:151], v[188:191], v[46:49]
	v_mfma_f32_16x16x32_bf16 v[42:45], v[156:159], v[188:191], v[42:45]
	v_mfma_f32_16x16x32_bf16 v[30:33], v[148:151], v[196:199], v[30:33]
	v_mfma_f32_16x16x32_bf16 v[26:29], v[156:159], v[196:199], v[26:29]
	v_mfma_f32_16x16x32_bf16 v[14:17], v[148:151], v[216:219], v[14:17]
	v_mfma_f32_16x16x32_bf16 v[10:13], v[156:159], v[216:219], v[10:13]
	v_mfma_f32_16x16x32_bf16 v[62:65], v[152:155], v[184:187], v[62:65]
	v_mfma_f32_16x16x32_bf16 v[58:61], v[160:163], v[184:187], v[58:61]
	v_mfma_f32_16x16x32_bf16 v[46:49], v[152:155], v[192:195], v[46:49]
	v_mfma_f32_16x16x32_bf16 v[42:45], v[160:163], v[192:195], v[42:45]
	v_mfma_f32_16x16x32_bf16 v[30:33], v[152:155], v[200:203], v[30:33]
	v_mfma_f32_16x16x32_bf16 v[26:29], v[160:163], v[200:203], v[26:29]
	v_mfma_f32_16x16x32_bf16 v[14:17], v[152:155], v[220:223], v[14:17]
	v_mfma_f32_16x16x32_bf16 v[10:13], v[160:163], v[220:223], v[10:13]
	v_mfma_f32_16x16x32_bf16 v[54:57], v[164:167], v[180:183], v[54:57]
	v_mfma_f32_16x16x32_bf16 v[50:53], v[172:175], v[180:183], v[50:53]
	v_mfma_f32_16x16x32_bf16 v[38:41], v[164:167], v[188:191], v[38:41]
	v_mfma_f32_16x16x32_bf16 v[34:37], v[172:175], v[188:191], v[34:37]
	v_mfma_f32_16x16x32_bf16 v[22:25], v[164:167], v[196:199], v[22:25]
	v_mfma_f32_16x16x32_bf16 v[18:21], v[172:175], v[196:199], v[18:21]
	v_mfma_f32_16x16x32_bf16 v[6:9], v[164:167], v[216:219], v[6:9]
	v_mfma_f32_16x16x32_bf16 v[2:5], v[172:175], v[216:219], v[2:5]
	v_mfma_f32_16x16x32_bf16 v[54:57], v[168:171], v[184:187], v[54:57]
	v_mfma_f32_16x16x32_bf16 v[50:53], v[176:179], v[184:187], v[50:53]
	v_mfma_f32_16x16x32_bf16 v[38:41], v[168:171], v[192:195], v[38:41]
	v_mfma_f32_16x16x32_bf16 v[34:37], v[176:179], v[192:195], v[34:37]
	v_mfma_f32_16x16x32_bf16 v[22:25], v[168:171], v[200:203], v[22:25]
	v_mfma_f32_16x16x32_bf16 v[18:21], v[176:179], v[200:203], v[18:21]
	v_mfma_f32_16x16x32_bf16 v[6:9], v[168:171], v[220:223], v[6:9]
	v_mfma_f32_16x16x32_bf16 v[2:5], v[176:179], v[220:223], v[2:5]
	s_setprio 0
	s_barrier
	s_add_i32 s17, 0, 0x18000
	v_add_u32_e32 v147, s17, v144
	s_add_i32 s20, 0, 0x1c000
	ds_read_b128 v[148:151], v147
	ds_read_b128 v[152:155], v147 offset:1024
	ds_read_b128 v[156:159], v147 offset:2048
	ds_read_b128 v[160:163], v147 offset:3072
	v_add_u32_e32 v147, s20, v144
	ds_read_b128 v[164:167], v147
	ds_read_b128 v[168:171], v147 offset:1024
	ds_read_b128 v[172:175], v147 offset:2048
	ds_read_b128 v[176:179], v147 offset:3072
	s_add_u32 s18, s30, 0x20000
	s_addc_u32 s19, s31, 0
	s_mov_b32 m0, s55
	v_lshl_add_u64 v[224:225], s[18:19], 0, v[130:131]
	ds_read_b128 v[180:183], v146 offset:32768
	ds_read_b128 v[184:187], v146 offset:33792
	ds_read_b128 v[188:191], v146 offset:34816
	ds_read_b128 v[192:195], v146 offset:35840
	ds_read_b128 v[196:199], v146 offset:36864
	ds_read_b128 v[200:203], v146 offset:37888
	ds_read_b128 v[216:219], v146 offset:38912
	ds_read_b128 v[220:223], v146 offset:39936
	global_load_lds_dwordx4 v[224:225], off
	v_lshl_add_u64 v[224:225], s[18:19], 0, v[134:135]
	s_mov_b32 m0, s56
	s_nop 0
	global_load_lds_dwordx4 v[224:225], off
	s_waitcnt vmcnt(8)
	s_waitcnt lgkmcnt(0)
	s_barrier
	s_setprio 1
	s_waitcnt lgkmcnt(0)
	v_mfma_f32_16x16x32_bf16 v[126:129], v[148:151], v[180:183], v[126:129]
	v_mfma_f32_16x16x32_bf16 v[122:125], v[156:159], v[180:183], v[122:125]
	v_mfma_f32_16x16x32_bf16 v[110:113], v[148:151], v[188:191], v[110:113]
	v_mfma_f32_16x16x32_bf16 v[106:109], v[156:159], v[188:191], v[106:109]
	v_mfma_f32_16x16x32_bf16 v[94:97], v[148:151], v[196:199], v[94:97]
	v_mfma_f32_16x16x32_bf16 v[90:93], v[156:159], v[196:199], v[90:93]
	v_mfma_f32_16x16x32_bf16 v[78:81], v[148:151], v[216:219], v[78:81]
	v_mfma_f32_16x16x32_bf16 v[74:77], v[156:159], v[216:219], v[74:77]
	v_mfma_f32_16x16x32_bf16 v[126:129], v[152:155], v[184:187], v[126:129]
	v_mfma_f32_16x16x32_bf16 v[122:125], v[160:163], v[184:187], v[122:125]
	v_mfma_f32_16x16x32_bf16 v[110:113], v[152:155], v[192:195], v[110:113]
	v_mfma_f32_16x16x32_bf16 v[106:109], v[160:163], v[192:195], v[106:109]
	v_mfma_f32_16x16x32_bf16 v[94:97], v[152:155], v[200:203], v[94:97]
	v_mfma_f32_16x16x32_bf16 v[90:93], v[160:163], v[200:203], v[90:93]
	v_mfma_f32_16x16x32_bf16 v[78:81], v[152:155], v[220:223], v[78:81]
	v_mfma_f32_16x16x32_bf16 v[74:77], v[160:163], v[220:223], v[74:77]
	v_mfma_f32_16x16x32_bf16 v[118:121], v[164:167], v[180:183], v[118:121]
	v_mfma_f32_16x16x32_bf16 v[114:117], v[172:175], v[180:183], v[114:117]
	v_mfma_f32_16x16x32_bf16 v[102:105], v[164:167], v[188:191], v[102:105]
	v_mfma_f32_16x16x32_bf16 v[98:101], v[172:175], v[188:191], v[98:101]
	v_mfma_f32_16x16x32_bf16 v[86:89], v[164:167], v[196:199], v[86:89]
	v_mfma_f32_16x16x32_bf16 v[82:85], v[172:175], v[196:199], v[82:85]
	v_mfma_f32_16x16x32_bf16 v[70:73], v[164:167], v[216:219], v[70:73]
	v_mfma_f32_16x16x32_bf16 v[66:69], v[172:175], v[216:219], v[66:69]
	v_mfma_f32_16x16x32_bf16 v[118:121], v[168:171], v[184:187], v[118:121]
	v_mfma_f32_16x16x32_bf16 v[114:117], v[176:179], v[184:187], v[114:117]
	v_mfma_f32_16x16x32_bf16 v[102:105], v[168:171], v[192:195], v[102:105]
	v_mfma_f32_16x16x32_bf16 v[98:101], v[176:179], v[192:195], v[98:101]
	v_mfma_f32_16x16x32_bf16 v[86:89], v[168:171], v[200:203], v[86:89]
	v_mfma_f32_16x16x32_bf16 v[82:85], v[176:179], v[200:203], v[82:85]
	v_mfma_f32_16x16x32_bf16 v[70:73], v[168:171], v[220:223], v[70:73]
	v_mfma_f32_16x16x32_bf16 v[66:69], v[176:179], v[220:223], v[66:69]
	s_setprio 0
	s_barrier
; #define PG8_STAGE(bufoff, gbase, voff) do { _Pragma("unroll") for (int _i = 0; _i < 2; ++_i) \
;         __builtin_amdgcn_global_load_lds((const unsigned*)((const char*)(gbase) + (voff)[_i]), (LAS unsigned*)(lds + (bufoff) + ldsw + _i * 8192), 16, 0, 0); } while (0)
; #define PG8_STAGE_A(bufoff, kptr, half, VO) do { if constexpr (GATHER) { _Pragma("unroll") for (int _i = 0; _i < 2; ++_i) \
;         __builtin_amdgcn_global_load_lds((const unsigned*)((const char*)(kptr) + (VO)[half][_i]), (LAS unsigned*)(lds + (bufoff) + ldsw + _i * 8192), 16, 0, 0); } \
;         else { PG8_STAGE(bufoff, (kptr) + (half) * hstepA, voffA); } } while (0)
; #define PG8_LDA(dst, b, h) do { _Pragma("unroll") for (int m = 0; m < 4; ++m) _Pragma("unroll") for (int k = 0; k < 2; ++k) dst[m][k] = *(const LAS bf16x8*)(lds + PG8_SA(b, h) + aoff + m * 2048 + k * 1024); } while (0)
; #define PG8_MMA(ai, bj, At, Bt) do { __builtin_amdgcn_s_setprio(1); _Pragma("unroll") for (int m = 0; m < 4; ++m) _Pragma("unroll") for (int n = 0; n < 2; ++n) _Pragma("unroll") for (int k = 0; k < 2; ++k) \
;         acc[ai][bj][m][n] = __builtin_amdgcn_mfma_f32_16x16x32_bf16(Bt[n][k], At[m][k], acc[ai][bj][m][n], 0, 0, 0); __builtin_amdgcn_s_setprio(0); } while (0)
; #define PG8_WAIT_V(n) asm volatile("s_waitcnt vmcnt(" #n ")" ::: "memory")
; #define PG8_WAIT_L(n) asm volatile("s_waitcnt lgkmcnt(" #n ")" ::: "memory")
; #define PG8_BAR __builtin_amdgcn_s_barrier()
; #define PG8_SCHED __builtin_amdgcn_sched_barrier(0)
;     ...
;             PG8_LDA(At, 1, 1); PG8_STAGE(PG8_SB(1, 0), b3, voffB); PG8_STAGE(PG8_SB(1, 1), b3 + hstepB, voffB); PG8_STAGE_A(PG8_SA(1, 0), a3, 0, g2);
;             PG8_WAIT_V(8); PG8_WAIT_L(0); PG8_BAR; PG8_MMA(1, 0, At, B0); PG8_MMA(1, 1, At, B1); PG8_BAR; PG8_SCHED;
	s_add_i32 s17, s17, s27
	v_lshl_add_u64 v[204:205], v[204:205], 0, s[8:9]
	s_mov_b32 m0, s17
	ds_read_b128 v[180:183], v146 offset:49152
	ds_read_b128 v[184:187], v146 offset:50176
	ds_read_b128 v[188:191], v146 offset:51200
	ds_read_b128 v[192:195], v146 offset:52224
	ds_read_b128 v[196:199], v146 offset:53248
	ds_read_b128 v[200:203], v146 offset:54272
	ds_read_b128 v[216:219], v146 offset:55296
	ds_read_b128 v[220:223], v146 offset:56320
	global_load_lds_dwordx4 v[204:205], off
	s_add_i32 m0, s17, 0x2000
	s_add_u32 s0, s0, 0x20080
	v_lshl_add_u64 v[204:205], v[208:209], 0, s[8:9]
	s_addc_u32 s1, s1, 0
	s_add_i32 s17, s20, s27
	global_load_lds_dwordx4 v[204:205], off
	v_lshl_add_u64 v[204:205], s[0:1], 0, v[132:133]
	s_mov_b32 m0, s17
	s_nop 0
	global_load_lds_dwordx4 v[204:205], off
	v_lshl_add_u64 v[204:205], s[0:1], 0, v[136:137]
	s_add_i32 m0, s17, 0x2000
	s_nop 0
	global_load_lds_dwordx4 v[204:205], off
	v_lshl_add_u64 v[204:205], v[210:211], 0, s[8:9]
	s_mov_b32 m0, s57
	s_nop 0
	global_load_lds_dwordx4 v[204:205], off
	v_lshl_add_u64 v[204:205], v[212:213], 0, s[8:9]
	s_mov_b32 m0, s58
	s_nop 0
	global_load_lds_dwordx4 v[204:205], off
	s_waitcnt vmcnt(8)
	s_waitcnt lgkmcnt(0)
	s_barrier
	s_setprio 1
	s_waitcnt lgkmcnt(0)
	v_mfma_f32_16x16x32_bf16 v[62:65], v[148:151], v[180:183], v[62:65]
	v_mfma_f32_16x16x32_bf16 v[58:61], v[156:159], v[180:183], v[58:61]
	v_mfma_f32_16x16x32_bf16 v[46:49], v[148:151], v[188:191], v[46:49]
	v_mfma_f32_16x16x32_bf16 v[42:45], v[156:159], v[188:191], v[42:45]
	v_mfma_f32_16x16x32_bf16 v[30:33], v[148:151], v[196:199], v[30:33]
	v_mfma_f32_16x16x32_bf16 v[26:29], v[156:159], v[196:199], v[26:29]
	v_mfma_f32_16x16x32_bf16 v[14:17], v[148:151], v[216:219], v[14:17]
	v_mfma_f32_16x16x32_bf16 v[10:13], v[156:159], v[216:219], v[10:13]
	v_mfma_f32_16x16x32_bf16 v[62:65], v[152:155], v[184:187], v[62:65]
	v_mfma_f32_16x16x32_bf16 v[58:61], v[160:163], v[184:187], v[58:61]
	v_mfma_f32_16x16x32_bf16 v[46:49], v[152:155], v[192:195], v[46:49]
	v_mfma_f32_16x16x32_bf16 v[42:45], v[160:163], v[192:195], v[42:45]
	v_mfma_f32_16x16x32_bf16 v[30:33], v[152:155], v[200:203], v[30:33]
	v_mfma_f32_16x16x32_bf16 v[26:29], v[160:163], v[200:203], v[26:29]
	v_mfma_f32_16x16x32_bf16 v[14:17], v[152:155], v[220:223], v[14:17]
	v_mfma_f32_16x16x32_bf16 v[10:13], v[160:163], v[220:223], v[10:13]
	v_mfma_f32_16x16x32_bf16 v[54:57], v[164:167], v[180:183], v[54:57]
	v_mfma_f32_16x16x32_bf16 v[50:53], v[172:175], v[180:183], v[50:53]
	v_mfma_f32_16x16x32_bf16 v[38:41], v[164:167], v[188:191], v[38:41]
	v_mfma_f32_16x16x32_bf16 v[34:37], v[172:175], v[188:191], v[34:37]
	v_mfma_f32_16x16x32_bf16 v[22:25], v[164:167], v[196:199], v[22:25]
	v_mfma_f32_16x16x32_bf16 v[18:21], v[172:175], v[196:199], v[18:21]
	v_mfma_f32_16x16x32_bf16 v[6:9], v[164:167], v[216:219], v[6:9]
	v_mfma_f32_16x16x32_bf16 v[2:5], v[172:175], v[216:219], v[2:5]
	v_mfma_f32_16x16x32_bf16 v[54:57], v[168:171], v[184:187], v[54:57]
	v_mfma_f32_16x16x32_bf16 v[50:53], v[176:179], v[184:187], v[50:53]
	v_mfma_f32_16x16x32_bf16 v[38:41], v[168:171], v[192:195], v[38:41]
	v_mfma_f32_16x16x32_bf16 v[34:37], v[176:179], v[192:195], v[34:37]
	v_mfma_f32_16x16x32_bf16 v[22:25], v[168:171], v[200:203], v[22:25]
	v_mfma_f32_16x16x32_bf16 v[18:21], v[176:179], v[200:203], v[18:21]
	v_mfma_f32_16x16x32_bf16 v[6:9], v[168:171], v[220:223], v[6:9]
	v_mfma_f32_16x16x32_bf16 v[2:5], v[176:179], v[220:223], v[2:5]
	s_setprio 0
	s_barrier
	s_add_i32 s16, s16, 2
	s_add_u32 s24, s24, 0x100
	s_addc_u32 s25, s25, 0
	s_add_u32 s14, s14, 0x100
	s_addc_u32 s15, s15, 0
	s_cmp_gt_u32 s16, 5
	s_cbranch_scc0 .LBB0_1318
	s_and_b64 vcc, exec, s[38:39]
	s_cbranch_vccz .LBB0_1321
	s_barrier

; #define PG8_STAGE(bufoff, gbase, voff) do { _Pragma("unroll") for (int _i = 0; _i < 2; ++_i) \
;         __builtin_amdgcn_global_load_lds((const unsigned*)((const char*)(gbase) + (voff)[_i]), (LAS unsigned*)(lds + (bufoff) + ldsw + _i * 8192), 16, 0, 0); } while (0)
; #define PG8_STAGE_A(bufoff, kptr, half, VO) do { if constexpr (GATHER) { _Pragma("unroll") for (int _i = 0; _i < 2; ++_i) \
;         __builtin_amdgcn_global_load_lds((const unsigned*)((const char*)(kptr) + (VO)[half][_i]), (LAS unsigned*)(lds + (bufoff) + ldsw + _i * 8192), 16, 0, 0); } \
;         else { PG8_STAGE(bufoff, (kptr) + (half) * hstepA, voffA); } } while (0)
; #define PG8_LDA(dst, b, h) do { _Pragma("unroll") for (int m = 0; m < 4; ++m) _Pragma("unroll") for (int k = 0; k < 2; ++k) dst[m][k] = *(const LAS bf16x8*)(lds + PG8_SA(b, h) + aoff + m * 2048 + k * 1024); } while (0)
; #define PG8_LDB(dst, b, h) do { _Pragma("unroll") for (int n = 0; n < 2; ++n) _Pragma("unroll") for (int k = 0; k < 2; ++k) dst[n][k] = *(const LAS bf16x8*)(lds + PG8_SB(b, h) + boff + n * 2048 + k * 1024); } while (0)
; #define PG8_WAIT_V(n) asm volatile("s_waitcnt vmcnt(" #n ")" ::: "memory")
; #define PG8_WAIT_L(n) asm volatile("s_waitcnt lgkmcnt(" #n ")" ::: "memory")
; #define PG8_BAR __builtin_amdgcn_s_barrier()
;     ...
;             const char* a1 = cA + (size_t)(t + 1) * kstep;
;             const char* a2 = last ? nA : cA + (size_t)(t + 2) * kstep; const char* b2 = last ? nB : cB + (size_t)(t + 2) * kstep;
;             const char* a3 = a2 + kstep; const char* b3 = b2 + kstep;
;             unsigned g2[2][2];
;             if constexpr (GATHER) {
; #pragma unroll
;                 for (int _h = 0; _h < 2; ++_h)
; #pragma unroll
;                     for (int _i = 0; _i < 2; ++_i) g2[_h][_i] = last ? gN[_h][_i] : gC[_h][_i]; }
;             if constexpr (SP2) {
;             PG8_LDB(B0, 0, 0); PG8_LDB(B1, 0, 1); PG8_SCHED; PG8_LDA(At, 0, 0); PG8_STAGE_A(PG8_SA(1, 1), a1, 1, gC);
;             PG8_WAIT_V(8); PG8_WAIT_L(0); PG8_BAR; PG8_MMA(0, 0, At, B0); PG8_MMA(0, 1, At, B1); PG8_BAR; PG8_SCHED;
;             PG8_LDA(At, 0, 1); PG8_STAGE(PG8_SB(0, 0), b2, voffB); PG8_STAGE(PG8_SB(0, 1), b2 + hstepB, voffB); PG8_STAGE_A(PG8_SA(0, 0), a2, 0, g2);
;             PG8_WAIT_V(8); PG8_WAIT_L(0); PG8_BAR; PG8_MMA(1, 0, At, B0); PG8_MMA(1, 1, At, B1); PG8_BAR; PG8_SCHED;
.LBB0_1443:
	s_add_u32 s0, s24, 0xfffe0080
	s_addc_u32 s1, s25, -1
	s_add_i32 s15, 0, 0x10000
	s_cmp_eq_u32 s14, 4
	s_cselect_b32 s31, s49, s1
	s_cselect_b32 s30, s48, s0
	s_cselect_b32 s1, s51, s13
	s_cselect_b32 s0, s50, s12
	s_add_i32 s18, 0, 0x14000
	v_add_u32_e32 v62, s15, v199
	v_add_u32_e32 v150, s18, v199
	ds_read_b128 v[38:41], v62
	ds_read_b128 v[46:49], v62 offset:1024
	ds_read_b128 v[54:57], v62 offset:2048
	ds_read_b128 v[62:65], v62 offset:3072
	ds_read_b128 v[122:125], v150
	ds_read_b128 v[130:133], v150 offset:1024
	ds_read_b128 v[142:145], v150 offset:2048
	ds_read_b128 v[150:153], v150 offset:3072
	v_lshl_add_u64 v[196:197], s[24:25], 0, v[180:181]
	s_add_i32 m0, s55, 0xc000
	ds_read_b128 v[154:157], v201
	ds_read_b128 v[158:161], v201 offset:1024
	ds_read_b128 v[166:169], v201 offset:2048
	ds_read_b128 v[184:187], v201 offset:3072
	ds_read_b128 v[188:191], v201 offset:4096
	ds_read_b128 v[192:195], v201 offset:5120
	ds_read_b128 v[202:205], v201 offset:6144
	ds_read_b128 v[216:219], v201 offset:7168
	global_load_lds_dwordx4 v[196:197], off
	v_lshl_add_u64 v[196:197], s[24:25], 0, v[182:183]
	s_add_i32 m0, s55, 0xe000
	s_nop 0
	global_load_lds_dwordx4 v[196:197], off
	s_waitcnt vmcnt(8)
	s_waitcnt lgkmcnt(0)
	s_barrier
	s_setprio 1
	s_waitcnt lgkmcnt(0)
	v_mfma_f32_16x16x32_bf16 v[170:173], v[38:41], v[154:157], v[170:173]
	v_mfma_f32_16x16x32_bf16 v[162:165], v[54:57], v[154:157], v[162:165]
	v_mfma_f32_16x16x32_bf16 v[134:137], v[38:41], v[166:169], v[134:137]
	v_mfma_f32_16x16x32_bf16 v[126:129], v[54:57], v[166:169], v[126:129]
	v_mfma_f32_16x16x32_bf16 v[110:113], v[38:41], v[188:191], v[110:113]
	v_mfma_f32_16x16x32_bf16 v[106:109], v[54:57], v[188:191], v[106:109]
	v_mfma_f32_16x16x32_bf16 v[94:97], v[38:41], v[202:205], v[94:97]
	v_mfma_f32_16x16x32_bf16 v[90:93], v[54:57], v[202:205], v[90:93]
	v_mfma_f32_16x16x32_bf16 v[170:173], v[46:49], v[158:161], v[170:173]
	v_mfma_f32_16x16x32_bf16 v[162:165], v[62:65], v[158:161], v[162:165]
	v_mfma_f32_16x16x32_bf16 v[134:137], v[46:49], v[184:187], v[134:137]
	v_mfma_f32_16x16x32_bf16 v[126:129], v[62:65], v[184:187], v[126:129]
	v_mfma_f32_16x16x32_bf16 v[110:113], v[46:49], v[192:195], v[110:113]
	v_mfma_f32_16x16x32_bf16 v[106:109], v[62:65], v[192:195], v[106:109]
	v_mfma_f32_16x16x32_bf16 v[94:97], v[46:49], v[216:219], v[94:97]
	v_mfma_f32_16x16x32_bf16 v[90:93], v[62:65], v[216:219], v[90:93]
	v_mfma_f32_16x16x32_bf16 v[146:149], v[122:125], v[154:157], v[146:149]
	v_mfma_f32_16x16x32_bf16 v[138:141], v[142:145], v[154:157], v[138:141]
	v_mfma_f32_16x16x32_bf16 v[118:121], v[122:125], v[166:169], v[118:121]
	v_mfma_f32_16x16x32_bf16 v[114:117], v[142:145], v[166:169], v[114:117]
	v_mfma_f32_16x16x32_bf16 v[102:105], v[122:125], v[188:191], v[102:105]
	v_mfma_f32_16x16x32_bf16 v[98:101], v[142:145], v[188:191], v[98:101]
	v_mfma_f32_16x16x32_bf16 v[86:89], v[122:125], v[202:205], v[86:89]
	v_mfma_f32_16x16x32_bf16 v[82:85], v[142:145], v[202:205], v[82:85]
	v_mfma_f32_16x16x32_bf16 v[146:149], v[130:133], v[158:161], v[146:149]
	v_mfma_f32_16x16x32_bf16 v[138:141], v[150:153], v[158:161], v[138:141]
	v_mfma_f32_16x16x32_bf16 v[118:121], v[130:133], v[184:187], v[118:121]
	v_mfma_f32_16x16x32_bf16 v[114:117], v[150:153], v[184:187], v[114:117]
	v_mfma_f32_16x16x32_bf16 v[102:105], v[130:133], v[192:195], v[102:105]
	v_mfma_f32_16x16x32_bf16 v[98:101], v[150:153], v[192:195], v[98:101]
	v_mfma_f32_16x16x32_bf16 v[86:89], v[130:133], v[216:219], v[86:89]
	v_mfma_f32_16x16x32_bf16 v[82:85], v[150:153], v[216:219], v[82:85]
	s_setprio 0
	s_barrier
	s_add_i32 s15, s15, s57
	v_lshl_add_u64 v[196:197], s[0:1], 0, v[206:207]
	s_mov_b32 m0, s15
	ds_read_b128 v[154:157], v201 offset:16384
	ds_read_b128 v[158:161], v201 offset:17408
	ds_read_b128 v[166:169], v201 offset:18432
	ds_read_b128 v[184:187], v201 offset:19456
	ds_read_b128 v[188:191], v201 offset:20480
	ds_read_b128 v[192:195], v201 offset:21504
	ds_read_b128 v[202:205], v201 offset:22528
	ds_read_b128 v[216:219], v201 offset:23552
	global_load_lds_dwordx4 v[196:197], off
	s_add_i32 m0, s15, 0x2000
	s_add_u32 s16, s0, 0x20000
	v_lshl_add_u64 v[208:209], s[0:1], 0, v[174:175]
	s_addc_u32 s17, s1, 0
	s_add_i32 s15, s18, s57
	global_load_lds_dwordx4 v[208:209], off
	v_lshl_add_u64 v[210:211], s[16:17], 0, v[206:207]
	s_mov_b32 m0, s15
	v_lshl_add_u64 v[212:213], s[30:31], 0, v[176:177]
	global_load_lds_dwordx4 v[210:211], off
	v_lshl_add_u64 v[210:211], s[16:17], 0, v[174:175]
	s_add_i32 m0, s15, 0x2000
	s_nop 0
	global_load_lds_dwordx4 v[210:211], off
	v_lshl_add_u64 v[210:211], s[30:31], 0, v[178:179]
	s_mov_b32 m0, s55
	s_nop 0
	global_load_lds_dwordx4 v[210:211], off
	s_mov_b32 m0, s63
	s_nop 0
	global_load_lds_dwordx4 v[212:213], off
	s_waitcnt vmcnt(8)
	s_waitcnt lgkmcnt(0)
	s_barrier
; #define PG8_STAGE_A(bufoff, kptr, half, VO) do { if constexpr (GATHER) { _Pragma("unroll") for (int _i = 0; _i < 2; ++_i) \
;         __builtin_amdgcn_global_load_lds((const unsigned*)((const char*)(kptr) + (VO)[half][_i]), (LAS unsigned*)(lds + (bufoff) + ldsw + _i * 8192), 16, 0, 0); } \
;         else { PG8_STAGE(bufoff, (kptr) + (half) * hstepA, voffA); } } while (0)
; #define PG8_LDA(dst, b, h) do { _Pragma("unroll") for (int m = 0; m < 4; ++m) _Pragma("unroll") for (int k = 0; k < 2; ++k) dst[m][k] = *(const LAS bf16x8*)(lds + PG8_SA(b, h) + aoff + m * 2048 + k * 1024); } while (0)
; #define PG8_LDB(dst, b, h) do { _Pragma("unroll") for (int n = 0; n < 2; ++n) _Pragma("unroll") for (int k = 0; k < 2; ++k) dst[n][k] = *(const LAS bf16x8*)(lds + PG8_SB(b, h) + boff + n * 2048 + k * 1024); } while (0)
; #define PG8_MMA(ai, bj, At, Bt) do { __builtin_amdgcn_s_setprio(1); _Pragma("unroll") for (int m = 0; m < 4; ++m) _Pragma("unroll") for (int n = 0; n < 2; ++n) _Pragma("unroll") for (int k = 0; k < 2; ++k) \
;         acc[ai][bj][m][n] = __builtin_amdgcn_mfma_f32_16x16x32_bf16(Bt[n][k], At[m][k], acc[ai][bj][m][n], 0, 0, 0); __builtin_amdgcn_s_setprio(0); } while (0)
; #define PG8_WAIT_V(n) asm volatile("s_waitcnt vmcnt(" #n ")" ::: "memory")
; #define PG8_WAIT_L(n) asm volatile("s_waitcnt lgkmcnt(" #n ")" ::: "memory")
; #define PG8_BAR __builtin_amdgcn_s_barrier()
; #define PG8_SCHED __builtin_amdgcn_sched_barrier(0)
;     ...
;             PG8_WAIT_V(8); PG8_WAIT_L(0); PG8_BAR; PG8_MMA(1, 0, At, B0); PG8_MMA(1, 1, At, B1); PG8_BAR; PG8_SCHED;
;             PG8_LDB(B0, 1, 0); PG8_LDB(B1, 1, 1); PG8_SCHED; PG8_LDA(At, 1, 0); PG8_STAGE_A(PG8_SA(0, 1), a2, 1, g2);
;             PG8_WAIT_V(8); PG8_WAIT_L(0); PG8_BAR; PG8_MMA(0, 0, At, B0); PG8_MMA(0, 1, At, B1); PG8_BAR; PG8_SCHED;
	s_setprio 1
	s_waitcnt lgkmcnt(0)
	v_mfma_f32_16x16x32_bf16 v[78:81], v[38:41], v[154:157], v[78:81]
	v_mfma_f32_16x16x32_bf16 v[74:77], v[54:57], v[154:157], v[74:77]
	v_mfma_f32_16x16x32_bf16 v[58:61], v[38:41], v[166:169], v[58:61]
	v_mfma_f32_16x16x32_bf16 v[50:53], v[54:57], v[166:169], v[50:53]
	v_mfma_f32_16x16x32_bf16 v[30:33], v[38:41], v[188:191], v[30:33]
	v_mfma_f32_16x16x32_bf16 v[26:29], v[54:57], v[188:191], v[26:29]
	v_mfma_f32_16x16x32_bf16 v[14:17], v[38:41], v[202:205], v[14:17]
	v_mfma_f32_16x16x32_bf16 v[10:13], v[54:57], v[202:205], v[10:13]
	v_mfma_f32_16x16x32_bf16 v[78:81], v[46:49], v[158:161], v[78:81]
	v_mfma_f32_16x16x32_bf16 v[74:77], v[62:65], v[158:161], v[74:77]
	v_mfma_f32_16x16x32_bf16 v[58:61], v[46:49], v[184:187], v[58:61]
	v_mfma_f32_16x16x32_bf16 v[50:53], v[62:65], v[184:187], v[50:53]
	v_mfma_f32_16x16x32_bf16 v[30:33], v[46:49], v[192:195], v[30:33]
	v_mfma_f32_16x16x32_bf16 v[26:29], v[62:65], v[192:195], v[26:29]
	v_mfma_f32_16x16x32_bf16 v[14:17], v[46:49], v[216:219], v[14:17]
	v_mfma_f32_16x16x32_bf16 v[10:13], v[62:65], v[216:219], v[10:13]
	v_mfma_f32_16x16x32_bf16 v[42:45], v[122:125], v[166:169], v[42:45]
	v_mfma_f32_16x16x32_bf16 v[34:37], v[142:145], v[166:169], v[34:37]
	v_mfma_f32_16x16x32_bf16 v[22:25], v[122:125], v[188:191], v[22:25]
	v_mfma_f32_16x16x32_bf16 v[18:21], v[142:145], v[188:191], v[18:21]
	v_mfma_f32_16x16x32_bf16 v[6:9], v[122:125], v[202:205], v[6:9]
	v_mfma_f32_16x16x32_bf16 v[2:5], v[142:145], v[202:205], v[2:5]
	v_mfma_f32_16x16x32_bf16 v[38:41], v[122:125], v[154:157], v[70:73]
	v_mfma_f32_16x16x32_bf16 v[46:49], v[142:145], v[154:157], v[66:69]
	v_mfma_f32_16x16x32_bf16 v[42:45], v[130:133], v[184:187], v[42:45]
	v_mfma_f32_16x16x32_bf16 v[34:37], v[150:153], v[184:187], v[34:37]
	v_mfma_f32_16x16x32_bf16 v[22:25], v[130:133], v[192:195], v[22:25]
	v_mfma_f32_16x16x32_bf16 v[18:21], v[150:153], v[192:195], v[18:21]
	v_mfma_f32_16x16x32_bf16 v[6:9], v[130:133], v[216:219], v[6:9]
	v_mfma_f32_16x16x32_bf16 v[2:5], v[150:153], v[216:219], v[2:5]
	v_mfma_f32_16x16x32_bf16 v[38:41], v[130:133], v[158:161], v[38:41]
	v_mfma_f32_16x16x32_bf16 v[46:49], v[150:153], v[158:161], v[46:49]
	s_setprio 0
	s_barrier
	s_add_i32 s15, 0, 0x18000
	s_add_i32 s18, 0, 0x1c000
	v_add_u32_e32 v70, s15, v199
	v_add_u32_e32 v150, s18, v199
	ds_read_b128 v[54:57], v70
	ds_read_b128 v[62:65], v70 offset:1024
	ds_read_b128 v[66:69], v70 offset:2048
	ds_read_b128 v[70:73], v70 offset:3072
	ds_read_b128 v[122:125], v150
	ds_read_b128 v[130:133], v150 offset:1024
	ds_read_b128 v[142:145], v150 offset:2048
	ds_read_b128 v[150:153], v150 offset:3072
	s_add_u32 s16, s30, 0x20000
	s_addc_u32 s17, s31, 0
	s_mov_b32 m0, s64
	v_lshl_add_u64 v[220:221], s[16:17], 0, v[178:179]
	ds_read_b128 v[154:157], v201 offset:32768
	ds_read_b128 v[158:161], v201 offset:33792
	ds_read_b128 v[166:169], v201 offset:34816
	ds_read_b128 v[184:187], v201 offset:35840
	ds_read_b128 v[188:191], v201 offset:36864
	ds_read_b128 v[192:195], v201 offset:37888
	ds_read_b128 v[202:205], v201 offset:38912
	ds_read_b128 v[216:219], v201 offset:39936
	global_load_lds_dwordx4 v[220:221], off
	v_lshl_add_u64 v[220:221], s[16:17], 0, v[176:177]
	s_mov_b32 m0, s65
	s_nop 0
	global_load_lds_dwordx4 v[220:221], off
	s_waitcnt vmcnt(8)
	s_waitcnt lgkmcnt(0)
	s_barrier
	s_setprio 1
	s_waitcnt lgkmcnt(0)
	v_mfma_f32_16x16x32_bf16 v[170:173], v[54:57], v[154:157], v[170:173]
	v_mfma_f32_16x16x32_bf16 v[162:165], v[66:69], v[154:157], v[162:165]
	v_mfma_f32_16x16x32_bf16 v[134:137], v[54:57], v[166:169], v[134:137]
	v_mfma_f32_16x16x32_bf16 v[126:129], v[66:69], v[166:169], v[126:129]
	v_mfma_f32_16x16x32_bf16 v[110:113], v[54:57], v[188:191], v[110:113]
	v_mfma_f32_16x16x32_bf16 v[106:109], v[66:69], v[188:191], v[106:109]
	v_mfma_f32_16x16x32_bf16 v[94:97], v[54:57], v[202:205], v[94:97]
	v_mfma_f32_16x16x32_bf16 v[90:93], v[66:69], v[202:205], v[90:93]
	v_mfma_f32_16x16x32_bf16 v[170:173], v[62:65], v[158:161], v[170:173]
	v_mfma_f32_16x16x32_bf16 v[162:165], v[70:73], v[158:161], v[162:165]
	v_mfma_f32_16x16x32_bf16 v[134:137], v[62:65], v[184:187], v[134:137]
	v_mfma_f32_16x16x32_bf16 v[126:129], v[70:73], v[184:187], v[126:129]
	v_mfma_f32_16x16x32_bf16 v[110:113], v[62:65], v[192:195], v[110:113]
	v_mfma_f32_16x16x32_bf16 v[106:109], v[70:73], v[192:195], v[106:109]
	v_mfma_f32_16x16x32_bf16 v[94:97], v[62:65], v[216:219], v[94:97]
	v_mfma_f32_16x16x32_bf16 v[90:93], v[70:73], v[216:219], v[90:93]
	v_mfma_f32_16x16x32_bf16 v[146:149], v[122:125], v[154:157], v[146:149]
	v_mfma_f32_16x16x32_bf16 v[138:141], v[142:145], v[154:157], v[138:141]
	v_mfma_f32_16x16x32_bf16 v[118:121], v[122:125], v[166:169], v[118:121]
	v_mfma_f32_16x16x32_bf16 v[114:117], v[142:145], v[166:169], v[114:117]
	v_mfma_f32_16x16x32_bf16 v[102:105], v[122:125], v[188:191], v[102:105]
	v_mfma_f32_16x16x32_bf16 v[98:101], v[142:145], v[188:191], v[98:101]
	v_mfma_f32_16x16x32_bf16 v[86:89], v[122:125], v[202:205], v[86:89]
	v_mfma_f32_16x16x32_bf16 v[82:85], v[142:145], v[202:205], v[82:85]
	v_mfma_f32_16x16x32_bf16 v[146:149], v[130:133], v[158:161], v[146:149]
	v_mfma_f32_16x16x32_bf16 v[138:141], v[150:153], v[158:161], v[138:141]
	v_mfma_f32_16x16x32_bf16 v[118:121], v[130:133], v[184:187], v[118:121]
	v_mfma_f32_16x16x32_bf16 v[114:117], v[150:153], v[184:187], v[114:117]
	v_mfma_f32_16x16x32_bf16 v[102:105], v[130:133], v[192:195], v[102:105]
	v_mfma_f32_16x16x32_bf16 v[98:101], v[150:153], v[192:195], v[98:101]
	v_mfma_f32_16x16x32_bf16 v[86:89], v[130:133], v[216:219], v[86:89]
	v_mfma_f32_16x16x32_bf16 v[82:85], v[150:153], v[216:219], v[82:85]
	s_setprio 0
	s_barrier
; #define PG8_STAGE(bufoff, gbase, voff) do { _Pragma("unroll") for (int _i = 0; _i < 2; ++_i) \
;         __builtin_amdgcn_global_load_lds((const unsigned*)((const char*)(gbase) + (voff)[_i]), (LAS unsigned*)(lds + (bufoff) + ldsw + _i * 8192), 16, 0, 0); } while (0)
; #define PG8_STAGE_A(bufoff, kptr, half, VO) do { if constexpr (GATHER) { _Pragma("unroll") for (int _i = 0; _i < 2; ++_i) \
;         __builtin_amdgcn_global_load_lds((const unsigned*)((const char*)(kptr) + (VO)[half][_i]), (LAS unsigned*)(lds + (bufoff) + ldsw + _i * 8192), 16, 0, 0); } \
;         else { PG8_STAGE(bufoff, (kptr) + (half) * hstepA, voffA); } } while (0)
; #define PG8_LDA(dst, b, h) do { _Pragma("unroll") for (int m = 0; m < 4; ++m) _Pragma("unroll") for (int k = 0; k < 2; ++k) dst[m][k] = *(const LAS bf16x8*)(lds + PG8_SA(b, h) + aoff + m * 2048 + k * 1024); } while (0)
; #define PG8_MMA(ai, bj, At, Bt) do { __builtin_amdgcn_s_setprio(1); _Pragma("unroll") for (int m = 0; m < 4; ++m) _Pragma("unroll") for (int n = 0; n < 2; ++n) _Pragma("unroll") for (int k = 0; k < 2; ++k) \
;         acc[ai][bj][m][n] = __builtin_amdgcn_mfma_f32_16x16x32_bf16(Bt[n][k], At[m][k], acc[ai][bj][m][n], 0, 0, 0); __builtin_amdgcn_s_setprio(0); } while (0)
; #define PG8_WAIT_V(n) asm volatile("s_waitcnt vmcnt(" #n ")" ::: "memory")
; #define PG8_WAIT_L(n) asm volatile("s_waitcnt lgkmcnt(" #n ")" ::: "memory")
; #define PG8_BAR __builtin_amdgcn_s_barrier()
; #define PG8_SCHED __builtin_amdgcn_sched_barrier(0)
;     ...
;             PG8_LDA(At, 1, 1); PG8_STAGE(PG8_SB(1, 0), b3, voffB); PG8_STAGE(PG8_SB(1, 1), b3 + hstepB, voffB); PG8_STAGE_A(PG8_SA(1, 0), a3, 0, g2);
;             PG8_WAIT_V(8); PG8_WAIT_L(0); PG8_BAR; PG8_MMA(1, 0, At, B0); PG8_MMA(1, 1, At, B1); PG8_BAR; PG8_SCHED;
	s_add_i32 s15, s15, s57
	v_lshl_add_u64 v[196:197], v[196:197], 0, s[8:9]
	s_mov_b32 m0, s15
	ds_read_b128 v[154:157], v201 offset:49152
	ds_read_b128 v[158:161], v201 offset:50176
	ds_read_b128 v[166:169], v201 offset:51200
	ds_read_b128 v[184:187], v201 offset:52224
	ds_read_b128 v[188:191], v201 offset:53248
	ds_read_b128 v[192:195], v201 offset:54272
	ds_read_b128 v[202:205], v201 offset:55296
	ds_read_b128 v[216:219], v201 offset:56320
	global_load_lds_dwordx4 v[196:197], off
	s_add_i32 m0, s15, 0x2000
	s_add_u32 s0, s0, 0x20080
	v_lshl_add_u64 v[196:197], v[208:209], 0, s[8:9]
	s_addc_u32 s1, s1, 0
	s_add_i32 s15, s18, s57
	global_load_lds_dwordx4 v[196:197], off
	v_lshl_add_u64 v[196:197], s[0:1], 0, v[206:207]
	s_mov_b32 m0, s15
	s_nop 0
	global_load_lds_dwordx4 v[196:197], off
	v_lshl_add_u64 v[196:197], s[0:1], 0, v[174:175]
	s_add_i32 m0, s15, 0x2000
	s_nop 0
	global_load_lds_dwordx4 v[196:197], off
	v_lshl_add_u64 v[196:197], v[210:211], 0, s[8:9]
	s_mov_b32 m0, s4
	s_nop 0
	global_load_lds_dwordx4 v[196:197], off
	v_lshl_add_u64 v[196:197], v[212:213], 0, s[8:9]
	s_mov_b32 m0, s66
	s_nop 0
	global_load_lds_dwordx4 v[196:197], off
	s_waitcnt vmcnt(8)
	s_waitcnt lgkmcnt(0)
	s_barrier
	s_setprio 1
	s_waitcnt lgkmcnt(0)
	v_mfma_f32_16x16x32_bf16 v[78:81], v[54:57], v[154:157], v[78:81]
	v_mfma_f32_16x16x32_bf16 v[74:77], v[66:69], v[154:157], v[74:77]
	v_mfma_f32_16x16x32_bf16 v[58:61], v[54:57], v[166:169], v[58:61]
	v_mfma_f32_16x16x32_bf16 v[50:53], v[66:69], v[166:169], v[50:53]
	v_mfma_f32_16x16x32_bf16 v[30:33], v[54:57], v[188:191], v[30:33]
	v_mfma_f32_16x16x32_bf16 v[26:29], v[66:69], v[188:191], v[26:29]
	v_mfma_f32_16x16x32_bf16 v[14:17], v[54:57], v[202:205], v[14:17]
	v_mfma_f32_16x16x32_bf16 v[10:13], v[66:69], v[202:205], v[10:13]
	v_mfma_f32_16x16x32_bf16 v[78:81], v[62:65], v[158:161], v[78:81]
	v_mfma_f32_16x16x32_bf16 v[74:77], v[70:73], v[158:161], v[74:77]
	v_mfma_f32_16x16x32_bf16 v[58:61], v[62:65], v[184:187], v[58:61]
	v_mfma_f32_16x16x32_bf16 v[50:53], v[70:73], v[184:187], v[50:53]
	v_mfma_f32_16x16x32_bf16 v[30:33], v[62:65], v[192:195], v[30:33]
	v_mfma_f32_16x16x32_bf16 v[26:29], v[70:73], v[192:195], v[26:29]
	v_mfma_f32_16x16x32_bf16 v[14:17], v[62:65], v[216:219], v[14:17]
	v_mfma_f32_16x16x32_bf16 v[10:13], v[70:73], v[216:219], v[10:13]
	v_mfma_f32_16x16x32_bf16 v[38:41], v[122:125], v[154:157], v[38:41]
	v_mfma_f32_16x16x32_bf16 v[70:73], v[130:133], v[158:161], v[38:41]
	v_mfma_f32_16x16x32_bf16 v[38:41], v[142:145], v[154:157], v[46:49]
	v_mfma_f32_16x16x32_bf16 v[66:69], v[150:153], v[158:161], v[38:41]
	v_mfma_f32_16x16x32_bf16 v[38:41], v[122:125], v[166:169], v[42:45]
	v_mfma_f32_16x16x32_bf16 v[34:37], v[142:145], v[166:169], v[34:37]
	v_mfma_f32_16x16x32_bf16 v[22:25], v[122:125], v[188:191], v[22:25]
	v_mfma_f32_16x16x32_bf16 v[18:21], v[142:145], v[188:191], v[18:21]
	v_mfma_f32_16x16x32_bf16 v[6:9], v[122:125], v[202:205], v[6:9]
	v_mfma_f32_16x16x32_bf16 v[2:5], v[142:145], v[202:205], v[2:5]
	v_mfma_f32_16x16x32_bf16 v[42:45], v[130:133], v[184:187], v[38:41]
	v_mfma_f32_16x16x32_bf16 v[34:37], v[150:153], v[184:187], v[34:37]
	v_mfma_f32_16x16x32_bf16 v[22:25], v[130:133], v[192:195], v[22:25]
	v_mfma_f32_16x16x32_bf16 v[18:21], v[150:153], v[192:195], v[18:21]
	v_mfma_f32_16x16x32_bf16 v[6:9], v[130:133], v[216:219], v[6:9]
	v_mfma_f32_16x16x32_bf16 v[2:5], v[150:153], v[216:219], v[2:5]
	s_setprio 0
	s_barrier
	s_add_i32 s14, s14, 2
	s_add_u32 s24, s24, 0x100
	s_addc_u32 s25, s25, 0
	s_add_u32 s12, s12, 0x100
	s_addc_u32 s13, s13, 0
	s_cmp_gt_u32 s14, 5
	s_cbranch_scc0 .LBB0_1443
	s_and_b64 vcc, exec, s[42:43]
	s_cbranch_vccz .LBB0_1446
	s_barrier

; #define PG8_STAGE(bufoff, gbase, voff) do { _Pragma("unroll") for (int _i = 0; _i < 2; ++_i) \
;         __builtin_amdgcn_global_load_lds((const unsigned*)((const char*)(gbase) + (voff)[_i]), (LAS unsigned*)(lds + (bufoff) + ldsw + _i * 8192), 16, 0, 0); } while (0)
; #define PG8_STAGE_A(bufoff, kptr, half, VO) do { if constexpr (GATHER) { _Pragma("unroll") for (int _i = 0; _i < 2; ++_i) \
;         __builtin_amdgcn_global_load_lds((const unsigned*)((const char*)(kptr) + (VO)[half][_i]), (LAS unsigned*)(lds + (bufoff) + ldsw + _i * 8192), 16, 0, 0); } \
;         else { PG8_STAGE(bufoff, (kptr) + (half) * hstepA, voffA); } } while (0)
; #define PG8_LDA(dst, b, h) do { _Pragma("unroll") for (int m = 0; m < 4; ++m) _Pragma("unroll") for (int k = 0; k < 2; ++k) dst[m][k] = *(const LAS bf16x8*)(lds + PG8_SA(b, h) + aoff + m * 2048 + k * 1024); } while (0)
; #define PG8_LDB(dst, b, h) do { _Pragma("unroll") for (int n = 0; n < 2; ++n) _Pragma("unroll") for (int k = 0; k < 2; ++k) dst[n][k] = *(const LAS bf16x8*)(lds + PG8_SB(b, h) + boff + n * 2048 + k * 1024); } while (0)
; #define PG8_WAIT_V(n) asm volatile("s_waitcnt vmcnt(" #n ")" ::: "memory")
; #define PG8_WAIT_L(n) asm volatile("s_waitcnt lgkmcnt(" #n ")" ::: "memory")
; #define PG8_BAR __builtin_amdgcn_s_barrier()
;     ...
;             const char* a1 = cA + (size_t)(t + 1) * kstep;
;             const char* a2 = last ? nA : cA + (size_t)(t + 2) * kstep; const char* b2 = last ? nB : cB + (size_t)(t + 2) * kstep;
;             const char* a3 = a2 + kstep; const char* b3 = b2 + kstep;
;             unsigned g2[2][2];
;             if constexpr (GATHER) {
; #pragma unroll
;                 for (int _h = 0; _h < 2; ++_h)
; #pragma unroll
;                     for (int _i = 0; _i < 2; ++_i) g2[_h][_i] = last ? gN[_h][_i] : gC[_h][_i]; }
;             if constexpr (SP2) {
;             PG8_LDB(B0, 0, 0); PG8_LDB(B1, 0, 1); PG8_SCHED; PG8_LDA(At, 0, 0); PG8_STAGE_A(PG8_SA(1, 1), a1, 1, gC);
;             PG8_WAIT_V(8); PG8_WAIT_L(0); PG8_BAR; PG8_MMA(0, 0, At, B0); PG8_MMA(0, 1, At, B1); PG8_BAR; PG8_SCHED;
;             PG8_LDA(At, 0, 1); PG8_STAGE(PG8_SB(0, 0), b2, voffB); PG8_STAGE(PG8_SB(0, 1), b2 + hstepB, voffB); PG8_STAGE_A(PG8_SA(0, 0), a2, 0, g2);
;             PG8_WAIT_V(8); PG8_WAIT_L(0); PG8_BAR; PG8_MMA(1, 0, At, B0); PG8_MMA(1, 1, At, B1); PG8_BAR; PG8_SCHED;
.LBB0_1669:
	s_add_u32 s0, s24, 0xfff80080
	s_addc_u32 s1, s25, -1
	s_add_i32 s15, 0, 0x10000
	s_cmp_eq_u32 s14, 28
	s_cselect_b32 s31, s45, s1
	s_cselect_b32 s30, s44, s0
	v_add_u32_e32 v158, s15, v161
	s_cselect_b32 s1, s47, s13
	s_cselect_b32 s0, s46, s12
	s_add_i32 s18, 0, 0x14000
	ds_read_b128 v[164:167], v158
	ds_read_b128 v[168:171], v158 offset:1024
	ds_read_b128 v[172:175], v158 offset:2048
	ds_read_b128 v[176:179], v158 offset:3072
	v_add_u32_e32 v158, s18, v161
	ds_read_b128 v[180:183], v158
	ds_read_b128 v[184:187], v158 offset:1024
	ds_read_b128 v[188:191], v158 offset:2048
	ds_read_b128 v[192:195], v158 offset:3072
	v_lshl_add_u64 v[158:159], s[24:25], 0, v[154:155]
	s_add_i32 m0, s49, 0xc000
	ds_read_b128 v[196:199], v163
	ds_read_b128 v[200:203], v163 offset:1024
	ds_read_b128 v[216:219], v163 offset:2048
	ds_read_b128 v[220:223], v163 offset:3072
	ds_read_b128 v[224:227], v163 offset:4096
	ds_read_b128 v[228:231], v163 offset:5120
	ds_read_b128 v[232:235], v163 offset:6144
	ds_read_b128 v[236:239], v163 offset:7168
	global_load_lds_dwordx4 v[158:159], off
	v_lshl_add_u64 v[158:159], s[24:25], 0, v[156:157]
	s_add_i32 m0, s49, 0xe000
	s_nop 0
	global_load_lds_dwordx4 v[158:159], off
	s_waitcnt vmcnt(8)
	s_waitcnt lgkmcnt(0)
	s_barrier
	s_setprio 1
	s_waitcnt lgkmcnt(0)
	v_mfma_f32_16x16x32_bf16 v[126:129], v[164:167], v[196:199], v[126:129]
	v_mfma_f32_16x16x32_bf16 v[122:125], v[172:175], v[196:199], v[122:125]
	v_mfma_f32_16x16x32_bf16 v[118:121], v[164:167], v[216:219], v[118:121]
	v_mfma_f32_16x16x32_bf16 v[114:117], v[172:175], v[216:219], v[114:117]
	v_mfma_f32_16x16x32_bf16 v[102:105], v[164:167], v[224:227], v[102:105]
	v_mfma_f32_16x16x32_bf16 v[98:101], v[172:175], v[224:227], v[98:101]
	v_mfma_f32_16x16x32_bf16 v[86:89], v[164:167], v[232:235], v[86:89]
	v_mfma_f32_16x16x32_bf16 v[82:85], v[172:175], v[232:235], v[82:85]
	v_mfma_f32_16x16x32_bf16 v[126:129], v[168:171], v[200:203], v[126:129]
	v_mfma_f32_16x16x32_bf16 v[122:125], v[176:179], v[200:203], v[122:125]
	v_mfma_f32_16x16x32_bf16 v[118:121], v[168:171], v[220:223], v[118:121]
	v_mfma_f32_16x16x32_bf16 v[114:117], v[176:179], v[220:223], v[114:117]
	v_mfma_f32_16x16x32_bf16 v[102:105], v[168:171], v[228:231], v[102:105]
	v_mfma_f32_16x16x32_bf16 v[98:101], v[176:179], v[228:231], v[98:101]
	v_mfma_f32_16x16x32_bf16 v[86:89], v[168:171], v[236:239], v[86:89]
	v_mfma_f32_16x16x32_bf16 v[82:85], v[176:179], v[236:239], v[82:85]
	v_mfma_f32_16x16x32_bf16 v[110:113], v[180:183], v[196:199], v[110:113]
	v_mfma_f32_16x16x32_bf16 v[106:109], v[188:191], v[196:199], v[106:109]
	v_mfma_f32_16x16x32_bf16 v[94:97], v[180:183], v[216:219], v[94:97]
	v_mfma_f32_16x16x32_bf16 v[90:93], v[188:191], v[216:219], v[90:93]
	v_mfma_f32_16x16x32_bf16 v[78:81], v[180:183], v[224:227], v[78:81]
	v_mfma_f32_16x16x32_bf16 v[74:77], v[188:191], v[224:227], v[74:77]
	v_mfma_f32_16x16x32_bf16 v[70:73], v[180:183], v[232:235], v[70:73]
	v_mfma_f32_16x16x32_bf16 v[66:69], v[188:191], v[232:235], v[66:69]
	v_mfma_f32_16x16x32_bf16 v[110:113], v[184:187], v[200:203], v[110:113]
	v_mfma_f32_16x16x32_bf16 v[106:109], v[192:195], v[200:203], v[106:109]
	v_mfma_f32_16x16x32_bf16 v[94:97], v[184:187], v[220:223], v[94:97]
	v_mfma_f32_16x16x32_bf16 v[90:93], v[192:195], v[220:223], v[90:93]
	v_mfma_f32_16x16x32_bf16 v[78:81], v[184:187], v[228:231], v[78:81]
	v_mfma_f32_16x16x32_bf16 v[74:77], v[192:195], v[228:231], v[74:77]
	v_mfma_f32_16x16x32_bf16 v[70:73], v[184:187], v[236:239], v[70:73]
	v_mfma_f32_16x16x32_bf16 v[66:69], v[192:195], v[236:239], v[66:69]
	s_setprio 0
	s_barrier
	s_add_i32 s15, s15, s52
	v_lshl_add_u64 v[158:159], s[0:1], 0, v[206:207]
	s_mov_b32 m0, s15
	ds_read_b128 v[196:199], v163 offset:16384
	ds_read_b128 v[200:203], v163 offset:17408
	ds_read_b128 v[216:219], v163 offset:18432
	ds_read_b128 v[220:223], v163 offset:19456
	ds_read_b128 v[224:227], v163 offset:20480
	ds_read_b128 v[228:231], v163 offset:21504
	ds_read_b128 v[232:235], v163 offset:22528
	ds_read_b128 v[236:239], v163 offset:23552
	global_load_lds_dwordx4 v[158:159], off
	s_add_i32 m0, s15, 0x2000
	s_add_u32 s16, s0, 0x80000
	v_lshl_add_u64 v[204:205], s[0:1], 0, v[130:131]
	s_addc_u32 s17, s1, 0
	s_add_i32 s15, s18, s52
	global_load_lds_dwordx4 v[204:205], off
	v_lshl_add_u64 v[208:209], s[16:17], 0, v[206:207]
	s_mov_b32 m0, s15
	v_lshl_add_u64 v[210:211], s[30:31], 0, v[132:133]
	global_load_lds_dwordx4 v[208:209], off
	v_lshl_add_u64 v[208:209], s[16:17], 0, v[130:131]
	s_add_i32 m0, s15, 0x2000
	s_nop 0
	global_load_lds_dwordx4 v[208:209], off
	v_lshl_add_u64 v[208:209], s[30:31], 0, v[134:135]
	s_mov_b32 m0, s49
	s_nop 0
	global_load_lds_dwordx4 v[208:209], off
	s_mov_b32 m0, s53
	s_nop 0
	global_load_lds_dwordx4 v[210:211], off
	s_waitcnt vmcnt(8)
	s_waitcnt lgkmcnt(0)
	s_barrier
; #define PG8_STAGE_A(bufoff, kptr, half, VO) do { if constexpr (GATHER) { _Pragma("unroll") for (int _i = 0; _i < 2; ++_i) \
;         __builtin_amdgcn_global_load_lds((const unsigned*)((const char*)(kptr) + (VO)[half][_i]), (LAS unsigned*)(lds + (bufoff) + ldsw + _i * 8192), 16, 0, 0); } \
;         else { PG8_STAGE(bufoff, (kptr) + (half) * hstepA, voffA); } } while (0)
; #define PG8_LDA(dst, b, h) do { _Pragma("unroll") for (int m = 0; m < 4; ++m) _Pragma("unroll") for (int k = 0; k < 2; ++k) dst[m][k] = *(const LAS bf16x8*)(lds + PG8_SA(b, h) + aoff + m * 2048 + k * 1024); } while (0)
; #define PG8_LDB(dst, b, h) do { _Pragma("unroll") for (int n = 0; n < 2; ++n) _Pragma("unroll") for (int k = 0; k < 2; ++k) dst[n][k] = *(const LAS bf16x8*)(lds + PG8_SB(b, h) + boff + n * 2048 + k * 1024); } while (0)
; #define PG8_MMA(ai, bj, At, Bt) do { __builtin_amdgcn_s_setprio(1); _Pragma("unroll") for (int m = 0; m < 4; ++m) _Pragma("unroll") for (int n = 0; n < 2; ++n) _Pragma("unroll") for (int k = 0; k < 2; ++k) \
;         acc[ai][bj][m][n] = __builtin_amdgcn_mfma_f32_16x16x32_bf16(Bt[n][k], At[m][k], acc[ai][bj][m][n], 0, 0, 0); __builtin_amdgcn_s_setprio(0); } while (0)
; #define PG8_WAIT_V(n) asm volatile("s_waitcnt vmcnt(" #n ")" ::: "memory")
; #define PG8_WAIT_L(n) asm volatile("s_waitcnt lgkmcnt(" #n ")" ::: "memory")
; #define PG8_BAR __builtin_amdgcn_s_barrier()
; #define PG8_SCHED __builtin_amdgcn_sched_barrier(0)
;     ...
;             PG8_WAIT_V(8); PG8_WAIT_L(0); PG8_BAR; PG8_MMA(1, 0, At, B0); PG8_MMA(1, 1, At, B1); PG8_BAR; PG8_SCHED;
;             PG8_LDB(B0, 1, 0); PG8_LDB(B1, 1, 1); PG8_SCHED; PG8_LDA(At, 1, 0); PG8_STAGE_A(PG8_SA(0, 1), a2, 1, g2);
;             PG8_WAIT_V(8); PG8_WAIT_L(0); PG8_BAR; PG8_MMA(0, 0, At, B0); PG8_MMA(0, 1, At, B1); PG8_BAR; PG8_SCHED;
	s_setprio 1
	s_waitcnt lgkmcnt(0)
	v_mfma_f32_16x16x32_bf16 v[62:65], v[164:167], v[196:199], v[62:65]
	v_mfma_f32_16x16x32_bf16 v[58:61], v[172:175], v[196:199], v[58:61]
	v_mfma_f32_16x16x32_bf16 v[54:57], v[164:167], v[216:219], v[54:57]
	v_mfma_f32_16x16x32_bf16 v[50:53], v[172:175], v[216:219], v[50:53]
	v_mfma_f32_16x16x32_bf16 v[38:41], v[164:167], v[224:227], v[38:41]
	v_mfma_f32_16x16x32_bf16 v[34:37], v[172:175], v[224:227], v[34:37]
	v_mfma_f32_16x16x32_bf16 v[22:25], v[164:167], v[232:235], v[22:25]
	v_mfma_f32_16x16x32_bf16 v[18:21], v[172:175], v[232:235], v[18:21]
	v_mfma_f32_16x16x32_bf16 v[62:65], v[168:171], v[200:203], v[62:65]
	v_mfma_f32_16x16x32_bf16 v[58:61], v[176:179], v[200:203], v[58:61]
	v_mfma_f32_16x16x32_bf16 v[54:57], v[168:171], v[220:223], v[54:57]
	v_mfma_f32_16x16x32_bf16 v[50:53], v[176:179], v[220:223], v[50:53]
	v_mfma_f32_16x16x32_bf16 v[38:41], v[168:171], v[228:231], v[38:41]
	v_mfma_f32_16x16x32_bf16 v[34:37], v[176:179], v[228:231], v[34:37]
	v_mfma_f32_16x16x32_bf16 v[22:25], v[168:171], v[236:239], v[22:25]
	v_mfma_f32_16x16x32_bf16 v[18:21], v[176:179], v[236:239], v[18:21]
	v_mfma_f32_16x16x32_bf16 v[46:49], v[180:183], v[196:199], v[46:49]
	v_mfma_f32_16x16x32_bf16 v[42:45], v[188:191], v[196:199], v[42:45]
	v_mfma_f32_16x16x32_bf16 v[30:33], v[180:183], v[216:219], v[30:33]
	v_mfma_f32_16x16x32_bf16 v[26:29], v[188:191], v[216:219], v[26:29]
	v_mfma_f32_16x16x32_bf16 v[14:17], v[180:183], v[224:227], v[14:17]
	v_mfma_f32_16x16x32_bf16 v[10:13], v[188:191], v[224:227], v[10:13]
	v_mfma_f32_16x16x32_bf16 v[6:9], v[180:183], v[232:235], v[6:9]
	v_mfma_f32_16x16x32_bf16 v[2:5], v[188:191], v[232:235], v[2:5]
	v_mfma_f32_16x16x32_bf16 v[46:49], v[184:187], v[200:203], v[46:49]
	v_mfma_f32_16x16x32_bf16 v[42:45], v[192:195], v[200:203], v[42:45]
	v_mfma_f32_16x16x32_bf16 v[30:33], v[184:187], v[220:223], v[30:33]
	v_mfma_f32_16x16x32_bf16 v[26:29], v[192:195], v[220:223], v[26:29]
	v_mfma_f32_16x16x32_bf16 v[14:17], v[184:187], v[228:231], v[14:17]
	v_mfma_f32_16x16x32_bf16 v[10:13], v[192:195], v[228:231], v[10:13]
	v_mfma_f32_16x16x32_bf16 v[6:9], v[184:187], v[236:239], v[6:9]
	v_mfma_f32_16x16x32_bf16 v[2:5], v[192:195], v[236:239], v[2:5]
	s_setprio 0
	s_barrier
	s_add_i32 s15, 0, 0x18000
	s_add_i32 s18, 0, 0x1c000
	v_add_u32_e32 v176, s15, v161
	v_add_u32_e32 v192, s18, v161
	ds_read_b128 v[164:167], v176
	ds_read_b128 v[168:171], v176 offset:1024
	ds_read_b128 v[172:175], v176 offset:2048
	ds_read_b128 v[176:179], v176 offset:3072
	ds_read_b128 v[180:183], v192
	ds_read_b128 v[184:187], v192 offset:1024
	ds_read_b128 v[188:191], v192 offset:2048
	ds_read_b128 v[192:195], v192 offset:3072
	s_add_u32 s16, s30, 0x80000
	s_addc_u32 s17, s31, 0
	s_mov_b32 m0, s59
	v_lshl_add_u64 v[212:213], s[16:17], 0, v[134:135]
	ds_read_b128 v[196:199], v163 offset:32768
	ds_read_b128 v[200:203], v163 offset:33792
	ds_read_b128 v[216:219], v163 offset:34816
	ds_read_b128 v[220:223], v163 offset:35840
	ds_read_b128 v[224:227], v163 offset:36864
	ds_read_b128 v[228:231], v163 offset:37888
	ds_read_b128 v[232:235], v163 offset:38912
	ds_read_b128 v[236:239], v163 offset:39936
	global_load_lds_dwordx4 v[212:213], off
	v_lshl_add_u64 v[212:213], s[16:17], 0, v[132:133]
	s_mov_b32 m0, s60
	s_nop 0
	global_load_lds_dwordx4 v[212:213], off
	s_waitcnt vmcnt(8)
	s_waitcnt lgkmcnt(0)
	s_barrier
	s_setprio 1
	s_waitcnt lgkmcnt(0)
	v_mfma_f32_16x16x32_bf16 v[126:129], v[164:167], v[196:199], v[126:129]
	v_mfma_f32_16x16x32_bf16 v[122:125], v[172:175], v[196:199], v[122:125]
	v_mfma_f32_16x16x32_bf16 v[118:121], v[164:167], v[216:219], v[118:121]
	v_mfma_f32_16x16x32_bf16 v[114:117], v[172:175], v[216:219], v[114:117]
	v_mfma_f32_16x16x32_bf16 v[102:105], v[164:167], v[224:227], v[102:105]
	v_mfma_f32_16x16x32_bf16 v[98:101], v[172:175], v[224:227], v[98:101]
	v_mfma_f32_16x16x32_bf16 v[86:89], v[164:167], v[232:235], v[86:89]
	v_mfma_f32_16x16x32_bf16 v[82:85], v[172:175], v[232:235], v[82:85]
	v_mfma_f32_16x16x32_bf16 v[126:129], v[168:171], v[200:203], v[126:129]
	v_mfma_f32_16x16x32_bf16 v[122:125], v[176:179], v[200:203], v[122:125]
	v_mfma_f32_16x16x32_bf16 v[118:121], v[168:171], v[220:223], v[118:121]
	v_mfma_f32_16x16x32_bf16 v[114:117], v[176:179], v[220:223], v[114:117]
	v_mfma_f32_16x16x32_bf16 v[102:105], v[168:171], v[228:231], v[102:105]
	v_mfma_f32_16x16x32_bf16 v[98:101], v[176:179], v[228:231], v[98:101]
	v_mfma_f32_16x16x32_bf16 v[86:89], v[168:171], v[236:239], v[86:89]
	v_mfma_f32_16x16x32_bf16 v[82:85], v[176:179], v[236:239], v[82:85]
	v_mfma_f32_16x16x32_bf16 v[110:113], v[180:183], v[196:199], v[110:113]
	v_mfma_f32_16x16x32_bf16 v[106:109], v[188:191], v[196:199], v[106:109]
	v_mfma_f32_16x16x32_bf16 v[94:97], v[180:183], v[216:219], v[94:97]
	v_mfma_f32_16x16x32_bf16 v[90:93], v[188:191], v[216:219], v[90:93]
	v_mfma_f32_16x16x32_bf16 v[78:81], v[180:183], v[224:227], v[78:81]
	v_mfma_f32_16x16x32_bf16 v[74:77], v[188:191], v[224:227], v[74:77]
	v_mfma_f32_16x16x32_bf16 v[70:73], v[180:183], v[232:235], v[70:73]
	v_mfma_f32_16x16x32_bf16 v[66:69], v[188:191], v[232:235], v[66:69]
	v_mfma_f32_16x16x32_bf16 v[110:113], v[184:187], v[200:203], v[110:113]
	v_mfma_f32_16x16x32_bf16 v[106:109], v[192:195], v[200:203], v[106:109]
	v_mfma_f32_16x16x32_bf16 v[94:97], v[184:187], v[220:223], v[94:97]
	v_mfma_f32_16x16x32_bf16 v[90:93], v[192:195], v[220:223], v[90:93]
	v_mfma_f32_16x16x32_bf16 v[78:81], v[184:187], v[228:231], v[78:81]
	v_mfma_f32_16x16x32_bf16 v[74:77], v[192:195], v[228:231], v[74:77]
	v_mfma_f32_16x16x32_bf16 v[70:73], v[184:187], v[236:239], v[70:73]
	v_mfma_f32_16x16x32_bf16 v[66:69], v[192:195], v[236:239], v[66:69]
	s_setprio 0
	s_barrier
; #define PG8_STAGE(bufoff, gbase, voff) do { _Pragma("unroll") for (int _i = 0; _i < 2; ++_i) \
;         __builtin_amdgcn_global_load_lds((const unsigned*)((const char*)(gbase) + (voff)[_i]), (LAS unsigned*)(lds + (bufoff) + ldsw + _i * 8192), 16, 0, 0); } while (0)
; #define PG8_STAGE_A(bufoff, kptr, half, VO) do { if constexpr (GATHER) { _Pragma("unroll") for (int _i = 0; _i < 2; ++_i) \
;         __builtin_amdgcn_global_load_lds((const unsigned*)((const char*)(kptr) + (VO)[half][_i]), (LAS unsigned*)(lds + (bufoff) + ldsw + _i * 8192), 16, 0, 0); } \
;         else { PG8_STAGE(bufoff, (kptr) + (half) * hstepA, voffA); } } while (0)
; #define PG8_LDA(dst, b, h) do { _Pragma("unroll") for (int m = 0; m < 4; ++m) _Pragma("unroll") for (int k = 0; k < 2; ++k) dst[m][k] = *(const LAS bf16x8*)(lds + PG8_SA(b, h) + aoff + m * 2048 + k * 1024); } while (0)
; #define PG8_MMA(ai, bj, At, Bt) do { __builtin_amdgcn_s_setprio(1); _Pragma("unroll") for (int m = 0; m < 4; ++m) _Pragma("unroll") for (int n = 0; n < 2; ++n) _Pragma("unroll") for (int k = 0; k < 2; ++k) \
;         acc[ai][bj][m][n] = __builtin_amdgcn_mfma_f32_16x16x32_bf16(Bt[n][k], At[m][k], acc[ai][bj][m][n], 0, 0, 0); __builtin_amdgcn_s_setprio(0); } while (0)
; #define PG8_WAIT_V(n) asm volatile("s_waitcnt vmcnt(" #n ")" ::: "memory")
; #define PG8_WAIT_L(n) asm volatile("s_waitcnt lgkmcnt(" #n ")" ::: "memory")
; #define PG8_BAR __builtin_amdgcn_s_barrier()
; #define PG8_SCHED __builtin_amdgcn_sched_barrier(0)
;     ...
;             PG8_LDA(At, 1, 1); PG8_STAGE(PG8_SB(1, 0), b3, voffB); PG8_STAGE(PG8_SB(1, 1), b3 + hstepB, voffB); PG8_STAGE_A(PG8_SA(1, 0), a3, 0, g2);
;             PG8_WAIT_V(8); PG8_WAIT_L(0); PG8_BAR; PG8_MMA(1, 0, At, B0); PG8_MMA(1, 1, At, B1); PG8_BAR; PG8_SCHED;
	s_add_i32 s15, s15, s52
	v_lshl_add_u64 v[158:159], v[158:159], 0, s[8:9]
	s_mov_b32 m0, s15
	ds_read_b128 v[196:199], v163 offset:49152
	ds_read_b128 v[200:203], v163 offset:50176
	ds_read_b128 v[216:219], v163 offset:51200
	ds_read_b128 v[220:223], v163 offset:52224
	ds_read_b128 v[224:227], v163 offset:53248
	ds_read_b128 v[228:231], v163 offset:54272
	ds_read_b128 v[232:235], v163 offset:55296
	ds_read_b128 v[236:239], v163 offset:56320
	global_load_lds_dwordx4 v[158:159], off
	s_add_i32 m0, s15, 0x2000
	s_add_u32 s0, s0, 0x80080
	v_lshl_add_u64 v[158:159], v[204:205], 0, s[8:9]
	s_addc_u32 s1, s1, 0
	s_add_i32 s15, s18, s52
	global_load_lds_dwordx4 v[158:159], off
	v_lshl_add_u64 v[158:159], s[0:1], 0, v[206:207]
	s_mov_b32 m0, s15
	s_nop 0
	global_load_lds_dwordx4 v[158:159], off
	v_lshl_add_u64 v[158:159], s[0:1], 0, v[130:131]
	s_add_i32 m0, s15, 0x2000
	s_nop 0
	global_load_lds_dwordx4 v[158:159], off
	v_lshl_add_u64 v[158:159], v[208:209], 0, s[8:9]
	s_mov_b32 m0, s61
	s_nop 0
	global_load_lds_dwordx4 v[158:159], off
	v_lshl_add_u64 v[158:159], v[210:211], 0, s[8:9]
	s_mov_b32 m0, s62
	s_nop 0
	global_load_lds_dwordx4 v[158:159], off
	s_waitcnt vmcnt(8)
	s_waitcnt lgkmcnt(0)
	s_barrier
	s_setprio 1
	s_waitcnt lgkmcnt(0)
	v_mfma_f32_16x16x32_bf16 v[62:65], v[164:167], v[196:199], v[62:65]
	v_mfma_f32_16x16x32_bf16 v[58:61], v[172:175], v[196:199], v[58:61]
	v_mfma_f32_16x16x32_bf16 v[54:57], v[164:167], v[216:219], v[54:57]
	v_mfma_f32_16x16x32_bf16 v[50:53], v[172:175], v[216:219], v[50:53]
	v_mfma_f32_16x16x32_bf16 v[38:41], v[164:167], v[224:227], v[38:41]
	v_mfma_f32_16x16x32_bf16 v[34:37], v[172:175], v[224:227], v[34:37]
	v_mfma_f32_16x16x32_bf16 v[22:25], v[164:167], v[232:235], v[22:25]
	v_mfma_f32_16x16x32_bf16 v[18:21], v[172:175], v[232:235], v[18:21]
	v_mfma_f32_16x16x32_bf16 v[62:65], v[168:171], v[200:203], v[62:65]
	v_mfma_f32_16x16x32_bf16 v[58:61], v[176:179], v[200:203], v[58:61]
	v_mfma_f32_16x16x32_bf16 v[54:57], v[168:171], v[220:223], v[54:57]
	v_mfma_f32_16x16x32_bf16 v[50:53], v[176:179], v[220:223], v[50:53]
	v_mfma_f32_16x16x32_bf16 v[38:41], v[168:171], v[228:231], v[38:41]
	v_mfma_f32_16x16x32_bf16 v[34:37], v[176:179], v[228:231], v[34:37]
	v_mfma_f32_16x16x32_bf16 v[22:25], v[168:171], v[236:239], v[22:25]
	v_mfma_f32_16x16x32_bf16 v[18:21], v[176:179], v[236:239], v[18:21]
	v_mfma_f32_16x16x32_bf16 v[46:49], v[180:183], v[196:199], v[46:49]
	v_mfma_f32_16x16x32_bf16 v[42:45], v[188:191], v[196:199], v[42:45]
	v_mfma_f32_16x16x32_bf16 v[30:33], v[180:183], v[216:219], v[30:33]
	v_mfma_f32_16x16x32_bf16 v[26:29], v[188:191], v[216:219], v[26:29]
	v_mfma_f32_16x16x32_bf16 v[14:17], v[180:183], v[224:227], v[14:17]
	v_mfma_f32_16x16x32_bf16 v[10:13], v[188:191], v[224:227], v[10:13]
	v_mfma_f32_16x16x32_bf16 v[6:9], v[180:183], v[232:235], v[6:9]
	v_mfma_f32_16x16x32_bf16 v[2:5], v[188:191], v[232:235], v[2:5]
	v_mfma_f32_16x16x32_bf16 v[46:49], v[184:187], v[200:203], v[46:49]
	v_mfma_f32_16x16x32_bf16 v[42:45], v[192:195], v[200:203], v[42:45]
	v_mfma_f32_16x16x32_bf16 v[30:33], v[184:187], v[220:223], v[30:33]
	v_mfma_f32_16x16x32_bf16 v[26:29], v[192:195], v[220:223], v[26:29]
	v_mfma_f32_16x16x32_bf16 v[14:17], v[184:187], v[228:231], v[14:17]
	v_mfma_f32_16x16x32_bf16 v[10:13], v[192:195], v[228:231], v[10:13]
	v_mfma_f32_16x16x32_bf16 v[6:9], v[184:187], v[236:239], v[6:9]
	v_mfma_f32_16x16x32_bf16 v[2:5], v[192:195], v[236:239], v[2:5]
	s_setprio 0
	s_barrier
	s_add_i32 s14, s14, 2
	s_add_u32 s24, s24, 0x100
	s_addc_u32 s25, s25, 0
	s_add_u32 s12, s12, 0x100
	s_addc_u32 s13, s13, 0
	s_cmp_gt_u32 s14, 29
	s_cbranch_scc0 .LBB0_1669
	s_and_b64 vcc, exec, s[38:39]
	s_cbranch_vccz .LBB0_1672
	s_barrier

; #define PG8_STAGE(bufoff, gbase, voff) do { _Pragma("unroll") for (int _i = 0; _i < 2; ++_i) \
;         __builtin_amdgcn_global_load_lds((const unsigned*)((const char*)(gbase) + (voff)[_i]), (LAS unsigned*)(lds + (bufoff) + ldsw + _i * 8192), 16, 0, 0); } while (0)
; #define PG8_STAGE_A(bufoff, kptr, half, VO) do { if constexpr (GATHER) { _Pragma("unroll") for (int _i = 0; _i < 2; ++_i) \
;         __builtin_amdgcn_global_load_lds((const unsigned*)((const char*)(kptr) + (VO)[half][_i]), (LAS unsigned*)(lds + (bufoff) + ldsw + _i * 8192), 16, 0, 0); } \
;         else { PG8_STAGE(bufoff, (kptr) + (half) * hstepA, voffA); } } while (0)
; #define PG8_LDA(dst, b, h) do { _Pragma("unroll") for (int m = 0; m < 4; ++m) _Pragma("unroll") for (int k = 0; k < 2; ++k) dst[m][k] = *(const LAS bf16x8*)(lds + PG8_SA(b, h) + aoff + m * 2048 + k * 1024); } while (0)
; #define PG8_LDB(dst, b, h) do { _Pragma("unroll") for (int n = 0; n < 2; ++n) _Pragma("unroll") for (int k = 0; k < 2; ++k) dst[n][k] = *(const LAS bf16x8*)(lds + PG8_SB(b, h) + boff + n * 2048 + k * 1024); } while (0)
; #define PG8_WAIT_V(n) asm volatile("s_waitcnt vmcnt(" #n ")" ::: "memory")
; #define PG8_WAIT_L(n) asm volatile("s_waitcnt lgkmcnt(" #n ")" ::: "memory")
; #define PG8_BAR __builtin_amdgcn_s_barrier()
;     ...
;             const char* a1 = cA + (size_t)(t + 1) * kstep;
;             const char* a2 = last ? nA : cA + (size_t)(t + 2) * kstep; const char* b2 = last ? nB : cB + (size_t)(t + 2) * kstep;
;             const char* a3 = a2 + kstep; const char* b3 = b2 + kstep;
;             unsigned g2[2][2];
;             if constexpr (GATHER) {
; #pragma unroll
;                 for (int _h = 0; _h < 2; ++_h)
; #pragma unroll
;                     for (int _i = 0; _i < 2; ++_i) g2[_h][_i] = last ? gN[_h][_i] : gC[_h][_i]; }
;             if constexpr (SP2) {
;             PG8_LDB(B0, 0, 0); PG8_LDB(B1, 0, 1); PG8_SCHED; PG8_LDA(At, 0, 0); PG8_STAGE_A(PG8_SA(1, 1), a1, 1, gC);
;             PG8_WAIT_V(8); PG8_WAIT_L(0); PG8_BAR; PG8_MMA(0, 0, At, B0); PG8_MMA(0, 1, At, B1); PG8_BAR; PG8_SCHED;
;             PG8_LDA(At, 0, 1); PG8_STAGE(PG8_SB(0, 0), b2, voffB); PG8_STAGE(PG8_SB(0, 1), b2 + hstepB, voffB); PG8_STAGE_A(PG8_SA(0, 0), a2, 0, g2);
;             PG8_WAIT_V(8); PG8_WAIT_L(0); PG8_BAR; PG8_MMA(1, 0, At, B0); PG8_MMA(1, 1, At, B1); PG8_BAR; PG8_SCHED;
.LBB0_1693:
	s_add_u32 s0, s24, 0xfff80080
	s_addc_u32 s1, s25, -1
	s_add_i32 s15, 0, 0x10000
	s_cmp_eq_u32 s14, 28
	s_cselect_b32 s31, s45, s1
	s_cselect_b32 s30, s44, s0
	s_cselect_b32 s1, s47, s13
	s_cselect_b32 s0, s46, s12
	s_add_i32 s18, 0, 0x14000
	v_add_u32_e32 v142, s15, v244
	v_add_u32_e32 v158, s18, v244
	ds_read_b128 v[122:125], v142
	ds_read_b128 v[126:129], v142 offset:1024
	ds_read_b128 v[134:137], v142 offset:2048
	ds_read_b128 v[142:145], v142 offset:3072
	ds_read_b128 v[146:149], v158
	ds_read_b128 v[150:153], v158 offset:1024
	ds_read_b128 v[154:157], v158 offset:2048
	ds_read_b128 v[158:161], v158 offset:3072
	v_lshl_add_u64 v[194:195], s[24:25], 0, v[222:223]
	s_add_i32 m0, s49, 0xc000
	ds_read_b128 v[162:165], v209
	ds_read_b128 v[166:169], v209 offset:1024
	ds_read_b128 v[170:173], v209 offset:2048
	ds_read_b128 v[174:177], v209 offset:3072
	ds_read_b128 v[178:181], v209 offset:4096
	ds_read_b128 v[182:185], v209 offset:5120
	ds_read_b128 v[186:189], v209 offset:6144
	ds_read_b128 v[190:193], v209 offset:7168
	global_load_lds_dwordx4 v[194:195], off
	v_lshl_add_u64 v[194:195], s[24:25], 0, v[224:225]
	s_add_i32 m0, s49, 0xe000
	s_nop 0
	global_load_lds_dwordx4 v[194:195], off
	s_waitcnt vmcnt(8)
	s_waitcnt lgkmcnt(0)
	s_barrier
	s_setprio 1
	s_waitcnt lgkmcnt(0)
	v_mfma_f32_16x16x32_bf16 v[138:141], v[122:125], v[162:165], v[138:141]
	v_mfma_f32_16x16x32_bf16 v[130:133], v[134:137], v[162:165], v[130:133]
	v_mfma_f32_16x16x32_bf16 v[114:117], v[122:125], v[170:173], v[114:117]
	v_mfma_f32_16x16x32_bf16 v[106:109], v[134:137], v[170:173], v[106:109]
	v_mfma_f32_16x16x32_bf16 v[98:101], v[122:125], v[178:181], v[98:101]
	v_mfma_f32_16x16x32_bf16 v[90:93], v[134:137], v[178:181], v[90:93]
	v_mfma_f32_16x16x32_bf16 v[82:85], v[122:125], v[186:189], v[82:85]
	v_mfma_f32_16x16x32_bf16 v[74:77], v[134:137], v[186:189], v[74:77]
	v_mfma_f32_16x16x32_bf16 v[138:141], v[126:129], v[166:169], v[138:141]
	v_mfma_f32_16x16x32_bf16 v[130:133], v[142:145], v[166:169], v[130:133]
	v_mfma_f32_16x16x32_bf16 v[114:117], v[126:129], v[174:177], v[114:117]
	v_mfma_f32_16x16x32_bf16 v[106:109], v[142:145], v[174:177], v[106:109]
	v_mfma_f32_16x16x32_bf16 v[98:101], v[126:129], v[182:185], v[98:101]
	v_mfma_f32_16x16x32_bf16 v[90:93], v[142:145], v[182:185], v[90:93]
	v_mfma_f32_16x16x32_bf16 v[82:85], v[126:129], v[190:193], v[82:85]
	v_mfma_f32_16x16x32_bf16 v[74:77], v[142:145], v[190:193], v[74:77]
	v_mfma_f32_16x16x32_bf16 v[118:121], v[146:149], v[162:165], v[118:121]
	v_mfma_f32_16x16x32_bf16 v[110:113], v[154:157], v[162:165], v[110:113]
	v_mfma_f32_16x16x32_bf16 v[102:105], v[146:149], v[170:173], v[102:105]
	v_mfma_f32_16x16x32_bf16 v[94:97], v[154:157], v[170:173], v[94:97]
	v_mfma_f32_16x16x32_bf16 v[86:89], v[146:149], v[178:181], v[86:89]
	v_mfma_f32_16x16x32_bf16 v[78:81], v[154:157], v[178:181], v[78:81]
	v_mfma_f32_16x16x32_bf16 v[70:73], v[146:149], v[186:189], v[70:73]
	v_mfma_f32_16x16x32_bf16 v[66:69], v[154:157], v[186:189], v[66:69]
	v_mfma_f32_16x16x32_bf16 v[118:121], v[150:153], v[166:169], v[118:121]
	v_mfma_f32_16x16x32_bf16 v[110:113], v[158:161], v[166:169], v[110:113]
	v_mfma_f32_16x16x32_bf16 v[102:105], v[150:153], v[174:177], v[102:105]
	v_mfma_f32_16x16x32_bf16 v[94:97], v[158:161], v[174:177], v[94:97]
	v_mfma_f32_16x16x32_bf16 v[86:89], v[150:153], v[182:185], v[86:89]
	v_mfma_f32_16x16x32_bf16 v[78:81], v[158:161], v[182:185], v[78:81]
	v_mfma_f32_16x16x32_bf16 v[70:73], v[150:153], v[190:193], v[70:73]
	v_mfma_f32_16x16x32_bf16 v[66:69], v[158:161], v[190:193], v[66:69]
	s_setprio 0
	s_barrier
	s_add_i32 s15, s15, s52
	v_lshl_add_u64 v[194:195], s[0:1], 0, v[206:207]
	s_mov_b32 m0, s15
	ds_read_b128 v[162:165], v209 offset:16384
	ds_read_b128 v[166:169], v209 offset:17408
	ds_read_b128 v[170:173], v209 offset:18432
	ds_read_b128 v[174:177], v209 offset:19456
	ds_read_b128 v[178:181], v209 offset:20480
	ds_read_b128 v[182:185], v209 offset:21504
	ds_read_b128 v[186:189], v209 offset:22528
	ds_read_b128 v[190:193], v209 offset:23552
	global_load_lds_dwordx4 v[194:195], off
	s_add_i32 m0, s15, 0x2000
	s_add_u32 s16, s0, 0x80000
	v_lshl_add_u64 v[196:197], s[0:1], 0, v[216:217]
	s_addc_u32 s17, s1, 0
	s_add_i32 s15, s18, s52
	global_load_lds_dwordx4 v[196:197], off
	v_lshl_add_u64 v[198:199], s[16:17], 0, v[206:207]
	s_mov_b32 m0, s15
	v_lshl_add_u64 v[200:201], s[30:31], 0, v[218:219]
	global_load_lds_dwordx4 v[198:199], off
	v_lshl_add_u64 v[198:199], s[16:17], 0, v[216:217]
	s_add_i32 m0, s15, 0x2000
	s_nop 0
	global_load_lds_dwordx4 v[198:199], off
	v_lshl_add_u64 v[198:199], s[30:31], 0, v[220:221]
	s_mov_b32 m0, s49
	s_nop 0
	global_load_lds_dwordx4 v[198:199], off
	s_mov_b32 m0, s53
	s_nop 0
	global_load_lds_dwordx4 v[200:201], off
	s_waitcnt vmcnt(8)
	s_waitcnt lgkmcnt(0)
	s_barrier
; #define PG8_STAGE_A(bufoff, kptr, half, VO) do { if constexpr (GATHER) { _Pragma("unroll") for (int _i = 0; _i < 2; ++_i) \
;         __builtin_amdgcn_global_load_lds((const unsigned*)((const char*)(kptr) + (VO)[half][_i]), (LAS unsigned*)(lds + (bufoff) + ldsw + _i * 8192), 16, 0, 0); } \
;         else { PG8_STAGE(bufoff, (kptr) + (half) * hstepA, voffA); } } while (0)
; #define PG8_LDA(dst, b, h) do { _Pragma("unroll") for (int m = 0; m < 4; ++m) _Pragma("unroll") for (int k = 0; k < 2; ++k) dst[m][k] = *(const LAS bf16x8*)(lds + PG8_SA(b, h) + aoff + m * 2048 + k * 1024); } while (0)
; #define PG8_LDB(dst, b, h) do { _Pragma("unroll") for (int n = 0; n < 2; ++n) _Pragma("unroll") for (int k = 0; k < 2; ++k) dst[n][k] = *(const LAS bf16x8*)(lds + PG8_SB(b, h) + boff + n * 2048 + k * 1024); } while (0)
; #define PG8_MMA(ai, bj, At, Bt) do { __builtin_amdgcn_s_setprio(1); _Pragma("unroll") for (int m = 0; m < 4; ++m) _Pragma("unroll") for (int n = 0; n < 2; ++n) _Pragma("unroll") for (int k = 0; k < 2; ++k) \
;         acc[ai][bj][m][n] = __builtin_amdgcn_mfma_f32_16x16x32_bf16(Bt[n][k], At[m][k], acc[ai][bj][m][n], 0, 0, 0); __builtin_amdgcn_s_setprio(0); } while (0)
; #define PG8_WAIT_V(n) asm volatile("s_waitcnt vmcnt(" #n ")" ::: "memory")
; #define PG8_WAIT_L(n) asm volatile("s_waitcnt lgkmcnt(" #n ")" ::: "memory")
; #define PG8_BAR __builtin_amdgcn_s_barrier()
; #define PG8_SCHED __builtin_amdgcn_sched_barrier(0)
;     ...
;             PG8_WAIT_V(8); PG8_WAIT_L(0); PG8_BAR; PG8_MMA(1, 0, At, B0); PG8_MMA(1, 1, At, B1); PG8_BAR; PG8_SCHED;
;             PG8_LDB(B0, 1, 0); PG8_LDB(B1, 1, 1); PG8_SCHED; PG8_LDA(At, 1, 0); PG8_STAGE_A(PG8_SA(0, 1), a2, 1, g2);
;             PG8_WAIT_V(8); PG8_WAIT_L(0); PG8_BAR; PG8_MMA(0, 0, At, B0); PG8_MMA(0, 1, At, B1); PG8_BAR; PG8_SCHED;
	s_setprio 1
	s_waitcnt lgkmcnt(0)
	v_mfma_f32_16x16x32_bf16 v[62:65], v[122:125], v[162:165], v[62:65]
	v_mfma_f32_16x16x32_bf16 v[58:61], v[134:137], v[162:165], v[58:61]
	v_mfma_f32_16x16x32_bf16 v[50:53], v[122:125], v[170:173], v[50:53]
	v_mfma_f32_16x16x32_bf16 v[42:45], v[134:137], v[170:173], v[42:45]
	v_mfma_f32_16x16x32_bf16 v[34:37], v[122:125], v[178:181], v[34:37]
	v_mfma_f32_16x16x32_bf16 v[26:29], v[134:137], v[178:181], v[26:29]
	v_mfma_f32_16x16x32_bf16 v[18:21], v[122:125], v[186:189], v[18:21]
	v_mfma_f32_16x16x32_bf16 v[10:13], v[134:137], v[186:189], v[10:13]
	v_mfma_f32_16x16x32_bf16 v[62:65], v[126:129], v[166:169], v[62:65]
	v_mfma_f32_16x16x32_bf16 v[58:61], v[142:145], v[166:169], v[58:61]
	v_mfma_f32_16x16x32_bf16 v[50:53], v[126:129], v[174:177], v[50:53]
	v_mfma_f32_16x16x32_bf16 v[42:45], v[142:145], v[174:177], v[42:45]
	v_mfma_f32_16x16x32_bf16 v[34:37], v[126:129], v[182:185], v[34:37]
	v_mfma_f32_16x16x32_bf16 v[26:29], v[142:145], v[182:185], v[26:29]
	v_mfma_f32_16x16x32_bf16 v[18:21], v[126:129], v[190:193], v[18:21]
	v_mfma_f32_16x16x32_bf16 v[10:13], v[142:145], v[190:193], v[10:13]
	v_mfma_f32_16x16x32_bf16 v[54:57], v[146:149], v[162:165], v[54:57]
	v_mfma_f32_16x16x32_bf16 v[46:49], v[154:157], v[162:165], v[46:49]
	v_mfma_f32_16x16x32_bf16 v[38:41], v[146:149], v[170:173], v[38:41]
	v_mfma_f32_16x16x32_bf16 v[30:33], v[154:157], v[170:173], v[30:33]
	v_mfma_f32_16x16x32_bf16 v[22:25], v[146:149], v[178:181], v[22:25]
	v_mfma_f32_16x16x32_bf16 v[14:17], v[154:157], v[178:181], v[14:17]
	v_mfma_f32_16x16x32_bf16 v[6:9], v[146:149], v[186:189], v[6:9]
	v_mfma_f32_16x16x32_bf16 v[2:5], v[154:157], v[186:189], v[2:5]
	v_mfma_f32_16x16x32_bf16 v[54:57], v[150:153], v[166:169], v[54:57]
	v_mfma_f32_16x16x32_bf16 v[46:49], v[158:161], v[166:169], v[46:49]
	v_mfma_f32_16x16x32_bf16 v[38:41], v[150:153], v[174:177], v[38:41]
	v_mfma_f32_16x16x32_bf16 v[30:33], v[158:161], v[174:177], v[30:33]
	v_mfma_f32_16x16x32_bf16 v[22:25], v[150:153], v[182:185], v[22:25]
	v_mfma_f32_16x16x32_bf16 v[14:17], v[158:161], v[182:185], v[14:17]
	v_mfma_f32_16x16x32_bf16 v[6:9], v[150:153], v[190:193], v[6:9]
	v_mfma_f32_16x16x32_bf16 v[2:5], v[158:161], v[190:193], v[2:5]
	s_setprio 0
	s_barrier
	s_add_i32 s15, 0, 0x18000
	s_add_i32 s18, 0, 0x1c000
	v_add_u32_e32 v142, s15, v244
	v_add_u32_e32 v158, s18, v244
	ds_read_b128 v[122:125], v142
	ds_read_b128 v[126:129], v142 offset:1024
	ds_read_b128 v[134:137], v142 offset:2048
	ds_read_b128 v[142:145], v142 offset:3072
	ds_read_b128 v[146:149], v158
	ds_read_b128 v[150:153], v158 offset:1024
	ds_read_b128 v[154:157], v158 offset:2048
	ds_read_b128 v[158:161], v158 offset:3072
	s_add_u32 s16, s30, 0x80000
	s_addc_u32 s17, s31, 0
	s_mov_b32 m0, s59
	v_lshl_add_u64 v[202:203], s[16:17], 0, v[220:221]
	ds_read_b128 v[162:165], v209 offset:32768
	ds_read_b128 v[166:169], v209 offset:33792
	ds_read_b128 v[170:173], v209 offset:34816
	ds_read_b128 v[174:177], v209 offset:35840
	ds_read_b128 v[178:181], v209 offset:36864
	ds_read_b128 v[182:185], v209 offset:37888
	ds_read_b128 v[186:189], v209 offset:38912
	ds_read_b128 v[190:193], v209 offset:39936
	global_load_lds_dwordx4 v[202:203], off
	v_lshl_add_u64 v[202:203], s[16:17], 0, v[218:219]
	s_mov_b32 m0, s60
	s_nop 0
	global_load_lds_dwordx4 v[202:203], off
	s_waitcnt vmcnt(8)
	s_waitcnt lgkmcnt(0)
	s_barrier
	s_setprio 1
	s_waitcnt lgkmcnt(0)
	v_mfma_f32_16x16x32_bf16 v[138:141], v[122:125], v[162:165], v[138:141]
	v_mfma_f32_16x16x32_bf16 v[130:133], v[134:137], v[162:165], v[130:133]
	v_mfma_f32_16x16x32_bf16 v[114:117], v[122:125], v[170:173], v[114:117]
	v_mfma_f32_16x16x32_bf16 v[106:109], v[134:137], v[170:173], v[106:109]
	v_mfma_f32_16x16x32_bf16 v[98:101], v[122:125], v[178:181], v[98:101]
	v_mfma_f32_16x16x32_bf16 v[90:93], v[134:137], v[178:181], v[90:93]
	v_mfma_f32_16x16x32_bf16 v[82:85], v[122:125], v[186:189], v[82:85]
	v_mfma_f32_16x16x32_bf16 v[74:77], v[134:137], v[186:189], v[74:77]
	v_mfma_f32_16x16x32_bf16 v[138:141], v[126:129], v[166:169], v[138:141]
	v_mfma_f32_16x16x32_bf16 v[130:133], v[142:145], v[166:169], v[130:133]
	v_mfma_f32_16x16x32_bf16 v[114:117], v[126:129], v[174:177], v[114:117]
	v_mfma_f32_16x16x32_bf16 v[106:109], v[142:145], v[174:177], v[106:109]
	v_mfma_f32_16x16x32_bf16 v[98:101], v[126:129], v[182:185], v[98:101]
	v_mfma_f32_16x16x32_bf16 v[90:93], v[142:145], v[182:185], v[90:93]
	v_mfma_f32_16x16x32_bf16 v[82:85], v[126:129], v[190:193], v[82:85]
	v_mfma_f32_16x16x32_bf16 v[74:77], v[142:145], v[190:193], v[74:77]
	v_mfma_f32_16x16x32_bf16 v[118:121], v[146:149], v[162:165], v[118:121]
	v_mfma_f32_16x16x32_bf16 v[110:113], v[154:157], v[162:165], v[110:113]
	v_mfma_f32_16x16x32_bf16 v[102:105], v[146:149], v[170:173], v[102:105]
	v_mfma_f32_16x16x32_bf16 v[94:97], v[154:157], v[170:173], v[94:97]
	v_mfma_f32_16x16x32_bf16 v[86:89], v[146:149], v[178:181], v[86:89]
	v_mfma_f32_16x16x32_bf16 v[78:81], v[154:157], v[178:181], v[78:81]
	v_mfma_f32_16x16x32_bf16 v[70:73], v[146:149], v[186:189], v[70:73]
	v_mfma_f32_16x16x32_bf16 v[66:69], v[154:157], v[186:189], v[66:69]
	v_mfma_f32_16x16x32_bf16 v[118:121], v[150:153], v[166:169], v[118:121]
	v_mfma_f32_16x16x32_bf16 v[110:113], v[158:161], v[166:169], v[110:113]
	v_mfma_f32_16x16x32_bf16 v[102:105], v[150:153], v[174:177], v[102:105]
	v_mfma_f32_16x16x32_bf16 v[94:97], v[158:161], v[174:177], v[94:97]
	v_mfma_f32_16x16x32_bf16 v[86:89], v[150:153], v[182:185], v[86:89]
	v_mfma_f32_16x16x32_bf16 v[78:81], v[158:161], v[182:185], v[78:81]
	v_mfma_f32_16x16x32_bf16 v[70:73], v[150:153], v[190:193], v[70:73]
	v_mfma_f32_16x16x32_bf16 v[66:69], v[158:161], v[190:193], v[66:69]
	s_setprio 0
	s_barrier
; #define PG8_STAGE(bufoff, gbase, voff) do { _Pragma("unroll") for (int _i = 0; _i < 2; ++_i) \
;         __builtin_amdgcn_global_load_lds((const unsigned*)((const char*)(gbase) + (voff)[_i]), (LAS unsigned*)(lds + (bufoff) + ldsw + _i * 8192), 16, 0, 0); } while (0)
; #define PG8_STAGE_A(bufoff, kptr, half, VO) do { if constexpr (GATHER) { _Pragma("unroll") for (int _i = 0; _i < 2; ++_i) \
;         __builtin_amdgcn_global_load_lds((const unsigned*)((const char*)(kptr) + (VO)[half][_i]), (LAS unsigned*)(lds + (bufoff) + ldsw + _i * 8192), 16, 0, 0); } \
;         else { PG8_STAGE(bufoff, (kptr) + (half) * hstepA, voffA); } } while (0)
; #define PG8_LDA(dst, b, h) do { _Pragma("unroll") for (int m = 0; m < 4; ++m) _Pragma("unroll") for (int k = 0; k < 2; ++k) dst[m][k] = *(const LAS bf16x8*)(lds + PG8_SA(b, h) + aoff + m * 2048 + k * 1024); } while (0)
; #define PG8_MMA(ai, bj, At, Bt) do { __builtin_amdgcn_s_setprio(1); _Pragma("unroll") for (int m = 0; m < 4; ++m) _Pragma("unroll") for (int n = 0; n < 2; ++n) _Pragma("unroll") for (int k = 0; k < 2; ++k) \
;         acc[ai][bj][m][n] = __builtin_amdgcn_mfma_f32_16x16x32_bf16(Bt[n][k], At[m][k], acc[ai][bj][m][n], 0, 0, 0); __builtin_amdgcn_s_setprio(0); } while (0)
; #define PG8_WAIT_V(n) asm volatile("s_waitcnt vmcnt(" #n ")" ::: "memory")
; #define PG8_WAIT_L(n) asm volatile("s_waitcnt lgkmcnt(" #n ")" ::: "memory")
; #define PG8_BAR __builtin_amdgcn_s_barrier()
; #define PG8_SCHED __builtin_amdgcn_sched_barrier(0)
;     ...
;             PG8_LDA(At, 1, 1); PG8_STAGE(PG8_SB(1, 0), b3, voffB); PG8_STAGE(PG8_SB(1, 1), b3 + hstepB, voffB); PG8_STAGE_A(PG8_SA(1, 0), a3, 0, g2);
;             PG8_WAIT_V(8); PG8_WAIT_L(0); PG8_BAR; PG8_MMA(1, 0, At, B0); PG8_MMA(1, 1, At, B1); PG8_BAR; PG8_SCHED;
	s_add_i32 s15, s15, s52
	v_lshl_add_u64 v[194:195], v[194:195], 0, s[8:9]
	s_mov_b32 m0, s15
	ds_read_b128 v[162:165], v209 offset:49152
	ds_read_b128 v[166:169], v209 offset:50176
	ds_read_b128 v[170:173], v209 offset:51200
	ds_read_b128 v[174:177], v209 offset:52224
	ds_read_b128 v[178:181], v209 offset:53248
	ds_read_b128 v[182:185], v209 offset:54272
	ds_read_b128 v[186:189], v209 offset:55296
	ds_read_b128 v[190:193], v209 offset:56320
	global_load_lds_dwordx4 v[194:195], off
	s_add_i32 m0, s15, 0x2000
	s_add_u32 s0, s0, 0x80080
	v_lshl_add_u64 v[194:195], v[196:197], 0, s[8:9]
	s_addc_u32 s1, s1, 0
	s_add_i32 s15, s18, s52
	global_load_lds_dwordx4 v[194:195], off
	v_lshl_add_u64 v[194:195], s[0:1], 0, v[206:207]
	s_mov_b32 m0, s15
	s_nop 0
	global_load_lds_dwordx4 v[194:195], off
	v_lshl_add_u64 v[194:195], s[0:1], 0, v[216:217]
	s_add_i32 m0, s15, 0x2000
	s_nop 0
	global_load_lds_dwordx4 v[194:195], off
	v_lshl_add_u64 v[194:195], v[198:199], 0, s[8:9]
	s_mov_b32 m0, s61
	s_nop 0
	global_load_lds_dwordx4 v[194:195], off
	v_lshl_add_u64 v[194:195], v[200:201], 0, s[8:9]
	s_mov_b32 m0, s62
	s_nop 0
	global_load_lds_dwordx4 v[194:195], off
	s_waitcnt vmcnt(8)
	s_waitcnt lgkmcnt(0)
	s_barrier
	s_setprio 1
	s_waitcnt lgkmcnt(0)
	v_mfma_f32_16x16x32_bf16 v[62:65], v[122:125], v[162:165], v[62:65]
	v_mfma_f32_16x16x32_bf16 v[58:61], v[134:137], v[162:165], v[58:61]
	v_mfma_f32_16x16x32_bf16 v[50:53], v[122:125], v[170:173], v[50:53]
	v_mfma_f32_16x16x32_bf16 v[42:45], v[134:137], v[170:173], v[42:45]
	v_mfma_f32_16x16x32_bf16 v[34:37], v[122:125], v[178:181], v[34:37]
	v_mfma_f32_16x16x32_bf16 v[26:29], v[134:137], v[178:181], v[26:29]
	v_mfma_f32_16x16x32_bf16 v[18:21], v[122:125], v[186:189], v[18:21]
	v_mfma_f32_16x16x32_bf16 v[10:13], v[134:137], v[186:189], v[10:13]
	v_mfma_f32_16x16x32_bf16 v[62:65], v[126:129], v[166:169], v[62:65]
	v_mfma_f32_16x16x32_bf16 v[58:61], v[142:145], v[166:169], v[58:61]
	v_mfma_f32_16x16x32_bf16 v[50:53], v[126:129], v[174:177], v[50:53]
	v_mfma_f32_16x16x32_bf16 v[42:45], v[142:145], v[174:177], v[42:45]
	v_mfma_f32_16x16x32_bf16 v[34:37], v[126:129], v[182:185], v[34:37]
	v_mfma_f32_16x16x32_bf16 v[26:29], v[142:145], v[182:185], v[26:29]
	v_mfma_f32_16x16x32_bf16 v[18:21], v[126:129], v[190:193], v[18:21]
	v_mfma_f32_16x16x32_bf16 v[10:13], v[142:145], v[190:193], v[10:13]
	v_mfma_f32_16x16x32_bf16 v[54:57], v[146:149], v[162:165], v[54:57]
	v_mfma_f32_16x16x32_bf16 v[46:49], v[154:157], v[162:165], v[46:49]
	v_mfma_f32_16x16x32_bf16 v[38:41], v[146:149], v[170:173], v[38:41]
	v_mfma_f32_16x16x32_bf16 v[30:33], v[154:157], v[170:173], v[30:33]
	v_mfma_f32_16x16x32_bf16 v[22:25], v[146:149], v[178:181], v[22:25]
	v_mfma_f32_16x16x32_bf16 v[14:17], v[154:157], v[178:181], v[14:17]
	v_mfma_f32_16x16x32_bf16 v[6:9], v[146:149], v[186:189], v[6:9]
	v_mfma_f32_16x16x32_bf16 v[2:5], v[154:157], v[186:189], v[2:5]
	v_mfma_f32_16x16x32_bf16 v[54:57], v[150:153], v[166:169], v[54:57]
	v_mfma_f32_16x16x32_bf16 v[46:49], v[158:161], v[166:169], v[46:49]
	v_mfma_f32_16x16x32_bf16 v[38:41], v[150:153], v[174:177], v[38:41]
	v_mfma_f32_16x16x32_bf16 v[30:33], v[158:161], v[174:177], v[30:33]
	v_mfma_f32_16x16x32_bf16 v[22:25], v[150:153], v[182:185], v[22:25]
	v_mfma_f32_16x16x32_bf16 v[14:17], v[158:161], v[182:185], v[14:17]
	v_mfma_f32_16x16x32_bf16 v[6:9], v[150:153], v[190:193], v[6:9]
	v_mfma_f32_16x16x32_bf16 v[2:5], v[158:161], v[190:193], v[2:5]
	s_setprio 0
	s_barrier
	s_add_i32 s14, s14, 2
	s_add_u32 s24, s24, 0x100
	s_addc_u32 s25, s25, 0
	s_add_u32 s12, s12, 0x100
	s_addc_u32 s13, s13, 0
	s_cmp_gt_u32 s14, 29
	s_cbranch_scc0 .LBB0_1693
	s_and_b64 vcc, exec, s[38:39]
	s_cbranch_vccz .LBB0_1696
	s_barrier

; #define PG8_STAGE(bufoff, gbase, voff) do { _Pragma("unroll") for (int _i = 0; _i < 2; ++_i) \
;         __builtin_amdgcn_global_load_lds((const unsigned*)((const char*)(gbase) + (voff)[_i]), (LAS unsigned*)(lds + (bufoff) + ldsw + _i * 8192), 16, 0, 0); } while (0)
; #define PG8_STAGE_A(bufoff, kptr, half, VO) do { if constexpr (GATHER) { _Pragma("unroll") for (int _i = 0; _i < 2; ++_i) \
;         __builtin_amdgcn_global_load_lds((const unsigned*)((const char*)(kptr) + (VO)[half][_i]), (LAS unsigned*)(lds + (bufoff) + ldsw + _i * 8192), 16, 0, 0); } \
;         else { PG8_STAGE(bufoff, (kptr) + (half) * hstepA, voffA); } } while (0)
; #define PG8_LDA(dst, b, h) do { _Pragma("unroll") for (int m = 0; m < 4; ++m) _Pragma("unroll") for (int k = 0; k < 2; ++k) dst[m][k] = *(const LAS bf16x8*)(lds + PG8_SA(b, h) + aoff + m * 2048 + k * 1024); } while (0)
; #define PG8_LDB(dst, b, h) do { _Pragma("unroll") for (int n = 0; n < 2; ++n) _Pragma("unroll") for (int k = 0; k < 2; ++k) dst[n][k] = *(const LAS bf16x8*)(lds + PG8_SB(b, h) + boff + n * 2048 + k * 1024); } while (0)
; #define PG8_WAIT_V(n) asm volatile("s_waitcnt vmcnt(" #n ")" ::: "memory")
; #define PG8_WAIT_L(n) asm volatile("s_waitcnt lgkmcnt(" #n ")" ::: "memory")
;     ...
;         for (int t = 0; t < nt; t += 2) {
;             const bool last = (t == nt - 2);
;             const char* a1 = cA + (size_t)(t + 1) * kstep;
;             const char* a2 = last ? nA : cA + (size_t)(t + 2) * kstep; const char* b2 = last ? nB : cB + (size_t)(t + 2) * kstep;
;             const char* a3 = a2 + kstep; const char* b3 = b2 + kstep;
;             unsigned g2[2][2];
;             if constexpr (GATHER) {
; #pragma unroll
;                 for (int _h = 0; _h < 2; ++_h)
; #pragma unroll
;                     for (int _i = 0; _i < 2; ++_i) g2[_h][_i] = last ? gN[_h][_i] : gC[_h][_i]; }
;             if constexpr (SP2) {
;             PG8_LDB(B0, 0, 0); PG8_LDB(B1, 0, 1); PG8_SCHED; PG8_LDA(At, 0, 0); PG8_STAGE_A(PG8_SA(1, 1), a1, 1, gC);
;             PG8_WAIT_V(8); PG8_WAIT_L(0); PG8_BAR; PG8_MMA(0, 0, At, B0); PG8_MMA(0, 1, At, B1); PG8_BAR; PG8_SCHED;
;             PG8_LDA(At, 0, 1); PG8_STAGE(PG8_SB(0, 0), b2, voffB); PG8_STAGE(PG8_SB(0, 1), b2 + hstepB, voffB); PG8_STAGE_A(PG8_SA(0, 0), a2, 0, g2);
;             PG8_WAIT_V(8); PG8_WAIT_L(0); PG8_BAR; PG8_MMA(1, 0, At, B0); PG8_MMA(1, 1, At, B1); PG8_BAR; PG8_SCHED;
.LBB0_2265:
	s_add_u32 s0, s34, s24
	s_addc_u32 s1, s35, s25
	s_add_u32 s19, s0, 0x100
	s_addc_u32 s20, s1, 0
	s_add_u32 s21, s16, s24
	s_addc_u32 s22, s17, s25
	s_cmpk_eq_i32 s24, 0xf00
	s_cselect_b64 vcc, -1, 0
	s_and_b64 s[0:1], vcc, exec
	s_cselect_b32 s31, s12, s20
	s_cselect_b32 s30, s13, s19
	s_cselect_b32 s1, s14, s22
	s_cselect_b32 s0, s15, s21
	s_add_i32 s19, 0, 0x10000
	v_add_u32_e32 v161, s19, v139
	s_add_i32 s22, 0, 0x14000
	ds_read_b128 v[162:165], v161
	ds_read_b128 v[166:169], v161 offset:1024
	ds_read_b128 v[170:173], v161 offset:2048
	ds_read_b128 v[174:177], v161 offset:3072
	v_add_u32_e32 v161, s22, v139
	ds_read_b128 v[178:181], v161
	ds_read_b128 v[182:185], v161 offset:1024
	ds_read_b128 v[186:189], v161 offset:2048
	ds_read_b128 v[190:193], v161 offset:3072
	v_cndmask_b32_e32 v206, v138, v160, vcc
	v_cndmask_b32_e32 v212, v136, v159, vcc
	v_cndmask_b32_e32 v135, v134, v157, vcc
	v_cndmask_b32_e32 v141, v140, v158, vcc
	v_lshl_add_u64 v[214:215], v[144:145], 0, s[24:25]
	s_add_i32 m0, s57, 0xc000
	ds_read_b128 v[194:197], v156
	ds_read_b128 v[198:201], v156 offset:1024
	ds_read_b128 v[202:205], v156 offset:2048
	ds_read_b128 v[208:211], v156 offset:3072
	ds_read_b128 v[216:219], v156 offset:4096
	ds_read_b128 v[220:223], v156 offset:5120
	ds_read_b128 v[224:227], v156 offset:6144
	ds_read_b128 v[228:231], v156 offset:7168
	global_load_lds_dwordx4 v[214:215], off
	v_lshl_add_u64 v[214:215], v[142:143], 0, s[24:25]
	s_add_i32 m0, s57, 0xe000
	s_nop 0
	global_load_lds_dwordx4 v[214:215], off
	s_waitcnt vmcnt(8)
	s_waitcnt lgkmcnt(0)
	s_barrier
	s_setprio 1
	s_waitcnt lgkmcnt(0)
	v_mfma_f32_16x16x32_bf16 v[126:129], v[162:165], v[194:197], v[126:129]
	v_mfma_f32_16x16x32_bf16 v[122:125], v[170:173], v[194:197], v[122:125]
	v_mfma_f32_16x16x32_bf16 v[110:113], v[162:165], v[202:205], v[110:113]
	v_mfma_f32_16x16x32_bf16 v[106:109], v[170:173], v[202:205], v[106:109]
	v_mfma_f32_16x16x32_bf16 v[94:97], v[162:165], v[216:219], v[94:97]
	v_mfma_f32_16x16x32_bf16 v[90:93], v[170:173], v[216:219], v[90:93]
	v_mfma_f32_16x16x32_bf16 v[78:81], v[162:165], v[224:227], v[78:81]
	v_mfma_f32_16x16x32_bf16 v[74:77], v[170:173], v[224:227], v[74:77]
	v_mfma_f32_16x16x32_bf16 v[126:129], v[166:169], v[198:201], v[126:129]
	v_mfma_f32_16x16x32_bf16 v[122:125], v[174:177], v[198:201], v[122:125]
	v_mfma_f32_16x16x32_bf16 v[110:113], v[166:169], v[208:211], v[110:113]
	v_mfma_f32_16x16x32_bf16 v[106:109], v[174:177], v[208:211], v[106:109]
	v_mfma_f32_16x16x32_bf16 v[94:97], v[166:169], v[220:223], v[94:97]
	v_mfma_f32_16x16x32_bf16 v[90:93], v[174:177], v[220:223], v[90:93]
	v_mfma_f32_16x16x32_bf16 v[78:81], v[166:169], v[228:231], v[78:81]
	v_mfma_f32_16x16x32_bf16 v[74:77], v[174:177], v[228:231], v[74:77]
	v_mfma_f32_16x16x32_bf16 v[118:121], v[178:181], v[194:197], v[118:121]
	v_mfma_f32_16x16x32_bf16 v[114:117], v[186:189], v[194:197], v[114:117]
	v_mfma_f32_16x16x32_bf16 v[102:105], v[178:181], v[202:205], v[102:105]
	v_mfma_f32_16x16x32_bf16 v[98:101], v[186:189], v[202:205], v[98:101]
	v_mfma_f32_16x16x32_bf16 v[86:89], v[178:181], v[216:219], v[86:89]
	v_mfma_f32_16x16x32_bf16 v[82:85], v[186:189], v[216:219], v[82:85]
	v_mfma_f32_16x16x32_bf16 v[70:73], v[178:181], v[224:227], v[70:73]
	v_mfma_f32_16x16x32_bf16 v[66:69], v[186:189], v[224:227], v[66:69]
	v_mfma_f32_16x16x32_bf16 v[118:121], v[182:185], v[198:201], v[118:121]
	v_mfma_f32_16x16x32_bf16 v[114:117], v[190:193], v[198:201], v[114:117]
	v_mfma_f32_16x16x32_bf16 v[102:105], v[182:185], v[208:211], v[102:105]
	v_mfma_f32_16x16x32_bf16 v[98:101], v[190:193], v[208:211], v[98:101]
	v_mfma_f32_16x16x32_bf16 v[86:89], v[182:185], v[220:223], v[86:89]
	v_mfma_f32_16x16x32_bf16 v[82:85], v[190:193], v[220:223], v[82:85]
	v_mfma_f32_16x16x32_bf16 v[70:73], v[182:185], v[228:231], v[70:73]
	v_mfma_f32_16x16x32_bf16 v[66:69], v[190:193], v[228:231], v[66:69]
	s_setprio 0
	s_barrier
	s_add_i32 s19, s19, s56
	v_lshl_add_u64 v[214:215], s[0:1], 0, v[130:131]
	s_mov_b32 m0, s19
	ds_read_b128 v[194:197], v156 offset:16384
	ds_read_b128 v[198:201], v156 offset:17408
	ds_read_b128 v[202:205], v156 offset:18432
	ds_read_b128 v[208:211], v156 offset:19456
	ds_read_b128 v[216:219], v156 offset:20480
	ds_read_b128 v[220:223], v156 offset:21504
	ds_read_b128 v[224:227], v156 offset:22528
	ds_read_b128 v[228:231], v156 offset:23552
	global_load_lds_dwordx4 v[214:215], off
	s_add_i32 m0, s19, 0x2000
	s_add_u32 s20, s0, 0x80000
	v_lshl_add_u64 v[232:233], s[0:1], 0, v[132:133]
	s_addc_u32 s21, s1, 0
	s_add_i32 s19, s22, s56
	global_load_lds_dwordx4 v[232:233], off
	v_lshl_add_u64 v[234:235], s[20:21], 0, v[130:131]
	s_mov_b32 m0, s19
	v_mov_b32_e32 v213, v207
	global_load_lds_dwordx4 v[234:235], off
	v_lshl_add_u64 v[234:235], s[20:21], 0, v[132:133]
	s_add_i32 m0, s19, 0x2000
	s_nop 0
	global_load_lds_dwordx4 v[234:235], off
	s_mov_b32 m0, s57
	v_lshl_add_u64 v[234:235], s[30:31], 0, v[206:207]
	global_load_lds_dwordx4 v206, s[30:31]
	s_mov_b32 m0, s58
	s_nop 0
	global_load_lds_dwordx4 v212, s[30:31]
	s_waitcnt vmcnt(8)
	s_waitcnt lgkmcnt(0)
	v_lshl_add_u64 v[212:213], s[30:31], 0, v[212:213]
	s_barrier
; #define PG8_STAGE_A(bufoff, kptr, half, VO) do { if constexpr (GATHER) { _Pragma("unroll") for (int _i = 0; _i < 2; ++_i) \
;         __builtin_amdgcn_global_load_lds((const unsigned*)((const char*)(kptr) + (VO)[half][_i]), (LAS unsigned*)(lds + (bufoff) + ldsw + _i * 8192), 16, 0, 0); } \
;         else { PG8_STAGE(bufoff, (kptr) + (half) * hstepA, voffA); } } while (0)
; #define PG8_LDA(dst, b, h) do { _Pragma("unroll") for (int m = 0; m < 4; ++m) _Pragma("unroll") for (int k = 0; k < 2; ++k) dst[m][k] = *(const LAS bf16x8*)(lds + PG8_SA(b, h) + aoff + m * 2048 + k * 1024); } while (0)
; #define PG8_LDB(dst, b, h) do { _Pragma("unroll") for (int n = 0; n < 2; ++n) _Pragma("unroll") for (int k = 0; k < 2; ++k) dst[n][k] = *(const LAS bf16x8*)(lds + PG8_SB(b, h) + boff + n * 2048 + k * 1024); } while (0)
; #define PG8_MMA(ai, bj, At, Bt) do { __builtin_amdgcn_s_setprio(1); _Pragma("unroll") for (int m = 0; m < 4; ++m) _Pragma("unroll") for (int n = 0; n < 2; ++n) _Pragma("unroll") for (int k = 0; k < 2; ++k) \
;         acc[ai][bj][m][n] = __builtin_amdgcn_mfma_f32_16x16x32_bf16(Bt[n][k], At[m][k], acc[ai][bj][m][n], 0, 0, 0); __builtin_amdgcn_s_setprio(0); } while (0)
; #define PG8_WAIT_V(n) asm volatile("s_waitcnt vmcnt(" #n ")" ::: "memory")
; #define PG8_WAIT_L(n) asm volatile("s_waitcnt lgkmcnt(" #n ")" ::: "memory")
; #define PG8_BAR __builtin_amdgcn_s_barrier()
; #define PG8_SCHED __builtin_amdgcn_sched_barrier(0)
;     ...
;             PG8_WAIT_V(8); PG8_WAIT_L(0); PG8_BAR; PG8_MMA(1, 0, At, B0); PG8_MMA(1, 1, At, B1); PG8_BAR; PG8_SCHED;
;             PG8_LDB(B0, 1, 0); PG8_LDB(B1, 1, 1); PG8_SCHED; PG8_LDA(At, 1, 0); PG8_STAGE_A(PG8_SA(0, 1), a2, 1, g2);
;             PG8_WAIT_V(8); PG8_WAIT_L(0); PG8_BAR; PG8_MMA(0, 0, At, B0); PG8_MMA(0, 1, At, B1); PG8_BAR; PG8_SCHED;
	s_setprio 1
	s_waitcnt lgkmcnt(0)
	v_mfma_f32_16x16x32_bf16 v[62:65], v[162:165], v[194:197], v[62:65]
	v_mfma_f32_16x16x32_bf16 v[58:61], v[170:173], v[194:197], v[58:61]
	v_mfma_f32_16x16x32_bf16 v[46:49], v[162:165], v[202:205], v[46:49]
	v_mfma_f32_16x16x32_bf16 v[42:45], v[170:173], v[202:205], v[42:45]
	v_mfma_f32_16x16x32_bf16 v[30:33], v[162:165], v[216:219], v[30:33]
	v_mfma_f32_16x16x32_bf16 v[26:29], v[170:173], v[216:219], v[26:29]
	v_mfma_f32_16x16x32_bf16 v[14:17], v[162:165], v[224:227], v[14:17]
	v_mfma_f32_16x16x32_bf16 v[10:13], v[170:173], v[224:227], v[10:13]
	v_mfma_f32_16x16x32_bf16 v[62:65], v[166:169], v[198:201], v[62:65]
	v_mfma_f32_16x16x32_bf16 v[58:61], v[174:177], v[198:201], v[58:61]
	v_mfma_f32_16x16x32_bf16 v[46:49], v[166:169], v[208:211], v[46:49]
	v_mfma_f32_16x16x32_bf16 v[42:45], v[174:177], v[208:211], v[42:45]
	v_mfma_f32_16x16x32_bf16 v[30:33], v[166:169], v[220:223], v[30:33]
	v_mfma_f32_16x16x32_bf16 v[26:29], v[174:177], v[220:223], v[26:29]
	v_mfma_f32_16x16x32_bf16 v[14:17], v[166:169], v[228:231], v[14:17]
	v_mfma_f32_16x16x32_bf16 v[10:13], v[174:177], v[228:231], v[10:13]
	v_mfma_f32_16x16x32_bf16 v[54:57], v[178:181], v[194:197], v[54:57]
	v_mfma_f32_16x16x32_bf16 v[50:53], v[186:189], v[194:197], v[50:53]
	v_mfma_f32_16x16x32_bf16 v[38:41], v[178:181], v[202:205], v[38:41]
	v_mfma_f32_16x16x32_bf16 v[34:37], v[186:189], v[202:205], v[34:37]
	v_mfma_f32_16x16x32_bf16 v[22:25], v[178:181], v[216:219], v[22:25]
	v_mfma_f32_16x16x32_bf16 v[18:21], v[186:189], v[216:219], v[18:21]
	v_mfma_f32_16x16x32_bf16 v[6:9], v[178:181], v[224:227], v[6:9]
	v_mfma_f32_16x16x32_bf16 v[2:5], v[186:189], v[224:227], v[2:5]
	v_mfma_f32_16x16x32_bf16 v[54:57], v[182:185], v[198:201], v[54:57]
	v_mfma_f32_16x16x32_bf16 v[50:53], v[190:193], v[198:201], v[50:53]
	v_mfma_f32_16x16x32_bf16 v[38:41], v[182:185], v[208:211], v[38:41]
	v_mfma_f32_16x16x32_bf16 v[34:37], v[190:193], v[208:211], v[34:37]
	v_mfma_f32_16x16x32_bf16 v[22:25], v[182:185], v[220:223], v[22:25]
	v_mfma_f32_16x16x32_bf16 v[18:21], v[190:193], v[220:223], v[18:21]
	v_mfma_f32_16x16x32_bf16 v[6:9], v[182:185], v[228:231], v[6:9]
	v_mfma_f32_16x16x32_bf16 v[2:5], v[190:193], v[228:231], v[2:5]
	s_setprio 0
	s_barrier
	s_add_i32 s19, 0, 0x18000
	v_add_u32_e32 v161, s19, v139
	s_add_i32 s20, 0, 0x1c000
	ds_read_b128 v[162:165], v161
	ds_read_b128 v[166:169], v161 offset:1024
	ds_read_b128 v[170:173], v161 offset:2048
	ds_read_b128 v[174:177], v161 offset:3072
	v_add_u32_e32 v161, s20, v139
	ds_read_b128 v[178:181], v161
	ds_read_b128 v[182:185], v161 offset:1024
	ds_read_b128 v[186:189], v161 offset:2048
	ds_read_b128 v[190:193], v161 offset:3072
	s_mov_b32 m0, s59
	ds_read_b128 v[194:197], v156 offset:32768
	ds_read_b128 v[198:201], v156 offset:33792
	ds_read_b128 v[202:205], v156 offset:34816
	ds_read_b128 v[208:211], v156 offset:35840
	ds_read_b128 v[216:219], v156 offset:36864
	ds_read_b128 v[220:223], v156 offset:37888
	ds_read_b128 v[224:227], v156 offset:38912
	ds_read_b128 v[228:231], v156 offset:39936
	global_load_lds_dwordx4 v135, s[30:31]
	s_mov_b32 m0, s60
	s_nop 0
	global_load_lds_dwordx4 v141, s[30:31]
	s_waitcnt vmcnt(8)
	s_waitcnt lgkmcnt(0)
	s_barrier
	s_setprio 1
	s_waitcnt lgkmcnt(0)
	v_mfma_f32_16x16x32_bf16 v[126:129], v[162:165], v[194:197], v[126:129]
	v_mfma_f32_16x16x32_bf16 v[122:125], v[170:173], v[194:197], v[122:125]
	v_mfma_f32_16x16x32_bf16 v[110:113], v[162:165], v[202:205], v[110:113]
	v_mfma_f32_16x16x32_bf16 v[106:109], v[170:173], v[202:205], v[106:109]
	v_mfma_f32_16x16x32_bf16 v[94:97], v[162:165], v[216:219], v[94:97]
	v_mfma_f32_16x16x32_bf16 v[90:93], v[170:173], v[216:219], v[90:93]
	v_mfma_f32_16x16x32_bf16 v[78:81], v[162:165], v[224:227], v[78:81]
	v_mfma_f32_16x16x32_bf16 v[74:77], v[170:173], v[224:227], v[74:77]
	v_mfma_f32_16x16x32_bf16 v[126:129], v[166:169], v[198:201], v[126:129]
	v_mfma_f32_16x16x32_bf16 v[122:125], v[174:177], v[198:201], v[122:125]
	v_mfma_f32_16x16x32_bf16 v[110:113], v[166:169], v[208:211], v[110:113]
	v_mfma_f32_16x16x32_bf16 v[106:109], v[174:177], v[208:211], v[106:109]
	v_mfma_f32_16x16x32_bf16 v[94:97], v[166:169], v[220:223], v[94:97]
	v_mfma_f32_16x16x32_bf16 v[90:93], v[174:177], v[220:223], v[90:93]
	v_mfma_f32_16x16x32_bf16 v[78:81], v[166:169], v[228:231], v[78:81]
	v_mfma_f32_16x16x32_bf16 v[74:77], v[174:177], v[228:231], v[74:77]
	v_mfma_f32_16x16x32_bf16 v[118:121], v[178:181], v[194:197], v[118:121]
	v_mfma_f32_16x16x32_bf16 v[114:117], v[186:189], v[194:197], v[114:117]
	v_mfma_f32_16x16x32_bf16 v[102:105], v[178:181], v[202:205], v[102:105]
	v_mfma_f32_16x16x32_bf16 v[98:101], v[186:189], v[202:205], v[98:101]
	v_mfma_f32_16x16x32_bf16 v[86:89], v[178:181], v[216:219], v[86:89]
	v_mfma_f32_16x16x32_bf16 v[82:85], v[186:189], v[216:219], v[82:85]
	v_mfma_f32_16x16x32_bf16 v[70:73], v[178:181], v[224:227], v[70:73]
	v_mfma_f32_16x16x32_bf16 v[66:69], v[186:189], v[224:227], v[66:69]
	v_mfma_f32_16x16x32_bf16 v[118:121], v[182:185], v[198:201], v[118:121]
	v_mfma_f32_16x16x32_bf16 v[114:117], v[190:193], v[198:201], v[114:117]
	v_mfma_f32_16x16x32_bf16 v[102:105], v[182:185], v[208:211], v[102:105]
	v_mfma_f32_16x16x32_bf16 v[98:101], v[190:193], v[208:211], v[98:101]
	v_mfma_f32_16x16x32_bf16 v[86:89], v[182:185], v[220:223], v[86:89]
	v_mfma_f32_16x16x32_bf16 v[82:85], v[190:193], v[220:223], v[82:85]
	v_mfma_f32_16x16x32_bf16 v[70:73], v[182:185], v[228:231], v[70:73]
	v_mfma_f32_16x16x32_bf16 v[66:69], v[190:193], v[228:231], v[66:69]
	s_setprio 0
	s_barrier
; #define PG8_STAGE(bufoff, gbase, voff) do { _Pragma("unroll") for (int _i = 0; _i < 2; ++_i) \
;         __builtin_amdgcn_global_load_lds((const unsigned*)((const char*)(gbase) + (voff)[_i]), (LAS unsigned*)(lds + (bufoff) + ldsw + _i * 8192), 16, 0, 0); } while (0)
; #define PG8_STAGE_A(bufoff, kptr, half, VO) do { if constexpr (GATHER) { _Pragma("unroll") for (int _i = 0; _i < 2; ++_i) \
;         __builtin_amdgcn_global_load_lds((const unsigned*)((const char*)(kptr) + (VO)[half][_i]), (LAS unsigned*)(lds + (bufoff) + ldsw + _i * 8192), 16, 0, 0); } \
;         else { PG8_STAGE(bufoff, (kptr) + (half) * hstepA, voffA); } } while (0)
; #define PG8_LDA(dst, b, h) do { _Pragma("unroll") for (int m = 0; m < 4; ++m) _Pragma("unroll") for (int k = 0; k < 2; ++k) dst[m][k] = *(const LAS bf16x8*)(lds + PG8_SA(b, h) + aoff + m * 2048 + k * 1024); } while (0)
; #define PG8_MMA(ai, bj, At, Bt) do { __builtin_amdgcn_s_setprio(1); _Pragma("unroll") for (int m = 0; m < 4; ++m) _Pragma("unroll") for (int n = 0; n < 2; ++n) _Pragma("unroll") for (int k = 0; k < 2; ++k) \
;         acc[ai][bj][m][n] = __builtin_amdgcn_mfma_f32_16x16x32_bf16(Bt[n][k], At[m][k], acc[ai][bj][m][n], 0, 0, 0); __builtin_amdgcn_s_setprio(0); } while (0)
; #define PG8_WAIT_V(n) asm volatile("s_waitcnt vmcnt(" #n ")" ::: "memory")
; #define PG8_WAIT_L(n) asm volatile("s_waitcnt lgkmcnt(" #n ")" ::: "memory")
; #define PG8_BAR __builtin_amdgcn_s_barrier()
; #define PG8_SCHED __builtin_amdgcn_sched_barrier(0)
;     ...
;             PG8_LDA(At, 1, 1); PG8_STAGE(PG8_SB(1, 0), b3, voffB); PG8_STAGE(PG8_SB(1, 1), b3 + hstepB, voffB); PG8_STAGE_A(PG8_SA(1, 0), a3, 0, g2);
;             PG8_WAIT_V(8); PG8_WAIT_L(0); PG8_BAR; PG8_MMA(1, 0, At, B0); PG8_MMA(1, 1, At, B1); PG8_BAR; PG8_SCHED;
	s_add_i32 s19, s19, s56
	v_lshl_add_u64 v[214:215], v[214:215], 0, s[8:9]
	s_mov_b32 m0, s19
	ds_read_b128 v[194:197], v156 offset:49152
	ds_read_b128 v[198:201], v156 offset:50176
	ds_read_b128 v[202:205], v156 offset:51200
	ds_read_b128 v[208:211], v156 offset:52224
	ds_read_b128 v[216:219], v156 offset:53248
	ds_read_b128 v[220:223], v156 offset:54272
	ds_read_b128 v[224:227], v156 offset:55296
	ds_read_b128 v[228:231], v156 offset:56320
	global_load_lds_dwordx4 v[214:215], off
	s_add_i32 m0, s19, 0x2000
	s_add_u32 s0, s0, 0x80080
	v_lshl_add_u64 v[214:215], v[232:233], 0, s[8:9]
	s_addc_u32 s1, s1, 0
	s_add_i32 s19, s20, s56
	global_load_lds_dwordx4 v[214:215], off
	v_lshl_add_u64 v[214:215], s[0:1], 0, v[130:131]
	s_mov_b32 m0, s19
	v_lshl_add_u64 v[212:213], v[212:213], 0, s[8:9]
	global_load_lds_dwordx4 v[214:215], off
	v_lshl_add_u64 v[214:215], s[0:1], 0, v[132:133]
	s_add_i32 m0, s19, 0x2000
	s_nop 0
	global_load_lds_dwordx4 v[214:215], off
	v_lshl_add_u64 v[214:215], v[234:235], 0, s[8:9]
	s_mov_b32 m0, s63
	s_nop 0
	global_load_lds_dwordx4 v[214:215], off
	s_mov_b32 m0, s64
	s_nop 0
	global_load_lds_dwordx4 v[212:213], off
	s_waitcnt vmcnt(8)
	s_waitcnt lgkmcnt(0)
	s_barrier
	s_setprio 1
	s_waitcnt lgkmcnt(0)
	v_mfma_f32_16x16x32_bf16 v[62:65], v[162:165], v[194:197], v[62:65]
	v_mfma_f32_16x16x32_bf16 v[58:61], v[170:173], v[194:197], v[58:61]
	v_mfma_f32_16x16x32_bf16 v[46:49], v[162:165], v[202:205], v[46:49]
	v_mfma_f32_16x16x32_bf16 v[42:45], v[170:173], v[202:205], v[42:45]
	v_mfma_f32_16x16x32_bf16 v[30:33], v[162:165], v[216:219], v[30:33]
	v_mfma_f32_16x16x32_bf16 v[26:29], v[170:173], v[216:219], v[26:29]
	v_mfma_f32_16x16x32_bf16 v[14:17], v[162:165], v[224:227], v[14:17]
	v_mfma_f32_16x16x32_bf16 v[10:13], v[170:173], v[224:227], v[10:13]
	v_mfma_f32_16x16x32_bf16 v[62:65], v[166:169], v[198:201], v[62:65]
	v_mfma_f32_16x16x32_bf16 v[58:61], v[174:177], v[198:201], v[58:61]
	v_mfma_f32_16x16x32_bf16 v[46:49], v[166:169], v[208:211], v[46:49]
	v_mfma_f32_16x16x32_bf16 v[42:45], v[174:177], v[208:211], v[42:45]
	v_mfma_f32_16x16x32_bf16 v[30:33], v[166:169], v[220:223], v[30:33]
	v_mfma_f32_16x16x32_bf16 v[26:29], v[174:177], v[220:223], v[26:29]
	v_mfma_f32_16x16x32_bf16 v[14:17], v[166:169], v[228:231], v[14:17]
	v_mfma_f32_16x16x32_bf16 v[10:13], v[174:177], v[228:231], v[10:13]
	v_mfma_f32_16x16x32_bf16 v[54:57], v[178:181], v[194:197], v[54:57]
	v_mfma_f32_16x16x32_bf16 v[50:53], v[186:189], v[194:197], v[50:53]
	v_mfma_f32_16x16x32_bf16 v[38:41], v[178:181], v[202:205], v[38:41]
	v_mfma_f32_16x16x32_bf16 v[34:37], v[186:189], v[202:205], v[34:37]
	v_mfma_f32_16x16x32_bf16 v[22:25], v[178:181], v[216:219], v[22:25]
	v_mfma_f32_16x16x32_bf16 v[18:21], v[186:189], v[216:219], v[18:21]
	v_mfma_f32_16x16x32_bf16 v[6:9], v[178:181], v[224:227], v[6:9]
	v_mfma_f32_16x16x32_bf16 v[2:5], v[186:189], v[224:227], v[2:5]
	v_mfma_f32_16x16x32_bf16 v[54:57], v[182:185], v[198:201], v[54:57]
	v_mfma_f32_16x16x32_bf16 v[50:53], v[190:193], v[198:201], v[50:53]
	v_mfma_f32_16x16x32_bf16 v[38:41], v[182:185], v[208:211], v[38:41]
	v_mfma_f32_16x16x32_bf16 v[34:37], v[190:193], v[208:211], v[34:37]
	v_mfma_f32_16x16x32_bf16 v[22:25], v[182:185], v[220:223], v[22:25]
	v_mfma_f32_16x16x32_bf16 v[18:21], v[190:193], v[220:223], v[18:21]
	v_mfma_f32_16x16x32_bf16 v[6:9], v[182:185], v[228:231], v[6:9]
	v_mfma_f32_16x16x32_bf16 v[2:5], v[190:193], v[228:231], v[2:5]
	s_setprio 0
	s_barrier
	s_add_i32 s18, s18, 2
	s_add_u32 s24, s24, 0x100
	s_addc_u32 s25, s25, 0
	s_cmp_gt_u32 s18, 29
	s_cbranch_scc0 .LBB0_2265
	s_and_b64 vcc, exec, s[42:43]
	s_cbranch_vccz .LBB0_2268
	s_barrier

; #define PG8_STAGE(bufoff, gbase, voff) do { _Pragma("unroll") for (int _i = 0; _i < 2; ++_i) \
;         __builtin_amdgcn_global_load_lds((const unsigned*)((const char*)(gbase) + (voff)[_i]), (LAS unsigned*)(lds + (bufoff) + ldsw + _i * 8192), 16, 0, 0); } while (0)
; #define PG8_STAGE_A(bufoff, kptr, half, VO) do { if constexpr (GATHER) { _Pragma("unroll") for (int _i = 0; _i < 2; ++_i) \
;         __builtin_amdgcn_global_load_lds((const unsigned*)((const char*)(kptr) + (VO)[half][_i]), (LAS unsigned*)(lds + (bufoff) + ldsw + _i * 8192), 16, 0, 0); } \
;         else { PG8_STAGE(bufoff, (kptr) + (half) * hstepA, voffA); } } while (0)
; #define PG8_LDA(dst, b, h) do { _Pragma("unroll") for (int m = 0; m < 4; ++m) _Pragma("unroll") for (int k = 0; k < 2; ++k) dst[m][k] = *(const LAS bf16x8*)(lds + PG8_SA(b, h) + aoff + m * 2048 + k * 1024); } while (0)
; #define PG8_LDB(dst, b, h) do { _Pragma("unroll") for (int n = 0; n < 2; ++n) _Pragma("unroll") for (int k = 0; k < 2; ++k) dst[n][k] = *(const LAS bf16x8*)(lds + PG8_SB(b, h) + boff + n * 2048 + k * 1024); } while (0)
; #define PG8_WAIT_V(n) asm volatile("s_waitcnt vmcnt(" #n ")" ::: "memory")
; #define PG8_WAIT_L(n) asm volatile("s_waitcnt lgkmcnt(" #n ")" ::: "memory")
; #define PG8_BAR __builtin_amdgcn_s_barrier()
;     ...
;             const char* a1 = cA + (size_t)(t + 1) * kstep;
;             const char* a2 = last ? nA : cA + (size_t)(t + 2) * kstep; const char* b2 = last ? nB : cB + (size_t)(t + 2) * kstep;
;             const char* a3 = a2 + kstep; const char* b3 = b2 + kstep;
;             unsigned g2[2][2];
;             if constexpr (GATHER) {
; #pragma unroll
;                 for (int _h = 0; _h < 2; ++_h)
; #pragma unroll
;                     for (int _i = 0; _i < 2; ++_i) g2[_h][_i] = last ? gN[_h][_i] : gC[_h][_i]; }
;             if constexpr (SP2) {
;             PG8_LDB(B0, 0, 0); PG8_LDB(B1, 0, 1); PG8_SCHED; PG8_LDA(At, 0, 0); PG8_STAGE_A(PG8_SA(1, 1), a1, 1, gC);
;             PG8_WAIT_V(8); PG8_WAIT_L(0); PG8_BAR; PG8_MMA(0, 0, At, B0); PG8_MMA(0, 1, At, B1); PG8_BAR; PG8_SCHED;
;             PG8_LDA(At, 0, 1); PG8_STAGE(PG8_SB(0, 0), b2, voffB); PG8_STAGE(PG8_SB(0, 1), b2 + hstepB, voffB); PG8_STAGE_A(PG8_SA(0, 0), a2, 0, g2);
;             PG8_WAIT_V(8); PG8_WAIT_L(0); PG8_BAR; PG8_MMA(1, 0, At, B0); PG8_MMA(1, 1, At, B1); PG8_BAR; PG8_SCHED;
.LBB0_2458:
	s_add_u32 s0, s24, 0xfffc0080
	s_addc_u32 s1, s25, -1
	s_add_i32 s19, 0, 0x10000
	s_cmp_eq_u32 s18, 12
	s_cselect_b32 s31, s12, s1
	s_cselect_b32 s30, s13, s0
	v_add_u32_e32 v140, s19, v145
	s_cselect_b32 s1, s14, s17
	s_cselect_b32 s0, s15, s16
	s_add_i32 s22, 0, 0x14000
	ds_read_b128 v[156:159], v140
	ds_read_b128 v[160:163], v140 offset:1024
	ds_read_b128 v[164:167], v140 offset:2048
	ds_read_b128 v[168:171], v140 offset:3072
	v_add_u32_e32 v140, s22, v145
	ds_read_b128 v[172:175], v140
	ds_read_b128 v[176:179], v140 offset:1024
	ds_read_b128 v[180:183], v140 offset:2048
	ds_read_b128 v[184:187], v140 offset:3072
	v_lshl_add_u64 v[142:143], s[24:25], 0, v[136:137]
	s_add_i32 m0, s37, 0xc000
	ds_read_b128 v[188:191], v155
	ds_read_b128 v[192:195], v155 offset:1024
	ds_read_b128 v[196:199], v155 offset:2048
	ds_read_b128 v[200:203], v155 offset:3072
	ds_read_b128 v[208:211], v155 offset:4096
	ds_read_b128 v[216:219], v155 offset:5120
	ds_read_b128 v[220:223], v155 offset:6144
	ds_read_b128 v[224:227], v155 offset:7168
	global_load_lds_dwordx4 v[142:143], off
	v_lshl_add_u64 v[142:143], s[24:25], 0, v[138:139]
	s_add_i32 m0, s37, 0xe000
	s_nop 0
	global_load_lds_dwordx4 v[142:143], off
	s_waitcnt vmcnt(8)
	s_waitcnt lgkmcnt(0)
	s_barrier
	s_setprio 1
	s_waitcnt lgkmcnt(0)
	v_mfma_f32_16x16x32_bf16 v[126:129], v[156:159], v[188:191], v[126:129]
	v_mfma_f32_16x16x32_bf16 v[122:125], v[164:167], v[188:191], v[122:125]
	v_mfma_f32_16x16x32_bf16 v[110:113], v[156:159], v[196:199], v[110:113]
	v_mfma_f32_16x16x32_bf16 v[106:109], v[164:167], v[196:199], v[106:109]
	v_mfma_f32_16x16x32_bf16 v[94:97], v[156:159], v[208:211], v[94:97]
	v_mfma_f32_16x16x32_bf16 v[90:93], v[164:167], v[208:211], v[90:93]
	v_mfma_f32_16x16x32_bf16 v[86:89], v[156:159], v[220:223], v[86:89]
	v_mfma_f32_16x16x32_bf16 v[78:81], v[164:167], v[220:223], v[78:81]
	v_mfma_f32_16x16x32_bf16 v[126:129], v[160:163], v[192:195], v[126:129]
	v_mfma_f32_16x16x32_bf16 v[122:125], v[168:171], v[192:195], v[122:125]
	v_mfma_f32_16x16x32_bf16 v[110:113], v[160:163], v[200:203], v[110:113]
	v_mfma_f32_16x16x32_bf16 v[106:109], v[168:171], v[200:203], v[106:109]
	v_mfma_f32_16x16x32_bf16 v[94:97], v[160:163], v[216:219], v[94:97]
	v_mfma_f32_16x16x32_bf16 v[90:93], v[168:171], v[216:219], v[90:93]
	v_mfma_f32_16x16x32_bf16 v[86:89], v[160:163], v[224:227], v[86:89]
	v_mfma_f32_16x16x32_bf16 v[78:81], v[168:171], v[224:227], v[78:81]
	v_mfma_f32_16x16x32_bf16 v[118:121], v[172:175], v[188:191], v[118:121]
	v_mfma_f32_16x16x32_bf16 v[114:117], v[180:183], v[188:191], v[114:117]
	v_mfma_f32_16x16x32_bf16 v[102:105], v[172:175], v[196:199], v[102:105]
	v_mfma_f32_16x16x32_bf16 v[98:101], v[180:183], v[196:199], v[98:101]
	v_mfma_f32_16x16x32_bf16 v[82:85], v[172:175], v[208:211], v[82:85]
	v_mfma_f32_16x16x32_bf16 v[74:77], v[180:183], v[208:211], v[74:77]
	v_mfma_f32_16x16x32_bf16 v[70:73], v[172:175], v[220:223], v[70:73]
	v_mfma_f32_16x16x32_bf16 v[66:69], v[180:183], v[220:223], v[66:69]
	v_mfma_f32_16x16x32_bf16 v[118:121], v[176:179], v[192:195], v[118:121]
	v_mfma_f32_16x16x32_bf16 v[114:117], v[184:187], v[192:195], v[114:117]
	v_mfma_f32_16x16x32_bf16 v[102:105], v[176:179], v[200:203], v[102:105]
	v_mfma_f32_16x16x32_bf16 v[98:101], v[184:187], v[200:203], v[98:101]
	v_mfma_f32_16x16x32_bf16 v[82:85], v[176:179], v[216:219], v[82:85]
	v_mfma_f32_16x16x32_bf16 v[74:77], v[184:187], v[216:219], v[74:77]
	v_mfma_f32_16x16x32_bf16 v[70:73], v[176:179], v[224:227], v[70:73]
	v_mfma_f32_16x16x32_bf16 v[66:69], v[184:187], v[224:227], v[66:69]
	s_setprio 0
	s_barrier
	s_add_i32 s19, s19, s62
	v_lshl_add_u64 v[142:143], s[0:1], 0, v[206:207]
	s_mov_b32 m0, s19
	ds_read_b128 v[188:191], v155 offset:16384
	ds_read_b128 v[192:195], v155 offset:17408
	ds_read_b128 v[196:199], v155 offset:18432
	ds_read_b128 v[200:203], v155 offset:19456
	ds_read_b128 v[208:211], v155 offset:20480
	ds_read_b128 v[216:219], v155 offset:21504
	ds_read_b128 v[220:223], v155 offset:22528
	ds_read_b128 v[224:227], v155 offset:23552
	global_load_lds_dwordx4 v[142:143], off
	s_add_i32 m0, s19, 0x2000
	s_add_u32 s20, s0, 0x40000
	v_lshl_add_u64 v[204:205], s[0:1], 0, v[134:135]
	s_addc_u32 s21, s1, 0
	s_add_i32 s19, s22, s62
	global_load_lds_dwordx4 v[204:205], off
	v_lshl_add_u64 v[212:213], s[20:21], 0, v[206:207]
	s_mov_b32 m0, s19
	v_lshl_add_u64 v[214:215], s[30:31], 0, v[132:133]
	global_load_lds_dwordx4 v[212:213], off
	v_lshl_add_u64 v[212:213], s[20:21], 0, v[134:135]
	s_add_i32 m0, s19, 0x2000
	s_nop 0
	global_load_lds_dwordx4 v[212:213], off
	v_lshl_add_u64 v[212:213], s[30:31], 0, v[130:131]
	s_mov_b32 m0, s37
	s_nop 0
	global_load_lds_dwordx4 v[212:213], off
	s_mov_b32 m0, s65
	s_nop 0
	global_load_lds_dwordx4 v[214:215], off
	s_waitcnt vmcnt(8)
	s_waitcnt lgkmcnt(0)
	s_barrier
; #define PG8_STAGE(bufoff, gbase, voff) do { _Pragma("unroll") for (int _i = 0; _i < 2; ++_i) \
;         __builtin_amdgcn_global_load_lds((const unsigned*)((const char*)(gbase) + (voff)[_i]), (LAS unsigned*)(lds + (bufoff) + ldsw + _i * 8192), 16, 0, 0); } while (0)
; #define PG8_STAGE_A(bufoff, kptr, half, VO) do { if constexpr (GATHER) { _Pragma("unroll") for (int _i = 0; _i < 2; ++_i) \
;         __builtin_amdgcn_global_load_lds((const unsigned*)((const char*)(kptr) + (VO)[half][_i]), (LAS unsigned*)(lds + (bufoff) + ldsw + _i * 8192), 16, 0, 0); } \
;         else { PG8_STAGE(bufoff, (kptr) + (half) * hstepA, voffA); } } while (0)
; #define PG8_LDA(dst, b, h) do { _Pragma("unroll") for (int m = 0; m < 4; ++m) _Pragma("unroll") for (int k = 0; k < 2; ++k) dst[m][k] = *(const LAS bf16x8*)(lds + PG8_SA(b, h) + aoff + m * 2048 + k * 1024); } while (0)
; #define PG8_LDB(dst, b, h) do { _Pragma("unroll") for (int n = 0; n < 2; ++n) _Pragma("unroll") for (int k = 0; k < 2; ++k) dst[n][k] = *(const LAS bf16x8*)(lds + PG8_SB(b, h) + boff + n * 2048 + k * 1024); } while (0)
; #define PG8_WAIT_V(n) asm volatile("s_waitcnt vmcnt(" #n ")" ::: "memory")
; #define PG8_WAIT_L(n) asm volatile("s_waitcnt lgkmcnt(" #n ")" ::: "memory")
; #define PG8_BAR __builtin_amdgcn_s_barrier()
; #define PG8_SCHED __builtin_amdgcn_sched_barrier(0)
;     ...
;             PG8_LDB(B0, 0, 0); PG8_LDB(B1, 0, 1); PG8_SCHED; PG8_LDA(At, 0, 0); PG8_STAGE_A(PG8_SA(1, 1), a1, 1, gC);
;             PG8_WAIT_V(8); PG8_WAIT_L(0); PG8_BAR; PG8_MMA(0, 0, At, B0); PG8_MMA(0, 1, At, B1); PG8_BAR; PG8_SCHED;
;             PG8_LDA(At, 0, 1); PG8_STAGE(PG8_SB(0, 0), b2, voffB); PG8_STAGE(PG8_SB(0, 1), b2 + hstepB, voffB); PG8_STAGE_A(PG8_SA(0, 0), a2, 0, g2);
;             PG8_WAIT_V(8); PG8_WAIT_L(0); PG8_BAR; PG8_MMA(1, 0, At, B0); PG8_MMA(1, 1, At, B1); PG8_BAR; PG8_SCHED;
;             PG8_LDB(B0, 1, 0); PG8_LDB(B1, 1, 1); PG8_SCHED; PG8_LDA(At, 1, 0); PG8_STAGE_A(PG8_SA(0, 1), a2, 1, g2);
;             PG8_WAIT_V(8); PG8_WAIT_L(0); PG8_BAR; PG8_MMA(0, 0, At, B0); PG8_MMA(0, 1, At, B1); PG8_BAR; PG8_SCHED;
;             PG8_LDA(At, 1, 1); PG8_STAGE(PG8_SB(1, 0), b3, voffB); PG8_STAGE(PG8_SB(1, 1), b3 + hstepB, voffB); PG8_STAGE_A(PG8_SA(1, 0), a3, 0, g2);
;             PG8_WAIT_V(8); PG8_WAIT_L(0); PG8_BAR; PG8_MMA(1, 0, At, B0); PG8_MMA(1, 1, At, B1); PG8_BAR; PG8_SCHED;
	s_setprio 1
	s_waitcnt lgkmcnt(0)
	v_mfma_f32_16x16x32_bf16 v[62:65], v[156:159], v[188:191], v[62:65]
	v_mfma_f32_16x16x32_bf16 v[58:61], v[164:167], v[188:191], v[58:61]
	v_mfma_f32_16x16x32_bf16 v[54:57], v[156:159], v[196:199], v[54:57]
	v_mfma_f32_16x16x32_bf16 v[46:49], v[164:167], v[196:199], v[46:49]
	v_mfma_f32_16x16x32_bf16 v[38:41], v[156:159], v[208:211], v[38:41]
	v_mfma_f32_16x16x32_bf16 v[30:33], v[164:167], v[208:211], v[30:33]
	v_mfma_f32_16x16x32_bf16 v[22:25], v[156:159], v[220:223], v[22:25]
	v_mfma_f32_16x16x32_bf16 v[14:17], v[164:167], v[220:223], v[14:17]
	v_mfma_f32_16x16x32_bf16 v[62:65], v[160:163], v[192:195], v[62:65]
	v_mfma_f32_16x16x32_bf16 v[58:61], v[168:171], v[192:195], v[58:61]
	v_mfma_f32_16x16x32_bf16 v[54:57], v[160:163], v[200:203], v[54:57]
	v_mfma_f32_16x16x32_bf16 v[46:49], v[168:171], v[200:203], v[46:49]
	v_mfma_f32_16x16x32_bf16 v[38:41], v[160:163], v[216:219], v[38:41]
	v_mfma_f32_16x16x32_bf16 v[30:33], v[168:171], v[216:219], v[30:33]
	v_mfma_f32_16x16x32_bf16 v[22:25], v[160:163], v[224:227], v[22:25]
	v_mfma_f32_16x16x32_bf16 v[14:17], v[168:171], v[224:227], v[14:17]
	v_mfma_f32_16x16x32_bf16 v[50:53], v[172:175], v[188:191], v[50:53]
	v_mfma_f32_16x16x32_bf16 v[42:45], v[180:183], v[188:191], v[42:45]
	v_mfma_f32_16x16x32_bf16 v[34:37], v[172:175], v[196:199], v[34:37]
	v_mfma_f32_16x16x32_bf16 v[26:29], v[180:183], v[196:199], v[26:29]
	v_mfma_f32_16x16x32_bf16 v[18:21], v[172:175], v[208:211], v[18:21]
	v_mfma_f32_16x16x32_bf16 v[10:13], v[180:183], v[208:211], v[10:13]
	v_mfma_f32_16x16x32_bf16 v[6:9], v[172:175], v[220:223], v[6:9]
	v_mfma_f32_16x16x32_bf16 v[2:5], v[180:183], v[220:223], v[2:5]
	v_mfma_f32_16x16x32_bf16 v[50:53], v[176:179], v[192:195], v[50:53]
	v_mfma_f32_16x16x32_bf16 v[42:45], v[184:187], v[192:195], v[42:45]
	v_mfma_f32_16x16x32_bf16 v[34:37], v[176:179], v[200:203], v[34:37]
	v_mfma_f32_16x16x32_bf16 v[26:29], v[184:187], v[200:203], v[26:29]
	v_mfma_f32_16x16x32_bf16 v[18:21], v[176:179], v[216:219], v[18:21]
	v_mfma_f32_16x16x32_bf16 v[10:13], v[184:187], v[216:219], v[10:13]
	v_mfma_f32_16x16x32_bf16 v[6:9], v[176:179], v[224:227], v[6:9]
	v_mfma_f32_16x16x32_bf16 v[2:5], v[184:187], v[224:227], v[2:5]
	s_setprio 0
	s_barrier
	s_add_i32 s19, 0, 0x18000
	v_add_u32_e32 v140, s19, v145
	s_add_i32 s22, 0, 0x1c000
	ds_read_b128 v[156:159], v140
	ds_read_b128 v[160:163], v140 offset:1024
	ds_read_b128 v[164:167], v140 offset:2048
	ds_read_b128 v[168:171], v140 offset:3072
	v_add_u32_e32 v140, s22, v145
	ds_read_b128 v[172:175], v140
	ds_read_b128 v[176:179], v140 offset:1024
	ds_read_b128 v[180:183], v140 offset:2048
	ds_read_b128 v[184:187], v140 offset:3072
	s_add_u32 s20, s30, 0x40000
	s_addc_u32 s21, s31, 0
	s_mov_b32 m0, s66
	v_lshl_add_u64 v[228:229], s[20:21], 0, v[130:131]
	ds_read_b128 v[188:191], v155 offset:32768
	ds_read_b128 v[192:195], v155 offset:33792
	ds_read_b128 v[196:199], v155 offset:34816
	ds_read_b128 v[200:203], v155 offset:35840
	ds_read_b128 v[208:211], v155 offset:36864
	ds_read_b128 v[216:219], v155 offset:37888
	ds_read_b128 v[220:223], v155 offset:38912
	ds_read_b128 v[224:227], v155 offset:39936
	global_load_lds_dwordx4 v[228:229], off
	v_lshl_add_u64 v[228:229], s[20:21], 0, v[132:133]
	s_mov_b32 m0, s67
	s_nop 0
	global_load_lds_dwordx4 v[228:229], off
	s_waitcnt vmcnt(8)
	s_waitcnt lgkmcnt(0)
	s_barrier
	s_setprio 1
	s_waitcnt lgkmcnt(0)
	v_mfma_f32_16x16x32_bf16 v[126:129], v[156:159], v[188:191], v[126:129]
	v_mfma_f32_16x16x32_bf16 v[122:125], v[164:167], v[188:191], v[122:125]
	v_mfma_f32_16x16x32_bf16 v[110:113], v[156:159], v[196:199], v[110:113]
	v_mfma_f32_16x16x32_bf16 v[106:109], v[164:167], v[196:199], v[106:109]
	v_mfma_f32_16x16x32_bf16 v[94:97], v[156:159], v[208:211], v[94:97]
	v_mfma_f32_16x16x32_bf16 v[90:93], v[164:167], v[208:211], v[90:93]
	v_mfma_f32_16x16x32_bf16 v[86:89], v[156:159], v[220:223], v[86:89]
	v_mfma_f32_16x16x32_bf16 v[78:81], v[164:167], v[220:223], v[78:81]
	v_mfma_f32_16x16x32_bf16 v[126:129], v[160:163], v[192:195], v[126:129]
	v_mfma_f32_16x16x32_bf16 v[122:125], v[168:171], v[192:195], v[122:125]
	v_mfma_f32_16x16x32_bf16 v[110:113], v[160:163], v[200:203], v[110:113]
	v_mfma_f32_16x16x32_bf16 v[106:109], v[168:171], v[200:203], v[106:109]
	v_mfma_f32_16x16x32_bf16 v[94:97], v[160:163], v[216:219], v[94:97]
	v_mfma_f32_16x16x32_bf16 v[90:93], v[168:171], v[216:219], v[90:93]
	v_mfma_f32_16x16x32_bf16 v[86:89], v[160:163], v[224:227], v[86:89]
	v_mfma_f32_16x16x32_bf16 v[78:81], v[168:171], v[224:227], v[78:81]
	v_mfma_f32_16x16x32_bf16 v[118:121], v[172:175], v[188:191], v[118:121]
	v_mfma_f32_16x16x32_bf16 v[114:117], v[180:183], v[188:191], v[114:117]
	v_mfma_f32_16x16x32_bf16 v[102:105], v[172:175], v[196:199], v[102:105]
	v_mfma_f32_16x16x32_bf16 v[98:101], v[180:183], v[196:199], v[98:101]
	v_mfma_f32_16x16x32_bf16 v[82:85], v[172:175], v[208:211], v[82:85]
	v_mfma_f32_16x16x32_bf16 v[74:77], v[180:183], v[208:211], v[74:77]
	v_mfma_f32_16x16x32_bf16 v[70:73], v[172:175], v[220:223], v[70:73]
	v_mfma_f32_16x16x32_bf16 v[66:69], v[180:183], v[220:223], v[66:69]
	v_mfma_f32_16x16x32_bf16 v[118:121], v[176:179], v[192:195], v[118:121]
	v_mfma_f32_16x16x32_bf16 v[114:117], v[184:187], v[192:195], v[114:117]
	v_mfma_f32_16x16x32_bf16 v[102:105], v[176:179], v[200:203], v[102:105]
	v_mfma_f32_16x16x32_bf16 v[98:101], v[184:187], v[200:203], v[98:101]
	v_mfma_f32_16x16x32_bf16 v[82:85], v[176:179], v[216:219], v[82:85]
	v_mfma_f32_16x16x32_bf16 v[74:77], v[184:187], v[216:219], v[74:77]
	v_mfma_f32_16x16x32_bf16 v[70:73], v[176:179], v[224:227], v[70:73]
	v_mfma_f32_16x16x32_bf16 v[66:69], v[184:187], v[224:227], v[66:69]
	s_setprio 0
	s_barrier
; #define PG8_STAGE(bufoff, gbase, voff) do { _Pragma("unroll") for (int _i = 0; _i < 2; ++_i) \
;         __builtin_amdgcn_global_load_lds((const unsigned*)((const char*)(gbase) + (voff)[_i]), (LAS unsigned*)(lds + (bufoff) + ldsw + _i * 8192), 16, 0, 0); } while (0)
; #define PG8_STAGE_A(bufoff, kptr, half, VO) do { if constexpr (GATHER) { _Pragma("unroll") for (int _i = 0; _i < 2; ++_i) \
;         __builtin_amdgcn_global_load_lds((const unsigned*)((const char*)(kptr) + (VO)[half][_i]), (LAS unsigned*)(lds + (bufoff) + ldsw + _i * 8192), 16, 0, 0); } \
;         else { PG8_STAGE(bufoff, (kptr) + (half) * hstepA, voffA); } } while (0)
; #define PG8_LDA(dst, b, h) do { _Pragma("unroll") for (int m = 0; m < 4; ++m) _Pragma("unroll") for (int k = 0; k < 2; ++k) dst[m][k] = *(const LAS bf16x8*)(lds + PG8_SA(b, h) + aoff + m * 2048 + k * 1024); } while (0)
; #define PG8_LDB(dst, b, h) do { _Pragma("unroll") for (int n = 0; n < 2; ++n) _Pragma("unroll") for (int k = 0; k < 2; ++k) dst[n][k] = *(const LAS bf16x8*)(lds + PG8_SB(b, h) + boff + n * 2048 + k * 1024); } while (0)
; #define PG8_MMA(ai, bj, At, Bt) do { __builtin_amdgcn_s_setprio(1); _Pragma("unroll") for (int m = 0; m < 4; ++m) _Pragma("unroll") for (int n = 0; n < 2; ++n) _Pragma("unroll") for (int k = 0; k < 2; ++k) \
;         acc[ai][bj][m][n] = __builtin_amdgcn_mfma_f32_16x16x32_bf16(Bt[n][k], At[m][k], acc[ai][bj][m][n], 0, 0, 0); __builtin_amdgcn_s_setprio(0); } while (0)
; #define PG8_WAIT_V(n) asm volatile("s_waitcnt vmcnt(" #n ")" ::: "memory")
; #define PG8_WAIT_L(n) asm volatile("s_waitcnt lgkmcnt(" #n ")" ::: "memory")
; #define PG8_BAR __builtin_amdgcn_s_barrier()
; #define PG8_SCHED __builtin_amdgcn_sched_barrier(0)
;     ...
;         for (int t = 0; t < nt; t += 2) {
;     ...
;             PG8_LDB(B0, 1, 0); PG8_LDB(B1, 1, 1); PG8_SCHED; PG8_LDA(At, 1, 0); PG8_STAGE_A(PG8_SA(0, 1), a2, 1, g2);
;             PG8_WAIT_V(8); PG8_WAIT_L(0); PG8_BAR; PG8_MMA(0, 0, At, B0); PG8_MMA(0, 1, At, B1); PG8_BAR; PG8_SCHED;
;             PG8_LDA(At, 1, 1); PG8_STAGE(PG8_SB(1, 0), b3, voffB); PG8_STAGE(PG8_SB(1, 1), b3 + hstepB, voffB); PG8_STAGE_A(PG8_SA(1, 0), a3, 0, g2);
;             PG8_WAIT_V(8); PG8_WAIT_L(0); PG8_BAR; PG8_MMA(1, 0, At, B0); PG8_MMA(1, 1, At, B1); PG8_BAR; PG8_SCHED;
	s_add_i32 s19, s19, s62
	v_lshl_add_u64 v[142:143], v[142:143], 0, s[8:9]
	s_mov_b32 m0, s19
	ds_read_b128 v[188:191], v155 offset:49152
	ds_read_b128 v[192:195], v155 offset:50176
	ds_read_b128 v[196:199], v155 offset:51200
	ds_read_b128 v[200:203], v155 offset:52224
	ds_read_b128 v[208:211], v155 offset:53248
	ds_read_b128 v[216:219], v155 offset:54272
	ds_read_b128 v[220:223], v155 offset:55296
	ds_read_b128 v[224:227], v155 offset:56320
	global_load_lds_dwordx4 v[142:143], off
	s_add_i32 m0, s19, 0x2000
	s_add_u32 s0, s0, 0x40080
	v_lshl_add_u64 v[142:143], v[204:205], 0, s[8:9]
	s_addc_u32 s1, s1, 0
	s_add_i32 s19, s22, s62
	global_load_lds_dwordx4 v[142:143], off
	v_lshl_add_u64 v[142:143], s[0:1], 0, v[206:207]
	s_mov_b32 m0, s19
	s_nop 0
	global_load_lds_dwordx4 v[142:143], off
	v_lshl_add_u64 v[142:143], s[0:1], 0, v[134:135]
	s_add_i32 m0, s19, 0x2000
	s_nop 0
	global_load_lds_dwordx4 v[142:143], off
	v_lshl_add_u64 v[142:143], v[212:213], 0, s[8:9]
	s_mov_b32 m0, s70
	s_nop 0
	global_load_lds_dwordx4 v[142:143], off
	v_lshl_add_u64 v[142:143], v[214:215], 0, s[8:9]
	s_mov_b32 m0, s71
	s_nop 0
	global_load_lds_dwordx4 v[142:143], off
	s_waitcnt vmcnt(8)
	s_waitcnt lgkmcnt(0)
	s_barrier
	s_setprio 1
	s_waitcnt lgkmcnt(0)
	v_mfma_f32_16x16x32_bf16 v[62:65], v[156:159], v[188:191], v[62:65]
	v_mfma_f32_16x16x32_bf16 v[58:61], v[164:167], v[188:191], v[58:61]
	v_mfma_f32_16x16x32_bf16 v[54:57], v[156:159], v[196:199], v[54:57]
	v_mfma_f32_16x16x32_bf16 v[46:49], v[164:167], v[196:199], v[46:49]
	v_mfma_f32_16x16x32_bf16 v[38:41], v[156:159], v[208:211], v[38:41]
	v_mfma_f32_16x16x32_bf16 v[30:33], v[164:167], v[208:211], v[30:33]
	v_mfma_f32_16x16x32_bf16 v[22:25], v[156:159], v[220:223], v[22:25]
	v_mfma_f32_16x16x32_bf16 v[14:17], v[164:167], v[220:223], v[14:17]
	v_mfma_f32_16x16x32_bf16 v[62:65], v[160:163], v[192:195], v[62:65]
	v_mfma_f32_16x16x32_bf16 v[58:61], v[168:171], v[192:195], v[58:61]
	v_mfma_f32_16x16x32_bf16 v[54:57], v[160:163], v[200:203], v[54:57]
	v_mfma_f32_16x16x32_bf16 v[46:49], v[168:171], v[200:203], v[46:49]
	v_mfma_f32_16x16x32_bf16 v[38:41], v[160:163], v[216:219], v[38:41]
	v_mfma_f32_16x16x32_bf16 v[30:33], v[168:171], v[216:219], v[30:33]
	v_mfma_f32_16x16x32_bf16 v[22:25], v[160:163], v[224:227], v[22:25]
	v_mfma_f32_16x16x32_bf16 v[14:17], v[168:171], v[224:227], v[14:17]
	v_mfma_f32_16x16x32_bf16 v[50:53], v[172:175], v[188:191], v[50:53]
	v_mfma_f32_16x16x32_bf16 v[42:45], v[180:183], v[188:191], v[42:45]
	v_mfma_f32_16x16x32_bf16 v[34:37], v[172:175], v[196:199], v[34:37]
	v_mfma_f32_16x16x32_bf16 v[26:29], v[180:183], v[196:199], v[26:29]
	v_mfma_f32_16x16x32_bf16 v[18:21], v[172:175], v[208:211], v[18:21]
	v_mfma_f32_16x16x32_bf16 v[10:13], v[180:183], v[208:211], v[10:13]
	v_mfma_f32_16x16x32_bf16 v[6:9], v[172:175], v[220:223], v[6:9]
	v_mfma_f32_16x16x32_bf16 v[2:5], v[180:183], v[220:223], v[2:5]
	v_mfma_f32_16x16x32_bf16 v[50:53], v[176:179], v[192:195], v[50:53]
	v_mfma_f32_16x16x32_bf16 v[42:45], v[184:187], v[192:195], v[42:45]
	v_mfma_f32_16x16x32_bf16 v[34:37], v[176:179], v[200:203], v[34:37]
	v_mfma_f32_16x16x32_bf16 v[26:29], v[184:187], v[200:203], v[26:29]
	v_mfma_f32_16x16x32_bf16 v[18:21], v[176:179], v[216:219], v[18:21]
	v_mfma_f32_16x16x32_bf16 v[10:13], v[184:187], v[216:219], v[10:13]
	v_mfma_f32_16x16x32_bf16 v[6:9], v[176:179], v[224:227], v[6:9]
	v_mfma_f32_16x16x32_bf16 v[2:5], v[184:187], v[224:227], v[2:5]
	s_setprio 0
	s_barrier
	s_add_i32 s18, s18, 2
	s_add_u32 s24, s24, 0x100
	s_addc_u32 s25, s25, 0
	s_add_u32 s16, s16, 0x100
	s_addc_u32 s17, s17, 0
	s_cmp_gt_u32 s18, 13
	s_cbranch_scc0 .LBB0_2458
	s_and_b64 vcc, exec, s[42:43]
	s_cbranch_vccz .LBB0_2461
	s_barrier
